# removed 242 dead zero-initialisations of dwords that two v_cvt_pk_fp8_f32 (low then high half) overwrite completely (converter loops and fp8 epilogues)
# baseline (speedup 1.0000x reference)
; #define LAS __attribute__((address_space(3)))
; #define LDS_WAIT() asm volatile("s_waitcnt lgkmcnt(0)" ::: "memory")
; __device__ __forceinline__ unsigned pk4_fp8(float a, float b, float c, float d) { int w = __builtin_amdgcn_cvt_pk_fp8_f32(a, b, 0, false); w = __builtin_amdgcn_cvt_pk_fp8_f32(c, d, w, true); return (unsigned)w; }
; __device__ __forceinline__ void tr_store_f8(unsigned char* WT, int K, int k0, int n0, LAS float* scr, int lane) {
;     const int c = lane & 3;
; #pragma unroll
;     for (int j = 0; j < 2; ++j) { const int nl = (lane >> 2) + 16 * j; const LAS float* s = scr + (16 * c) * 33 + nl; u32x4 o;
; #pragma unroll
;         for (int q = 0; q < 4; ++q) o[q] = pk4_fp8(s[(4 * q) * 33] * WSCALE, s[(4 * q + 1) * 33] * WSCALE, s[(4 * q + 2) * 33] * WSCALE, s[(4 * q + 3) * 33] * WSCALE);
;         *(u32x4*)(WT + (size_t)(n0 + nl) * K + k0 + 16 * c) = o; }
; }
; __device__ __forceinline__ void p0_prologue(Frame& F) {
;     ...
;     { float va[32]; int it = gw;
;       if (it < NITEMS) TR_LOAD(it);
;       while (it < NITEMS) {
; #pragma unroll
;           for (int i = 0; i < 32; ++i) scr[(2 * i + (F.lane >> 5)) * 33 + (F.lane & 31)] = va[i];
;           const int itn = it + NGW;
;           if (itn < NITEMS) TR_LOAD(itn);
;           LDS_WAIT(); asm volatile("" ::: "memory");
;           TR_STORE(it);
;           LDS_WAIT(); asm volatile("" ::: "memory");
;           it = itn;
;       } }
.LBB0_68:
	s_andn2_b64 vcc, exec, s[64:65]
	s_cbranch_vccnz .LBB0_70
	ds_read2_b32 v[34:35], v81 offset1:16
	ds_read2_b32 v[36:37], v81 offset0:33 offset1:49
	ds_read2_b32 v[62:63], v81 offset0:66 offset1:82
	ds_read2_b32 v[64:65], v81 offset0:99 offset1:115
	s_waitcnt lgkmcnt(3)
	v_mul_f32_e32 v34, 0x42800000, v34
	s_waitcnt lgkmcnt(2)
	v_mul_f32_e32 v36, 0x42800000, v36
	v_cvt_pk_fp8_f32 v38, v34, v36
	ds_read2_b32 v[66:67], v81 offset0:132 offset1:148
	ds_read2_b32 v[68:69], v81 offset0:165 offset1:181
	ds_read2_b32 v[70:71], v81 offset0:198 offset1:214
	s_waitcnt lgkmcnt(4)
	v_mul_f32_e32 v39, 0x42800000, v62
	s_waitcnt lgkmcnt(3)
	v_mul_f32_e32 v34, 0x42800000, v64
	v_cvt_pk_fp8_f32 v38, v39, v34 op_sel:[0,0,1]
	s_waitcnt lgkmcnt(2)
	v_mul_f32_e32 v34, 0x42800000, v66
	s_waitcnt lgkmcnt(1)
	v_mul_f32_e32 v36, 0x42800000, v68
	ds_read2_b32 v[72:73], v81 offset0:231 offset1:247
	v_cvt_pk_fp8_f32 v39, v34, v36
	v_add_u32_e32 v34, 0x400, v81
	ds_read2_b32 v[86:87], v34 offset0:8 offset1:24
	ds_read2_b32 v[88:89], v34 offset0:41 offset1:57
	ds_read2_b32 v[90:91], v34 offset0:74 offset1:90
	ds_read2_b32 v[92:93], v34 offset0:107 offset1:123
	ds_read2_b32 v[94:95], v34 offset0:140 offset1:156
	ds_read2_b32 v[96:97], v34 offset0:173 offset1:189
	s_waitcnt lgkmcnt(7)
	v_mul_f32_e32 v40, 0x42800000, v70
	s_waitcnt lgkmcnt(6)
	v_mul_f32_e32 v36, 0x42800000, v72
	v_cvt_pk_fp8_f32 v39, v40, v36 op_sel:[0,0,1]
	s_waitcnt lgkmcnt(5)
	v_mul_f32_e32 v36, 0x42800000, v86
	s_waitcnt lgkmcnt(4)
	v_mul_f32_e32 v41, 0x42800000, v88
	ds_read2_b32 v[98:99], v34 offset0:206 offset1:222
	ds_read2_b32 v[100:101], v34 offset0:239 offset1:255
	v_cvt_pk_fp8_f32 v40, v36, v41
	s_waitcnt lgkmcnt(3)
	v_mul_f32_e32 v36, 0x42800000, v94
	s_waitcnt lgkmcnt(2)
	v_mul_f32_e32 v64, 0x42800000, v96
	v_cvt_pk_fp8_f32 v41, v36, v64
	s_add_i32 s64, s3, 0xfffdbc00
	s_and_b32 s64, s64, 0x7e0
	s_waitcnt lgkmcnt(1)
	v_mul_f32_e32 v34, 0x42800000, v98
	s_waitcnt lgkmcnt(0)
	v_mul_f32_e32 v36, 0x42800000, v100
	v_mul_f32_e32 v42, 0x42800000, v90
	v_mul_f32_e32 v62, 0x42800000, v92
	v_cvt_pk_fp8_f32 v41, v34, v36 op_sel:[0,0,1]
	v_or_b32_e32 v34, s64, v80
	v_cvt_pk_fp8_f32 v40, v42, v62 op_sel:[0,0,1]
	v_lshlrev_b32_e32 v42, 11, v34
	v_mul_f32_e32 v35, 0x42800000, v35
	v_mul_f32_e32 v36, 0x42800000, v37
	s_add_i32 s40, s70, 0xffffede0
	v_cvt_pk_fp8_f32 v34, v35, v36
	v_mul_f32_e32 v36, 0x42800000, v67
	v_mul_f32_e32 v62, 0x42800000, v69
	s_andn2_b32 s40, s40, 63
	v_cvt_pk_fp8_f32 v35, v36, v62
	v_lshl_add_u64 v[60:61], v[50:51], 0, s[40:41]
	v_lshl_add_u64 v[102:103], v[60:61], 0, v[42:43]
	v_mul_f32_e32 v37, 0x42800000, v63
	v_mul_f32_e32 v42, 0x42800000, v65
	v_cvt_pk_fp8_f32 v34, v37, v42 op_sel:[0,0,1]
	v_mul_f32_e32 v36, 0x42800000, v71
	v_mul_f32_e32 v37, 0x42800000, v73
	v_cvt_pk_fp8_f32 v35, v36, v37 op_sel:[0,0,1]
	v_mul_f32_e32 v37, 0x42800000, v87
	v_mul_f32_e32 v42, 0x42800000, v89
	v_cvt_pk_fp8_f32 v36, v37, v42
	v_mul_f32_e32 v42, 0x42800000, v95
	v_mul_f32_e32 v64, 0x42800000, v97
	v_cvt_pk_fp8_f32 v37, v42, v64
	v_mul_f32_e32 v62, 0x42800000, v91
	v_mul_f32_e32 v63, 0x42800000, v93
	v_cvt_pk_fp8_f32 v36, v62, v63 op_sel:[0,0,1]
	v_mul_f32_e32 v42, 0x42800000, v99
	v_mul_f32_e32 v62, 0x42800000, v101
	v_cvt_pk_fp8_f32 v37, v42, v62 op_sel:[0,0,1]
	v_or_b32_e32 v64, s64, v82
	s_mov_b64 s[66:67], 11
	global_store_dwordx4 v[102:103], v[38:41], off

; #define LAS __attribute__((address_space(3)))
; __device__ __forceinline__ unsigned pk4_fp8(float a, float b, float c, float d) { int w = __builtin_amdgcn_cvt_pk_fp8_f32(a, b, 0, false); w = __builtin_amdgcn_cvt_pk_fp8_f32(c, d, w, true); return (unsigned)w; }
;     __device__ __forceinline__ CvtDesc desc(int qq) const { return cvt_desc(*F, item_of(qq), qq & 1, h); }
;     __device__ __forceinline__ void flush() { if (fitem >= 0) { cvt_flush(cvt_desc(*F, fitem, 0, h), img, h, F->lane); fitem = -1; } }
; __device__ __forceinline__ void cvt_to_lds(const CvtBuf& b, const CvtDesc& d, LAS unsigned char* img, const LAS float* gl, int sub2, int h, int lane) {
;     const int hh = lane >> 5, l5 = lane & 31;
;     float gs[16];
;     const bool use_g = d.map == 2;
; #pragma unroll
;     for (int q = 0; q < 4; ++q) { const f32x4 gv = *(const LAS f32x4*)(gl + d.k0 + 16 * hh + 4 * q);
; #pragma unroll
;         for (int j = 0; j < 4; ++j) gs[4 * q + j] = use_g ? gv[j] : WSCALE; }
;     const int c8 = 4 * h + 2 * sub2 + hh;
; #pragma unroll
;     for (int j = 0; j < 4; ++j) { u32x4 o;
; #pragma unroll
;         for (int q = 0; q < 4; ++q) { const int i = 4 * q; o[q] = pk4_fp8(b.v[i][j] * gs[i], b.v[i + 1][j] * gs[i + 1], b.v[i + 2][j] * gs[i + 2], b.v[i + 3][j] * gs[i + 3]); }
;         *(LAS u32x4*)(img + (4 * l5 + j) * 128 + 16 * (c8 ^ (l5 & 7))) = o; }
; }
;     __device__ __forceinline__ void drain() {
;     ...
;         while (q < nq) {
;             if (q + 1 < nq) cvt_load(b2, desc(q + 1), F->lane);
;             cvt_to_lds(buf, desc(q), img, gl, q & 1, h, F->lane); if (q & 1) fitem = item_of(q); ++q;
;             if (fitem >= 0) { __syncthreads(); flush(); __syncthreads(); }
;             if (q >= nq) break;
;             if (q + 1 < nq) cvt_load(buf, desc(q + 1), F->lane);
;             cvt_to_lds(b2, desc(q), img, gl, q & 1, h, F->lane); if (q & 1) fitem = item_of(q); ++q;
;             if (fitem >= 0) { __syncthreads(); flush(); __syncthreads(); }
.LBB0_300:
	s_cmpk_lt_i32 s44, 0x4000
	s_cselect_b64 s[0:1], -1, 0
	s_and_b64 s[10:11], s[0:1], exec
	s_cselect_b32 s4, 5, 4
	s_lshr_b32 s4, s44, s4
	s_lshl_b32 s4, s4, 9
	s_and_b32 s4, s4, 0x1e00
	v_add_u32_e32 v136, s4, v139
	ds_read_b128 v[152:155], v136 offset:49152
	ds_read_b128 v[156:159], v136 offset:49168
	ds_read_b128 v[160:163], v136 offset:49184
	ds_read_b128 v[164:167], v136 offset:49200
	s_andn2_b64 vcc, exec, s[6:7]
	s_waitcnt lgkmcnt(3)
	v_cndmask_b32_e64 v132, v151, v152, s[0:1]
	v_cndmask_b32_e64 v137, v151, v153, s[0:1]
	v_cndmask_b32_e64 v168, v151, v154, s[0:1]
	s_waitcnt lgkmcnt(2)
	v_cndmask_b32_e64 v170, v151, v156, s[0:1]
	v_cndmask_b32_e64 v171, v151, v157, s[0:1]
	s_waitcnt vmcnt(31)
	v_mul_f32_e32 v153, v2, v132
	s_waitcnt vmcnt(30)
	v_mul_f32_e32 v154, v6, v137
	v_cvt_pk_fp8_f32 v152, v153, v154
	s_waitcnt vmcnt(27)
	v_mul_f32_e32 v154, v18, v170
	s_waitcnt vmcnt(26)
	v_mul_f32_e32 v157, v22, v171
	v_cvt_pk_fp8_f32 v153, v154, v157
	v_cndmask_b32_e64 v169, v151, v155, s[0:1]
	v_cndmask_b32_e64 v172, v151, v158, s[0:1]
	v_cndmask_b32_e64 v173, v151, v159, s[0:1]
	v_mul_f32_e32 v155, v10, v168
	v_mul_f32_e32 v156, v14, v169
	s_waitcnt lgkmcnt(1)
	v_cndmask_b32_e64 v174, v151, v160, s[0:1]
	v_cndmask_b32_e64 v175, v151, v161, s[0:1]
	v_cvt_pk_fp8_f32 v152, v155, v156 op_sel:[0,0,1]
	s_waitcnt vmcnt(25)
	v_mul_f32_e32 v154, v26, v172
	s_waitcnt vmcnt(24)
	v_mul_f32_e32 v155, v30, v173
	s_waitcnt lgkmcnt(0)
	v_cndmask_b32_e64 v178, v151, v164, s[0:1]
	v_cndmask_b32_e64 v179, v151, v165, s[0:1]
	v_cvt_pk_fp8_f32 v153, v154, v155 op_sel:[0,0,1]
	s_waitcnt vmcnt(23)
	v_mul_f32_e32 v155, v34, v174
	s_waitcnt vmcnt(22)
	v_mul_f32_e32 v156, v38, v175
	v_cvt_pk_fp8_f32 v154, v155, v156
	s_waitcnt vmcnt(19)
	v_mul_f32_e32 v156, v50, v178
	s_waitcnt vmcnt(18)
	v_mul_f32_e32 v159, v54, v179
	v_cvt_pk_fp8_f32 v155, v156, v159
	v_cndmask_b32_e64 v176, v151, v162, s[0:1]
	v_cndmask_b32_e64 v177, v151, v163, s[0:1]
	v_cndmask_b32_e64 v180, v151, v166, s[0:1]
	v_cndmask_b32_e64 v181, v151, v167, s[0:1]
	v_mul_f32_e32 v157, v42, v176
	v_mul_f32_e32 v158, v46, v177
	v_cvt_pk_fp8_f32 v154, v157, v158 op_sel:[0,0,1]
	s_waitcnt vmcnt(17)
	v_mul_f32_e32 v156, v58, v180
	s_waitcnt vmcnt(16)
	v_mul_f32_e32 v157, v62, v181
	v_cvt_pk_fp8_f32 v155, v156, v157 op_sel:[0,0,1]
	v_mul_f32_e32 v157, v3, v132
	v_mul_f32_e32 v158, v7, v137
	v_cvt_pk_fp8_f32 v156, v157, v158
	v_mul_f32_e32 v158, v19, v170
	v_mul_f32_e32 v161, v23, v171
	v_cvt_pk_fp8_f32 v157, v158, v161
	v_mul_f32_e32 v159, v11, v168
	v_mul_f32_e32 v160, v15, v169
	v_cvt_pk_fp8_f32 v156, v159, v160 op_sel:[0,0,1]
	v_mul_f32_e32 v158, v27, v172
	v_mul_f32_e32 v159, v31, v173
	v_cvt_pk_fp8_f32 v157, v158, v159 op_sel:[0,0,1]
	v_mul_f32_e32 v159, v35, v174
	v_mul_f32_e32 v160, v39, v175
	v_cvt_pk_fp8_f32 v158, v159, v160
	v_mul_f32_e32 v160, v51, v178
	v_mul_f32_e32 v163, v55, v179
	v_cvt_pk_fp8_f32 v159, v160, v163
	v_mul_f32_e32 v161, v43, v176
	v_mul_f32_e32 v162, v47, v177
	v_cvt_pk_fp8_f32 v158, v161, v162 op_sel:[0,0,1]
	v_mul_f32_e32 v160, v59, v180
	v_mul_f32_e32 v161, v63, v181
	v_cvt_pk_fp8_f32 v159, v160, v161 op_sel:[0,0,1]
	v_mul_f32_e32 v161, v4, v132
	v_mul_f32_e32 v162, v8, v137
	v_cvt_pk_fp8_f32 v160, v161, v162
	v_mul_f32_e32 v162, v20, v170
	v_mul_f32_e32 v165, v24, v171
	v_cvt_pk_fp8_f32 v161, v162, v165
	v_mul_f32_e32 v163, v12, v168
	v_mul_f32_e32 v164, v16, v169
	v_cvt_pk_fp8_f32 v160, v163, v164 op_sel:[0,0,1]
	v_mul_f32_e32 v162, v28, v172
	v_mul_f32_e32 v163, v32, v173
	v_cvt_pk_fp8_f32 v161, v162, v163 op_sel:[0,0,1]
	v_mul_f32_e32 v163, v36, v174
	v_mul_f32_e32 v164, v40, v175
	v_cvt_pk_fp8_f32 v162, v163, v164
	v_mul_f32_e32 v164, v52, v178
	v_mul_f32_e32 v167, v56, v179
	v_cvt_pk_fp8_f32 v163, v164, v167
	v_mul_f32_e32 v165, v44, v176
	v_mul_f32_e32 v166, v48, v177
	v_cvt_pk_fp8_f32 v162, v165, v166 op_sel:[0,0,1]
	v_mul_f32_e32 v164, v60, v180
	v_mul_f32_e32 v165, v64, v181
	v_cvt_pk_fp8_f32 v163, v164, v165 op_sel:[0,0,1]
	v_mul_f32_e32 v132, v5, v132
	v_mul_f32_e32 v137, v9, v137
	v_cvt_pk_fp8_f32 v164, v132, v137
	v_mul_f32_e32 v132, v21, v170
	v_mul_f32_e32 v137, v25, v171
	v_cvt_pk_fp8_f32 v165, v132, v137
	v_mul_f32_e32 v166, v13, v168
	v_mul_f32_e32 v167, v17, v169
	v_mul_f32_e32 v132, v29, v172
	v_mul_f32_e32 v137, v33, v173
	v_cvt_pk_fp8_f32 v164, v166, v167 op_sel:[0,0,1]
	v_cvt_pk_fp8_f32 v165, v132, v137 op_sel:[0,0,1]
	v_mul_f32_e32 v132, v37, v174
	v_mul_f32_e32 v137, v41, v175
	v_cvt_pk_fp8_f32 v166, v132, v137
	v_mul_f32_e32 v132, v53, v178
	v_mul_f32_e32 v137, v57, v179
	v_cvt_pk_fp8_f32 v167, v132, v137
	v_mul_f32_e32 v168, v45, v176
	v_mul_f32_e32 v169, v49, v177
	v_mul_f32_e32 v132, v61, v180
	v_mul_f32_e32 v137, v65, v181
	v_cvt_pk_fp8_f32 v166, v168, v169 op_sel:[0,0,1]
	v_cvt_pk_fp8_f32 v167, v132, v137 op_sel:[0,0,1]
	s_mov_b64 s[6:7], -1
	ds_write_b128 v149, v[152:155]
	ds_write_b128 v149, v[156:159] offset:128
	ds_write_b128 v149, v[160:163] offset:256
	ds_write_b128 v149, v[164:167] offset:384
	s_cbranch_vccnz .LBB0_293
	s_add_i32 s43, s43, 2
	s_cmp_ge_i32 s43, s34
	s_cselect_b64 s[6:7], -1, 0
	s_and_b64 vcc, exec, s[6:7]
	s_cbranch_vccz .Ldr1_goB
	s_waitcnt vmcnt(0)
	s_branch .LBB0_307

; #define LAS __attribute__((address_space(3)))
; __device__ __forceinline__ unsigned pk4_fp8(float a, float b, float c, float d) { int w = __builtin_amdgcn_cvt_pk_fp8_f32(a, b, 0, false); w = __builtin_amdgcn_cvt_pk_fp8_f32(c, d, w, true); return (unsigned)w; }
;     __device__ __forceinline__ CvtDesc desc(int qq) const { return cvt_desc(*F, item_of(qq), qq & 1, h); }
;     __device__ __forceinline__ void flush() { if (fitem >= 0) { cvt_flush(cvt_desc(*F, fitem, 0, h), img, h, F->lane); fitem = -1; } }
; __device__ __forceinline__ void cvt_to_lds(const CvtBuf& b, const CvtDesc& d, LAS unsigned char* img, const LAS float* gl, int sub2, int h, int lane) {
;     const int hh = lane >> 5, l5 = lane & 31;
;     float gs[16];
;     const bool use_g = d.map == 2;
; #pragma unroll
;     for (int q = 0; q < 4; ++q) { const f32x4 gv = *(const LAS f32x4*)(gl + d.k0 + 16 * hh + 4 * q);
; #pragma unroll
;         for (int j = 0; j < 4; ++j) gs[4 * q + j] = use_g ? gv[j] : WSCALE; }
;     const int c8 = 4 * h + 2 * sub2 + hh;
; #pragma unroll
;     for (int j = 0; j < 4; ++j) { u32x4 o;
; #pragma unroll
;         for (int q = 0; q < 4; ++q) { const int i = 4 * q; o[q] = pk4_fp8(b.v[i][j] * gs[i], b.v[i + 1][j] * gs[i + 1], b.v[i + 2][j] * gs[i + 2], b.v[i + 3][j] * gs[i + 3]); }
;         *(LAS u32x4*)(img + (4 * l5 + j) * 128 + 16 * (c8 ^ (l5 & 7))) = o; }
; }
;     __device__ __forceinline__ void drain() {
;     ...
;             cvt_to_lds(buf, desc(q), img, gl, q & 1, h, F->lane); if (q & 1) fitem = item_of(q); ++q;
;             if (fitem >= 0) { __syncthreads(); flush(); __syncthreads(); }
;             if (q >= nq) break;
;             if (q + 1 < nq) cvt_load(buf, desc(q + 1), F->lane);
;             cvt_to_lds(b2, desc(q), img, gl, q & 1, h, F->lane); if (q & 1) fitem = item_of(q); ++q;
;             if (fitem >= 0) { __syncthreads(); flush(); __syncthreads(); }
.LBB0_307:
	ds_read_b128 v[152:155], v136 offset:49280
	ds_read_b128 v[156:159], v136 offset:49296
	ds_read_b128 v[160:163], v136 offset:49312
	ds_read_b128 v[164:167], v136 offset:49328
	s_cmp_lt_i32 s44, 0
	s_waitcnt lgkmcnt(3)
	v_cndmask_b32_e64 v132, v151, v152, s[0:1]
	v_cndmask_b32_e64 v136, v151, v153, s[0:1]
	v_cndmask_b32_e64 v137, v151, v154, s[0:1]
	s_waitcnt lgkmcnt(2)
	v_cndmask_b32_e64 v169, v151, v156, s[0:1]
	v_cndmask_b32_e64 v170, v151, v157, s[0:1]
	v_mul_f32_e32 v153, v70, v132
	v_mul_f32_e32 v154, v66, v136
	v_cvt_pk_fp8_f32 v152, v153, v154
	v_mul_f32_e32 v154, v86, v169
	v_mul_f32_e32 v157, v82, v170
	v_cvt_pk_fp8_f32 v153, v154, v157
	v_cndmask_b32_e64 v168, v151, v155, s[0:1]
	v_cndmask_b32_e64 v171, v151, v158, s[0:1]
	v_cndmask_b32_e64 v172, v151, v159, s[0:1]
	v_mul_f32_e32 v155, v78, v137
	v_mul_f32_e32 v156, v74, v168
	s_waitcnt lgkmcnt(1)
	v_cndmask_b32_e64 v173, v151, v160, s[0:1]
	v_cndmask_b32_e64 v174, v151, v161, s[0:1]
	v_cvt_pk_fp8_f32 v152, v155, v156 op_sel:[0,0,1]
	v_mul_f32_e32 v154, v94, v171
	v_mul_f32_e32 v155, v90, v172
	s_waitcnt lgkmcnt(0)
	v_cndmask_b32_e64 v164, v151, v164, s[0:1]
	v_cndmask_b32_e64 v165, v151, v165, s[0:1]
	v_cvt_pk_fp8_f32 v153, v154, v155 op_sel:[0,0,1]
	v_mul_f32_e32 v155, v98, v173
	v_mul_f32_e32 v156, v102, v174
	v_cvt_pk_fp8_f32 v154, v155, v156
	v_mul_f32_e32 v156, v114, v164
	v_mul_f32_e32 v159, v118, v165
	v_cvt_pk_fp8_f32 v155, v156, v159
	v_cndmask_b32_e64 v162, v151, v162, s[0:1]
	v_cndmask_b32_e64 v163, v151, v163, s[0:1]
	v_cndmask_b32_e64 v166, v151, v166, s[0:1]
	v_cndmask_b32_e64 v167, v151, v167, s[0:1]
	v_mul_f32_e32 v157, v106, v162
	v_mul_f32_e32 v158, v110, v163
	v_cvt_pk_fp8_f32 v154, v157, v158 op_sel:[0,0,1]
	v_mul_f32_e32 v156, v122, v166
	v_mul_f32_e32 v157, v126, v167
	v_cvt_pk_fp8_f32 v155, v156, v157 op_sel:[0,0,1]
	v_mul_f32_e32 v157, v83, v170
	v_mul_f32_e32 v156, v75, v168
	v_mul_f32_e32 v159, v119, v165
	ds_write_b128 v150, v[152:155]
	v_mul_f32_e32 v153, v71, v132
	v_mul_f32_e32 v154, v67, v136
	v_cvt_pk_fp8_f32 v152, v153, v154
	v_mul_f32_e32 v154, v87, v169
	v_cvt_pk_fp8_f32 v153, v154, v157
	v_mul_f32_e32 v155, v79, v137
	v_cvt_pk_fp8_f32 v152, v155, v156 op_sel:[0,0,1]
	v_mul_f32_e32 v154, v95, v171
	v_mul_f32_e32 v155, v91, v172
	v_cvt_pk_fp8_f32 v153, v154, v155 op_sel:[0,0,1]
	v_mul_f32_e32 v155, v99, v173
	v_mul_f32_e32 v156, v103, v174
	v_cvt_pk_fp8_f32 v154, v155, v156
	v_mul_f32_e32 v156, v115, v164
	v_cvt_pk_fp8_f32 v155, v156, v159
	v_mul_f32_e32 v157, v107, v162
	v_mul_f32_e32 v158, v111, v163
	v_cvt_pk_fp8_f32 v154, v157, v158 op_sel:[0,0,1]
	v_mul_f32_e32 v156, v123, v166
	v_mul_f32_e32 v157, v127, v167
	v_cvt_pk_fp8_f32 v155, v156, v157 op_sel:[0,0,1]
	v_mul_f32_e32 v157, v72, v132
	v_mul_f32_e32 v158, v68, v136
	v_cvt_pk_fp8_f32 v156, v157, v158
	v_mul_f32_e32 v158, v88, v169
	v_mul_f32_e32 v161, v84, v170
	v_cvt_pk_fp8_f32 v157, v158, v161
	v_mul_f32_e32 v159, v80, v137
	v_mul_f32_e32 v160, v76, v168
	v_cvt_pk_fp8_f32 v156, v159, v160 op_sel:[0,0,1]
	v_mul_f32_e32 v158, v96, v171
	v_mul_f32_e32 v159, v92, v172
	v_cvt_pk_fp8_f32 v157, v158, v159 op_sel:[0,0,1]
	v_mul_f32_e32 v159, v100, v173
	v_mul_f32_e32 v160, v104, v174
	v_cvt_pk_fp8_f32 v158, v159, v160
	v_mul_f32_e32 v160, v116, v164
	v_mul_f32_e32 v176, v120, v165
	v_cvt_pk_fp8_f32 v159, v160, v176
	v_mul_f32_e32 v161, v108, v162
	v_mul_f32_e32 v175, v112, v163
	v_cvt_pk_fp8_f32 v158, v161, v175 op_sel:[0,0,1]
	v_mul_f32_e32 v160, v124, v166
	v_mul_f32_e32 v161, v128, v167
	v_cvt_pk_fp8_f32 v159, v160, v161 op_sel:[0,0,1]
	v_mul_f32_e32 v132, v73, v132
	v_mul_f32_e32 v136, v69, v136
	v_cvt_pk_fp8_f32 v160, v132, v136
	v_mul_f32_e32 v132, v89, v169
	v_mul_f32_e32 v136, v85, v170
	v_cvt_pk_fp8_f32 v161, v132, v136
	v_mul_f32_e32 v137, v81, v137
	v_mul_f32_e32 v168, v77, v168
	v_mul_f32_e32 v132, v97, v171
	v_mul_f32_e32 v136, v93, v172
	v_cvt_pk_fp8_f32 v160, v137, v168 op_sel:[0,0,1]
	v_cvt_pk_fp8_f32 v161, v132, v136 op_sel:[0,0,1]
	v_mul_f32_e32 v132, v101, v173
	v_mul_f32_e32 v136, v105, v174
	v_mul_f32_e32 v137, v109, v162
	v_mul_f32_e32 v168, v113, v163
	v_cvt_pk_fp8_f32 v162, v132, v136
	v_mul_f32_e32 v132, v117, v164
	v_mul_f32_e32 v136, v121, v165
	v_cvt_pk_fp8_f32 v163, v132, v136
	v_mul_f32_e32 v132, v125, v166
	v_mul_f32_e32 v136, v129, v167
	v_cvt_pk_fp8_f32 v162, v137, v168 op_sel:[0,0,1]
	v_cvt_pk_fp8_f32 v163, v132, v136 op_sel:[0,0,1]
	ds_write_b128 v150, v[152:155] offset:128
	ds_write_b128 v150, v[156:159] offset:256
	ds_write_b128 v150, v[160:163] offset:384
	s_cbranch_scc1 .LBB0_293
	s_cmpk_lt_u32 s44, 0x4000
	s_cselect_b64 s[0:1], -1, 0
	s_cmpk_gt_u32 s44, 0x3fff
	s_mov_b64 s[14:15], -1
	s_waitcnt lgkmcnt(0)
	s_barrier
	s_cbranch_scc0 .LBB0_310
	s_add_i32 s4, s44, 0xffffc000
	s_lshr_b32 s4, s4, 8
	s_lshr_b32 s36, s44, 4
	s_lshl_b64 s[10:11], s[4:5], 22
	s_add_u32 s10, s39, s10
	s_addc_u32 s11, s40, s11
	s_mov_b64 s[14:15], 0

; #define LAS __attribute__((address_space(3)))
; __device__ __forceinline__ unsigned pk4_fp8(float a, float b, float c, float d) { int w = __builtin_amdgcn_cvt_pk_fp8_f32(a, b, 0, false); w = __builtin_amdgcn_cvt_pk_fp8_f32(c, d, w, true); return (unsigned)w; }
;     __device__ __forceinline__ CvtDesc desc(int qq) const { return cvt_desc(*F, item_of(qq), qq & 1, h); }
; __device__ __forceinline__ void cvt_to_lds(const CvtBuf& b, const CvtDesc& d, LAS unsigned char* img, const LAS float* gl, int sub2, int h, int lane) {
;     const int hh = lane >> 5, l5 = lane & 31;
;     float gs[16];
;     const bool use_g = d.map == 2;
; #pragma unroll
;     for (int q = 0; q < 4; ++q) { const f32x4 gv = *(const LAS f32x4*)(gl + d.k0 + 16 * hh + 4 * q);
; #pragma unroll
;         for (int j = 0; j < 4; ++j) gs[4 * q + j] = use_g ? gv[j] : WSCALE; }
;     const int c8 = 4 * h + 2 * sub2 + hh;
; #pragma unroll
;     for (int j = 0; j < 4; ++j) { u32x4 o;
; #pragma unroll
;         for (int q = 0; q < 4; ++q) { const int i = 4 * q; o[q] = pk4_fp8(b.v[i][j] * gs[i], b.v[i + 1][j] * gs[i + 1], b.v[i + 2][j] * gs[i + 2], b.v[i + 3][j] * gs[i + 3]); }
;         *(LAS u32x4*)(img + (4 * l5 + j) * 128 + 16 * (c8 ^ (l5 & 7))) = o; }
; }
;     __device__ __forceinline__ void proc() { cvt_to_lds(buf, desc(q), img, gl, q & 1, h, F->lane); if (q & 1) fitem = item_of(q); ++q; }
.LBB0_448:
	s_xor_b64 s[94:95], s[92:93], -1
	s_xor_b64 s[90:91], s[96:97], -1
	s_cmp_lt_i32 s38, 2
	s_mov_b64 s[6:7], -1
	s_cbranch_scc1 .LBB0_452
	s_cmp_eq_u32 s38, 2
	s_mov_b32 s61, s14
	s_mov_b32 s11, s38
	s_mov_b32 s62, s58
	s_cbranch_scc0 .LBB0_451
	s_ashr_i32 s6, s58, 1
	s_mul_i32 s6, s6, s55
	s_add_i32 s6, s6, s3
	s_cmpk_lt_i32 s6, 0x4000
	s_cselect_b64 vcc, -1, 0
	s_and_b64 s[66:67], vcc, exec
	s_cselect_b32 s7, 5, 4
	s_lshr_b32 s7, s6, s7
	s_lshl_b32 s7, s7, 9
	s_and_b32 s7, s7, 0x1e00
	s_lshl_b32 s11, s58, 7
	s_add_i32 s7, s76, s7
	s_and_b32 s11, s11, 0x80
	s_add_i32 s7, s7, s11
	v_add_u32_e32 v2, s7, v198
	ds_read_b128 v[36:39], v2 offset:49152
	ds_read_b128 v[40:43], v2 offset:49168
	ds_read_b128 v[44:47], v2 offset:49184
	ds_read_b128 v[48:51], v2 offset:49200
	s_lshl_b32 s7, s58, 1
	s_and_b32 s7, s7, 2
	s_waitcnt lgkmcnt(0)
	v_cndmask_b32_e32 v2, v215, v36, vcc
	v_cndmask_b32_e32 v52, v215, v37, vcc
	v_bitop3_b32 v36, s7, v200, v202 bitop3:0x36
	v_cndmask_b32_e32 v53, v215, v38, vcc
	v_lshl_add_u32 v55, v36, 4, v199
	s_waitcnt vmcnt(0)
	v_mul_f32_e32 v37, v108, v2
	v_mul_f32_e32 v38, v104, v52
	v_cvt_pk_fp8_f32 v36, v37, v38
	v_cndmask_b32_e32 v54, v215, v39, vcc
	s_waitcnt lgkmcnt(2)
	v_cndmask_b32_e32 v40, v215, v40, vcc
	v_cndmask_b32_e32 v41, v215, v41, vcc
	v_mul_f32_e32 v39, v156, v53
	v_mul_f32_e32 v56, v144, v54
	v_cvt_pk_fp8_f32 v36, v39, v56 op_sel:[0,0,1]
	v_mul_f32_e32 v38, v152, v40
	v_mul_f32_e32 v39, v140, v41
	v_cvt_pk_fp8_f32 v37, v38, v39
	v_cndmask_b32_e32 v42, v215, v42, vcc
	v_cndmask_b32_e32 v43, v215, v43, vcc
	s_waitcnt lgkmcnt(1)
	v_cndmask_b32_e32 v44, v215, v44, vcc
	v_cndmask_b32_e32 v45, v215, v45, vcc
	v_mul_f32_e32 v56, v136, v42
	v_mul_f32_e32 v57, v128, v43
	v_cvt_pk_fp8_f32 v37, v56, v57 op_sel:[0,0,1]
	v_mul_f32_e32 v39, v116, v44
	v_mul_f32_e32 v56, v124, v45
	v_cvt_pk_fp8_f32 v38, v39, v56
	v_cndmask_b32_e32 v46, v215, v46, vcc
	v_cndmask_b32_e32 v47, v215, v47, vcc
	s_waitcnt lgkmcnt(0)
	v_cndmask_b32_e32 v48, v215, v48, vcc
	v_cndmask_b32_e32 v49, v215, v49, vcc
	v_mul_f32_e32 v57, v132, v46
	v_mul_f32_e32 v58, v148, v47
	v_cvt_pk_fp8_f32 v38, v57, v58 op_sel:[0,0,1]
	v_mul_f32_e32 v56, v112, v48
	v_mul_f32_e32 v57, v120, v49
	v_cvt_pk_fp8_f32 v39, v56, v57
	v_cndmask_b32_e32 v50, v215, v50, vcc
	v_cndmask_b32_e32 v51, v215, v51, vcc
	v_mul_f32_e32 v58, v96, v50
	v_mul_f32_e32 v59, v100, v51
	v_cvt_pk_fp8_f32 v39, v58, v59 op_sel:[0,0,1]
	v_mul_f32_e32 v56, v145, v54
	v_mul_f32_e32 v57, v129, v43
	v_mul_f32_e32 v58, v149, v47
	ds_write_b128 v55, v[36:39]
	v_mul_f32_e32 v37, v109, v2
	v_mul_f32_e32 v38, v105, v52
	v_cvt_pk_fp8_f32 v36, v37, v38
	v_mul_f32_e32 v39, v157, v53
	v_mul_f32_e32 v38, v153, v40
	v_cvt_pk_fp8_f32 v36, v39, v56 op_sel:[0,0,1]
	v_mul_f32_e32 v39, v141, v41
	v_cvt_pk_fp8_f32 v37, v38, v39
	v_mul_f32_e32 v56, v137, v42
	v_mul_f32_e32 v39, v117, v44
	v_cvt_pk_fp8_f32 v37, v56, v57 op_sel:[0,0,1]
	v_mul_f32_e32 v56, v125, v45
	v_cvt_pk_fp8_f32 v38, v39, v56
	v_mul_f32_e32 v57, v133, v46
	v_mul_f32_e32 v56, v113, v48
	v_cvt_pk_fp8_f32 v38, v57, v58 op_sel:[0,0,1]
	v_mul_f32_e32 v57, v121, v49
	v_cvt_pk_fp8_f32 v39, v56, v57
	v_mul_f32_e32 v58, v97, v50
	v_mul_f32_e32 v59, v101, v51
	v_mul_f32_e32 v56, v146, v54
	v_cvt_pk_fp8_f32 v39, v58, v59 op_sel:[0,0,1]
	v_mul_f32_e32 v57, v130, v43
	v_mul_f32_e32 v58, v150, v47
	v_mul_f32_e32 v59, v102, v51
	ds_write_b128 v55, v[36:39] offset:128
	v_mul_f32_e32 v37, v110, v2
	v_mul_f32_e32 v38, v106, v52
	v_cvt_pk_fp8_f32 v36, v37, v38
	v_mul_f32_e32 v39, v158, v53
	v_mul_f32_e32 v38, v154, v40
	v_cvt_pk_fp8_f32 v36, v39, v56 op_sel:[0,0,1]
	v_mul_f32_e32 v39, v142, v41
	v_cvt_pk_fp8_f32 v37, v38, v39
	v_mul_f32_e32 v56, v138, v42
	v_mul_f32_e32 v39, v118, v44
	v_cvt_pk_fp8_f32 v37, v56, v57 op_sel:[0,0,1]
	v_mul_f32_e32 v56, v126, v45
	v_cvt_pk_fp8_f32 v38, v39, v56
	v_mul_f32_e32 v57, v134, v46
	v_mul_f32_e32 v56, v114, v48
	v_cvt_pk_fp8_f32 v38, v57, v58 op_sel:[0,0,1]
	v_mul_f32_e32 v57, v122, v49
	v_cvt_pk_fp8_f32 v39, v56, v57
	v_mul_f32_e32 v58, v98, v50
	v_mul_f32_e32 v2, v111, v2
	s_bitcmp0_b32 s58, 0
	v_cvt_pk_fp8_f32 v39, v58, v59 op_sel:[0,0,1]
	s_mov_b32 s11, 0
	s_cselect_b32 s61, s14, s6
	s_add_i32 s62, s58, 1
	ds_write_b128 v55, v[36:39] offset:256
	v_mul_f32_e32 v37, v107, v52
	v_cvt_pk_fp8_f32 v36, v2, v37
	v_mul_f32_e32 v38, v159, v53
	v_mul_f32_e32 v39, v147, v54
	v_mul_f32_e32 v2, v155, v40
	v_cvt_pk_fp8_f32 v36, v38, v39 op_sel:[0,0,1]
	v_mul_f32_e32 v38, v143, v41
	v_cvt_pk_fp8_f32 v37, v2, v38
	v_mul_f32_e32 v39, v139, v42
	v_mul_f32_e32 v40, v131, v43
	v_mul_f32_e32 v2, v119, v44
	v_cvt_pk_fp8_f32 v37, v39, v40 op_sel:[0,0,1]
	v_mul_f32_e32 v39, v127, v45
	v_cvt_pk_fp8_f32 v38, v2, v39
	v_mul_f32_e32 v40, v135, v46
	v_mul_f32_e32 v41, v151, v47
	v_mul_f32_e32 v2, v115, v48
	v_cvt_pk_fp8_f32 v38, v40, v41 op_sel:[0,0,1]
	v_mul_f32_e32 v40, v123, v49
	v_cvt_pk_fp8_f32 v39, v2, v40
	v_mul_f32_e32 v41, v99, v50
	v_mul_f32_e32 v42, v103, v51
	v_cvt_pk_fp8_f32 v39, v41, v42 op_sel:[0,0,1]
	ds_write_b128 v55, v[36:39] offset:384

; #define LAS __attribute__((address_space(3)))
; __device__ __forceinline__ unsigned pk4_fp8(float a, float b, float c, float d) { int w = __builtin_amdgcn_cvt_pk_fp8_f32(a, b, 0, false); w = __builtin_amdgcn_cvt_pk_fp8_f32(c, d, w, true); return (unsigned)w; }
;     __device__ __forceinline__ CvtDesc desc(int qq) const { return cvt_desc(*F, item_of(qq), qq & 1, h); }
; __device__ __forceinline__ void cvt_to_lds(const CvtBuf& b, const CvtDesc& d, LAS unsigned char* img, const LAS float* gl, int sub2, int h, int lane) {
;     const int hh = lane >> 5, l5 = lane & 31;
;     float gs[16];
;     const bool use_g = d.map == 2;
; #pragma unroll
;     for (int q = 0; q < 4; ++q) { const f32x4 gv = *(const LAS f32x4*)(gl + d.k0 + 16 * hh + 4 * q);
; #pragma unroll
;         for (int j = 0; j < 4; ++j) gs[4 * q + j] = use_g ? gv[j] : WSCALE; }
;     const int c8 = 4 * h + 2 * sub2 + hh;
; #pragma unroll
;     for (int j = 0; j < 4; ++j) { u32x4 o;
; #pragma unroll
;         for (int q = 0; q < 4; ++q) { const int i = 4 * q; o[q] = pk4_fp8(b.v[i][j] * gs[i], b.v[i + 1][j] * gs[i + 1], b.v[i + 2][j] * gs[i + 2], b.v[i + 3][j] * gs[i + 3]); }
;         *(LAS u32x4*)(img + (4 * l5 + j) * 128 + 16 * (c8 ^ (l5 & 7))) = o; }
; }
;     __device__ __forceinline__ void proc() { cvt_to_lds(buf, desc(q), img, gl, q & 1, h, F->lane); if (q & 1) fitem = item_of(q); ++q; }
.LBB0_613:
	s_ashr_i32 s6, s62, 1
	s_mul_i32 s6, s6, s55
	s_add_i32 s6, s6, s3
	s_cmpk_lt_i32 s6, 0x4000
	s_cselect_b64 vcc, -1, 0
	s_and_b64 s[10:11], vcc, exec
	s_cselect_b32 s7, 5, 4
	s_lshr_b32 s7, s6, s7
	s_lshl_b32 s7, s7, 9
	s_and_b32 s7, s7, 0x1e00
	s_lshl_b32 s10, s62, 7
	s_add_i32 s7, s12, s7
	s_and_b32 s10, s10, 0x80
	s_add_i32 s7, s7, s10
	v_add_u32_e32 v46, s7, v166
	ds_read_b128 v[34:37], v46 offset:49152
	ds_read_b128 v[38:41], v46 offset:49168
	ds_read_b128 v[42:45], v46 offset:49184
	ds_read_b128 v[46:49], v46 offset:49200
	s_lshl_b32 s7, s62, 1
	s_and_b32 s7, s7, 2
	s_waitcnt lgkmcnt(0)
	v_cndmask_b32_e32 v50, v183, v34, vcc
	v_cndmask_b32_e32 v51, v183, v35, vcc
	v_bitop3_b32 v34, s7, v168, v172 bitop3:0x36
	v_cndmask_b32_e32 v52, v183, v36, vcc
	v_lshl_add_u32 v54, v34, 4, v167
	s_waitcnt vmcnt(0)
	v_mul_f32_e32 v35, v108, v50
	v_mul_f32_e32 v36, v104, v51
	v_cvt_pk_fp8_f32 v34, v35, v36
	v_cndmask_b32_e32 v53, v183, v37, vcc
	s_waitcnt lgkmcnt(2)
	v_cndmask_b32_e32 v38, v183, v38, vcc
	v_cndmask_b32_e32 v39, v183, v39, vcc
	v_mul_f32_e32 v37, v156, v52
	v_mul_f32_e32 v55, v144, v53
	v_cvt_pk_fp8_f32 v34, v37, v55 op_sel:[0,0,1]
	v_mul_f32_e32 v36, v152, v38
	v_mul_f32_e32 v37, v140, v39
	v_cvt_pk_fp8_f32 v35, v36, v37
	v_cndmask_b32_e32 v40, v183, v40, vcc
	v_cndmask_b32_e32 v41, v183, v41, vcc
	s_waitcnt lgkmcnt(1)
	v_cndmask_b32_e32 v42, v183, v42, vcc
	v_cndmask_b32_e32 v43, v183, v43, vcc
	v_mul_f32_e32 v55, v136, v40
	v_mul_f32_e32 v56, v128, v41
	v_cvt_pk_fp8_f32 v35, v55, v56 op_sel:[0,0,1]
	v_mul_f32_e32 v37, v116, v42
	v_mul_f32_e32 v55, v124, v43
	v_cvt_pk_fp8_f32 v36, v37, v55
	v_cndmask_b32_e32 v44, v183, v44, vcc
	v_cndmask_b32_e32 v45, v183, v45, vcc
	s_waitcnt lgkmcnt(0)
	v_cndmask_b32_e32 v46, v183, v46, vcc
	v_cndmask_b32_e32 v47, v183, v47, vcc
	v_mul_f32_e32 v56, v132, v44
	v_mul_f32_e32 v57, v148, v45
	v_cvt_pk_fp8_f32 v36, v56, v57 op_sel:[0,0,1]
	v_mul_f32_e32 v55, v112, v46
	v_mul_f32_e32 v56, v120, v47
	v_cvt_pk_fp8_f32 v37, v55, v56
	v_cndmask_b32_e32 v48, v183, v48, vcc
	v_cndmask_b32_e32 v49, v183, v49, vcc
	v_mul_f32_e32 v57, v96, v48
	v_mul_f32_e32 v58, v100, v49
	v_cvt_pk_fp8_f32 v37, v57, v58 op_sel:[0,0,1]
	v_mul_f32_e32 v55, v145, v53
	v_mul_f32_e32 v56, v129, v41
	v_mul_f32_e32 v57, v149, v45
	ds_write_b128 v54, v[34:37]
	v_mul_f32_e32 v35, v109, v50
	v_mul_f32_e32 v36, v105, v51
	v_cvt_pk_fp8_f32 v34, v35, v36
	v_mul_f32_e32 v37, v157, v52
	v_mul_f32_e32 v36, v153, v38
	v_cvt_pk_fp8_f32 v34, v37, v55 op_sel:[0,0,1]
	v_mul_f32_e32 v37, v141, v39
	v_cvt_pk_fp8_f32 v35, v36, v37
	v_mul_f32_e32 v55, v137, v40
	v_mul_f32_e32 v37, v117, v42
	v_cvt_pk_fp8_f32 v35, v55, v56 op_sel:[0,0,1]
	v_mul_f32_e32 v55, v125, v43
	v_cvt_pk_fp8_f32 v36, v37, v55
	v_mul_f32_e32 v56, v133, v44
	v_mul_f32_e32 v55, v113, v46
	v_cvt_pk_fp8_f32 v36, v56, v57 op_sel:[0,0,1]
	v_mul_f32_e32 v56, v121, v47
	v_cvt_pk_fp8_f32 v37, v55, v56
	v_mul_f32_e32 v57, v97, v48
	v_mul_f32_e32 v58, v101, v49
	v_mul_f32_e32 v55, v146, v53
	v_cvt_pk_fp8_f32 v37, v57, v58 op_sel:[0,0,1]
	v_mul_f32_e32 v56, v130, v41
	v_mul_f32_e32 v57, v150, v45
	v_mul_f32_e32 v58, v102, v49
	ds_write_b128 v54, v[34:37] offset:128
	v_mul_f32_e32 v35, v110, v50
	v_mul_f32_e32 v36, v106, v51
	v_cvt_pk_fp8_f32 v34, v35, v36
	v_mul_f32_e32 v37, v158, v52
	v_mul_f32_e32 v36, v154, v38
	v_cvt_pk_fp8_f32 v34, v37, v55 op_sel:[0,0,1]
	v_mul_f32_e32 v37, v142, v39
	v_cvt_pk_fp8_f32 v35, v36, v37
	v_mul_f32_e32 v55, v138, v40
	v_mul_f32_e32 v37, v118, v42
	v_cvt_pk_fp8_f32 v35, v55, v56 op_sel:[0,0,1]
	v_mul_f32_e32 v55, v126, v43
	v_cvt_pk_fp8_f32 v36, v37, v55
	v_mul_f32_e32 v56, v134, v44
	v_mul_f32_e32 v55, v114, v46
	v_cvt_pk_fp8_f32 v36, v56, v57 op_sel:[0,0,1]
	v_mul_f32_e32 v56, v122, v47
	v_cvt_pk_fp8_f32 v37, v55, v56
	v_mul_f32_e32 v57, v98, v48
	s_bitcmp0_b32 s62, 0
	s_mov_b32 s11, 0
	v_cvt_pk_fp8_f32 v37, v57, v58 op_sel:[0,0,1]
	s_cselect_b32 s61, s14, s6
	s_add_i32 s10, s62, 1
	ds_write_b128 v54, v[34:37] offset:256
	v_mul_f32_e32 v35, v111, v50
	v_mul_f32_e32 v36, v107, v51
	v_cvt_pk_fp8_f32 v34, v35, v36
	v_mul_f32_e32 v37, v159, v52
	v_mul_f32_e32 v50, v147, v53
	v_mul_f32_e32 v36, v155, v38
	v_cvt_pk_fp8_f32 v34, v37, v50 op_sel:[0,0,1]
	v_mul_f32_e32 v37, v143, v39
	v_cvt_pk_fp8_f32 v35, v36, v37
	v_mul_f32_e32 v38, v139, v40
	v_mul_f32_e32 v39, v131, v41
	v_mul_f32_e32 v37, v119, v42
	v_cvt_pk_fp8_f32 v35, v38, v39 op_sel:[0,0,1]
	v_mul_f32_e32 v38, v127, v43
	v_cvt_pk_fp8_f32 v36, v37, v38
	v_mul_f32_e32 v39, v135, v44
	v_mul_f32_e32 v40, v151, v45
	v_mul_f32_e32 v38, v115, v46
	v_cvt_pk_fp8_f32 v36, v39, v40 op_sel:[0,0,1]
	v_mul_f32_e32 v39, v123, v47
	v_cvt_pk_fp8_f32 v37, v38, v39
	v_mul_f32_e32 v40, v99, v48
	v_mul_f32_e32 v41, v103, v49
	v_cvt_pk_fp8_f32 v37, v40, v41 op_sel:[0,0,1]
	ds_write_b128 v54, v[34:37] offset:384
	s_cbranch_execnz .LBB0_593
	s_branch .LBB0_590

; #define LAS __attribute__((address_space(3)))
; __device__ __forceinline__ unsigned pk4_fp8(float a, float b, float c, float d) { int w = __builtin_amdgcn_cvt_pk_fp8_f32(a, b, 0, false); w = __builtin_amdgcn_cvt_pk_fp8_f32(c, d, w, true); return (unsigned)w; }
;     __device__ __forceinline__ void proc() { cvt_to_lds(buf, desc(q), img, gl, q & 1, h, F->lane); if (q & 1) fitem = item_of(q); ++q; }
;     __device__ __forceinline__ void flush() { if (fitem >= 0) { cvt_flush(cvt_desc(*F, fitem, 0, h), img, h, F->lane); fitem = -1; } }
; __device__ __forceinline__ void cvt_to_lds(const CvtBuf& b, const CvtDesc& d, LAS unsigned char* img, const LAS float* gl, int sub2, int h, int lane) {
;     const int hh = lane >> 5, l5 = lane & 31;
;     float gs[16];
;     const bool use_g = d.map == 2;
; #pragma unroll
;     for (int q = 0; q < 4; ++q) { const f32x4 gv = *(const LAS f32x4*)(gl + d.k0 + 16 * hh + 4 * q);
; #pragma unroll
;         for (int j = 0; j < 4; ++j) gs[4 * q + j] = use_g ? gv[j] : WSCALE; }
;     const int c8 = 4 * h + 2 * sub2 + hh;
; #pragma unroll
;     for (int j = 0; j < 4; ++j) { u32x4 o;
; #pragma unroll
;         for (int q = 0; q < 4; ++q) { const int i = 4 * q; o[q] = pk4_fp8(b.v[i][j] * gs[i], b.v[i + 1][j] * gs[i + 1], b.v[i + 2][j] * gs[i + 2], b.v[i + 3][j] * gs[i + 3]); }
;         *(LAS u32x4*)(img + (4 * l5 + j) * 128 + 16 * (c8 ^ (l5 & 7))) = o; }
; }
;     __device__ __forceinline__ void drain() {
;         __syncthreads(); flush(); __syncthreads();
;         if (state != 0) { proc(); state = 0; if (fitem >= 0) { __syncthreads(); flush(); __syncthreads(); } }
;         if (q >= nq) { __syncthreads(); return; }
.LBB0_670:
	s_cmp_eq_u32 s38, 0
	s_barrier
	s_cbranch_scc1 .LBB0_680
	s_ashr_i32 s0, s10, 1
	s_mul_i32 s0, s0, s55
	s_add_i32 s0, s0, s3
	s_cmpk_lt_i32 s0, 0x4000
	s_cselect_b64 vcc, -1, 0
	s_and_b64 s[4:5], vcc, exec
	s_cselect_b32 s1, 5, 4
	s_lshr_b32 s1, s0, s1
	s_lshl_b32 s1, s1, 9
	s_and_b32 s1, s1, 0x1e00
	s_add_i32 s1, s1, 0
	s_lshl_b32 s4, s49, 8
	s_add_i32 s1, s1, s4
	s_lshl_b32 s4, s10, 7
	s_and_b32 s4, s4, 0x80
	v_lshrrev_b32_e32 v18, 5, v190
	s_add_i32 s1, s1, s4
	v_lshl_add_u32 v14, v18, 6, s1
	ds_read_b128 v[2:5], v14 offset:49152
	ds_read_b128 v[6:9], v14 offset:49168
	ds_read_b128 v[10:13], v14 offset:49184
	ds_read_b128 v[14:17], v14 offset:49200
	s_lshl_b32 s4, s10, 1
	v_mov_b32_e32 v1, 0x42800000
	s_lshl_b32 s1, s49, 2
	s_and_b32 s4, s4, 2
	s_waitcnt lgkmcnt(3)
	v_cndmask_b32_e32 v20, v1, v3, vcc
	s_or_b32 s1, s4, s1
	v_and_b32_e32 v3, 7, v0
	v_cndmask_b32_e32 v19, v1, v2, vcc
	v_lshlrev_b32_e32 v2, 9, v0
	v_bitop3_b32 v3, s1, v3, v18 bitop3:0x36
	v_and_b32_e32 v2, 0x3e00, v2
	v_lshlrev_b32_e32 v3, 4, v3
	v_cndmask_b32_e32 v21, v1, v4, vcc
	v_cndmask_b32_e32 v22, v1, v5, vcc
	s_waitcnt lgkmcnt(2)
	v_cndmask_b32_e32 v23, v1, v6, vcc
	v_cndmask_b32_e32 v24, v1, v7, vcc
	v_cndmask_b32_e32 v25, v1, v8, vcc
	v_cndmask_b32_e32 v26, v1, v9, vcc
	s_waitcnt lgkmcnt(1)
	v_cndmask_b32_e32 v27, v1, v10, vcc
	v_cndmask_b32_e32 v28, v1, v11, vcc
	v_cndmask_b32_e32 v29, v1, v12, vcc
	v_cndmask_b32_e32 v30, v1, v13, vcc
	s_waitcnt lgkmcnt(0)
	v_cndmask_b32_e32 v31, v1, v14, vcc
	v_cndmask_b32_e32 v32, v1, v15, vcc
	v_cndmask_b32_e32 v16, v1, v16, vcc
	v_cndmask_b32_e32 v1, v1, v17, vcc
	v_add3_u32 v17, s50, v2, v3
	v_mul_f32_e32 v3, v108, v19
	v_mul_f32_e32 v4, v104, v20
	v_cvt_pk_fp8_f32 v2, v3, v4
	v_mul_f32_e32 v4, v152, v23
	v_mul_f32_e32 v7, v140, v24
	v_cvt_pk_fp8_f32 v3, v4, v7
	v_mul_f32_e32 v5, v156, v21
	v_mul_f32_e32 v6, v144, v22
	v_cvt_pk_fp8_f32 v2, v5, v6 op_sel:[0,0,1]
	v_mul_f32_e32 v4, v136, v25
	v_mul_f32_e32 v5, v128, v26
	v_cvt_pk_fp8_f32 v3, v4, v5 op_sel:[0,0,1]
	v_mul_f32_e32 v5, v116, v27
	v_mul_f32_e32 v6, v124, v28
	v_cvt_pk_fp8_f32 v4, v5, v6
	v_mul_f32_e32 v6, v112, v31
	v_mul_f32_e32 v9, v120, v32
	v_cvt_pk_fp8_f32 v5, v6, v9
	v_mul_f32_e32 v7, v132, v29
	v_mul_f32_e32 v8, v148, v30
	v_cvt_pk_fp8_f32 v4, v7, v8 op_sel:[0,0,1]
	v_mul_f32_e32 v6, v96, v16
	v_mul_f32_e32 v7, v100, v1
	v_cvt_pk_fp8_f32 v5, v6, v7 op_sel:[0,0,1]
	v_mul_f32_e32 v7, v109, v19
	v_mul_f32_e32 v8, v105, v20
	v_cvt_pk_fp8_f32 v6, v7, v8
	v_mul_f32_e32 v8, v153, v23
	v_mul_f32_e32 v11, v141, v24
	v_cvt_pk_fp8_f32 v7, v8, v11
	v_mul_f32_e32 v9, v157, v21
	v_mul_f32_e32 v10, v145, v22
	v_cvt_pk_fp8_f32 v6, v9, v10 op_sel:[0,0,1]
	v_mul_f32_e32 v8, v137, v25
	v_mul_f32_e32 v9, v129, v26
	v_cvt_pk_fp8_f32 v7, v8, v9 op_sel:[0,0,1]
	v_mul_f32_e32 v9, v117, v27
	v_mul_f32_e32 v10, v125, v28
	v_cvt_pk_fp8_f32 v8, v9, v10
	v_mul_f32_e32 v10, v113, v31
	v_mul_f32_e32 v13, v121, v32
	v_cvt_pk_fp8_f32 v9, v10, v13
	v_mul_f32_e32 v11, v133, v29
	v_mul_f32_e32 v12, v149, v30
	v_cvt_pk_fp8_f32 v8, v11, v12 op_sel:[0,0,1]
	v_mul_f32_e32 v10, v97, v16
	v_mul_f32_e32 v11, v101, v1
	v_cvt_pk_fp8_f32 v9, v10, v11 op_sel:[0,0,1]
	v_mul_f32_e32 v11, v110, v19
	v_mul_f32_e32 v12, v106, v20
	v_cvt_pk_fp8_f32 v10, v11, v12
	v_mul_f32_e32 v12, v154, v23
	v_mul_f32_e32 v15, v142, v24
	v_cvt_pk_fp8_f32 v11, v12, v15
	v_mul_f32_e32 v13, v158, v21
	v_mul_f32_e32 v14, v146, v22
	v_cvt_pk_fp8_f32 v10, v13, v14 op_sel:[0,0,1]
	v_mul_f32_e32 v12, v138, v25
	v_mul_f32_e32 v13, v130, v26
	v_cvt_pk_fp8_f32 v11, v12, v13 op_sel:[0,0,1]
	v_mul_f32_e32 v13, v118, v27
	v_mul_f32_e32 v14, v126, v28
	v_cvt_pk_fp8_f32 v12, v13, v14
	v_mul_f32_e32 v14, v114, v31
	v_mul_f32_e32 v33, v122, v32
	v_cvt_pk_fp8_f32 v13, v14, v33
	v_mul_f32_e32 v15, v134, v29
	v_mul_f32_e32 v18, v150, v30
	v_cvt_pk_fp8_f32 v12, v15, v18 op_sel:[0,0,1]
	v_mul_f32_e32 v14, v98, v16
	v_mul_f32_e32 v15, v102, v1
	v_cvt_pk_fp8_f32 v13, v14, v15 op_sel:[0,0,1]
	ds_write_b128 v17, v[2:5]
	ds_write_b128 v17, v[6:9] offset:128
	ds_write_b128 v17, v[10:13] offset:256
	v_mul_f32_e32 v2, v111, v19
	v_mul_f32_e32 v3, v107, v20
	v_cvt_pk_fp8_f32 v12, v2, v3
	v_mul_f32_e32 v2, v155, v23
	v_mul_f32_e32 v3, v143, v24
	v_cvt_pk_fp8_f32 v13, v2, v3
	v_mul_f32_e32 v2, v139, v25
	v_mul_f32_e32 v3, v131, v26
	v_cvt_pk_fp8_f32 v13, v2, v3 op_sel:[0,0,1]
	v_mul_f32_e32 v2, v119, v27
	v_mul_f32_e32 v3, v127, v28
	v_cvt_pk_fp8_f32 v14, v2, v3
	v_mul_f32_e32 v2, v115, v31
	v_mul_f32_e32 v3, v123, v32
	v_cvt_pk_fp8_f32 v15, v2, v3
	v_mul_f32_e32 v4, v159, v21
	v_mul_f32_e32 v5, v147, v22
	v_cvt_pk_fp8_f32 v12, v4, v5 op_sel:[0,0,1]
	v_mul_f32_e32 v4, v135, v29
	v_mul_f32_e32 v5, v151, v30
	v_mul_f32_e32 v2, v99, v16
	v_mul_f32_e32 v1, v103, v1
	v_cvt_pk_fp8_f32 v14, v4, v5 op_sel:[0,0,1]
	v_cvt_pk_fp8_f32 v15, v2, v1 op_sel:[0,0,1]
	s_bitcmp0_b32 s10, 0
	s_cselect_b32 s61, s61, s0
	s_cmp_lt_i32 s61, 0
	ds_write_b128 v17, v[12:15] offset:384
	s_cbranch_scc1 .LBB0_679
	s_cmpk_lt_u32 s61, 0x4000
	s_cselect_b64 s[0:1], -1, 0
	s_cmpk_gt_u32 s61, 0x3fff
	s_waitcnt lgkmcnt(0)
	s_barrier
	s_cbranch_scc0 .LBB0_674
	s_add_i32 s4, s61, 0xffffc000
	s_lshr_b32 s4, s4, 8
	s_mov_b32 s5, 0
	s_lshr_b32 s9, s61, 4
	s_and_b32 s8, s61, 15
	s_lshl_b64 s[4:5], s[4:5], 22
	s_add_u32 s4, s30, s4
	s_addc_u32 s5, s31, s5
	s_add_u32 s4, s4, 0x50000000
	s_addc_u32 s5, s5, 0
	s_cbranch_execz .LBB0_675
	s_branch .LBB0_676

; #define LAS __attribute__((address_space(3)))
; __device__ __forceinline__ unsigned pk4_fp8(float a, float b, float c, float d) { int w = __builtin_amdgcn_cvt_pk_fp8_f32(a, b, 0, false); w = __builtin_amdgcn_cvt_pk_fp8_f32(c, d, w, true); return (unsigned)w; }
;     __device__ __forceinline__ CvtDesc desc(int qq) const { return cvt_desc(*F, item_of(qq), qq & 1, h); }
;     __device__ __forceinline__ void flush() { if (fitem >= 0) { cvt_flush(cvt_desc(*F, fitem, 0, h), img, h, F->lane); fitem = -1; } }
; __device__ __forceinline__ void cvt_to_lds(const CvtBuf& b, const CvtDesc& d, LAS unsigned char* img, const LAS float* gl, int sub2, int h, int lane) {
;     const int hh = lane >> 5, l5 = lane & 31;
;     float gs[16];
;     const bool use_g = d.map == 2;
; #pragma unroll
;     for (int q = 0; q < 4; ++q) { const f32x4 gv = *(const LAS f32x4*)(gl + d.k0 + 16 * hh + 4 * q);
; #pragma unroll
;         for (int j = 0; j < 4; ++j) gs[4 * q + j] = use_g ? gv[j] : WSCALE; }
;     const int c8 = 4 * h + 2 * sub2 + hh;
; #pragma unroll
;     for (int j = 0; j < 4; ++j) { u32x4 o;
; #pragma unroll
;         for (int q = 0; q < 4; ++q) { const int i = 4 * q; o[q] = pk4_fp8(b.v[i][j] * gs[i], b.v[i + 1][j] * gs[i + 1], b.v[i + 2][j] * gs[i + 2], b.v[i + 3][j] * gs[i + 3]); }
;         *(LAS u32x4*)(img + (4 * l5 + j) * 128 + 16 * (c8 ^ (l5 & 7))) = o; }
; }
;     __device__ __forceinline__ void drain() {
;     ...
;         while (q < nq) {
;             if (q + 1 < nq) cvt_load(b2, desc(q + 1), F->lane);
;             cvt_to_lds(buf, desc(q), img, gl, q & 1, h, F->lane); if (q & 1) fitem = item_of(q); ++q;
;             if (fitem >= 0) { __syncthreads(); flush(); __syncthreads(); }
.LBB0_695:
	s_ashr_i32 s0, s10, 1
	s_mul_i32 s0, s0, s55
	s_add_i32 s0, s0, s3
	s_cmpk_lt_i32 s0, 0x4000
	s_cselect_b64 vcc, -1, 0
	s_and_b64 s[14:15], vcc, exec
	s_cselect_b32 s1, 5, 4
	s_lshr_b32 s1, s0, s1
	s_lshl_b32 s4, s10, 5
	s_lshl_b32 s1, s1, 9
	s_and_b32 s41, s4, 32
	s_and_b32 s1, s1, 0x1e00
	s_add_i32 s1, s11, s1
	s_lshl_b32 s4, s41, 2
	s_add_i32 s1, s1, s4
	v_add_u32_e32 v130, s1, v133
	ds_read_b128 v[152:155], v130 offset:49152
	ds_read_b128 v[156:159], v130 offset:49168
	ds_read_b128 v[160:163], v130 offset:49184
	ds_read_b128 v[164:167], v130 offset:49200
	s_lshl_b32 s1, s10, 1
	s_waitcnt lgkmcnt(3)
	v_cndmask_b32_e32 v130, v151, v152, vcc
	v_cndmask_b32_e32 v136, v151, v153, vcc
	v_cndmask_b32_e32 v137, v151, v154, vcc
	s_waitcnt lgkmcnt(2)
	v_cndmask_b32_e32 v169, v151, v156, vcc
	v_cndmask_b32_e32 v170, v151, v157, vcc
	s_waitcnt vmcnt(31)
	v_mul_f32_e32 v153, v2, v130
	s_waitcnt vmcnt(30)
	v_mul_f32_e32 v154, v6, v136
	v_cvt_pk_fp8_f32 v152, v153, v154
	s_waitcnt vmcnt(27)
	v_mul_f32_e32 v154, v18, v169
	s_waitcnt vmcnt(26)
	v_mul_f32_e32 v157, v22, v170
	v_cvt_pk_fp8_f32 v153, v154, v157
	v_cndmask_b32_e32 v168, v151, v155, vcc
	v_cndmask_b32_e32 v171, v151, v158, vcc
	v_cndmask_b32_e32 v172, v151, v159, vcc
	v_mul_f32_e32 v155, v10, v137
	v_mul_f32_e32 v156, v14, v168
	s_waitcnt lgkmcnt(1)
	v_cndmask_b32_e32 v173, v151, v160, vcc
	v_cndmask_b32_e32 v174, v151, v161, vcc
	v_cvt_pk_fp8_f32 v152, v155, v156 op_sel:[0,0,1]
	s_waitcnt vmcnt(25)
	v_mul_f32_e32 v154, v26, v171
	s_waitcnt vmcnt(24)
	v_mul_f32_e32 v155, v30, v172
	s_waitcnt lgkmcnt(0)
	v_cndmask_b32_e32 v164, v151, v164, vcc
	v_cndmask_b32_e32 v165, v151, v165, vcc
	v_cvt_pk_fp8_f32 v153, v154, v155 op_sel:[0,0,1]
	s_waitcnt vmcnt(23)
	v_mul_f32_e32 v155, v34, v173
	s_waitcnt vmcnt(22)
	v_mul_f32_e32 v156, v38, v174
	v_cvt_pk_fp8_f32 v154, v155, v156
	s_waitcnt vmcnt(19)
	v_mul_f32_e32 v156, v50, v164
	s_waitcnt vmcnt(18)
	v_mul_f32_e32 v159, v54, v165
	v_cvt_pk_fp8_f32 v155, v156, v159
	v_cndmask_b32_e32 v175, v151, v162, vcc
	v_cndmask_b32_e32 v176, v151, v163, vcc
	v_cndmask_b32_e32 v166, v151, v166, vcc
	v_cndmask_b32_e32 v167, v151, v167, vcc
	v_mul_f32_e32 v157, v42, v175
	v_mul_f32_e32 v158, v46, v176
	v_cvt_pk_fp8_f32 v154, v157, v158 op_sel:[0,0,1]
	s_waitcnt vmcnt(17)
	v_mul_f32_e32 v156, v58, v166
	s_waitcnt vmcnt(16)
	v_mul_f32_e32 v157, v62, v167
	v_cvt_pk_fp8_f32 v155, v156, v157 op_sel:[0,0,1]
	v_mul_f32_e32 v157, v3, v130
	v_mul_f32_e32 v158, v7, v136
	v_cvt_pk_fp8_f32 v156, v157, v158
	v_mul_f32_e32 v158, v19, v169
	v_mul_f32_e32 v161, v23, v170
	v_cvt_pk_fp8_f32 v157, v158, v161
	v_mul_f32_e32 v159, v11, v137
	v_mul_f32_e32 v160, v15, v168
	v_cvt_pk_fp8_f32 v156, v159, v160 op_sel:[0,0,1]
	v_mul_f32_e32 v158, v27, v171
	v_mul_f32_e32 v159, v31, v172
	v_cvt_pk_fp8_f32 v157, v158, v159 op_sel:[0,0,1]
	v_mul_f32_e32 v159, v35, v173
	v_mul_f32_e32 v160, v39, v174
	v_cvt_pk_fp8_f32 v158, v159, v160
	v_mul_f32_e32 v160, v51, v164
	v_mul_f32_e32 v163, v55, v165
	v_cvt_pk_fp8_f32 v159, v160, v163
	v_mul_f32_e32 v161, v43, v175
	v_mul_f32_e32 v162, v47, v176
	v_cvt_pk_fp8_f32 v158, v161, v162 op_sel:[0,0,1]
	v_mul_f32_e32 v160, v59, v166
	v_mul_f32_e32 v161, v63, v167
	v_cvt_pk_fp8_f32 v159, v160, v161 op_sel:[0,0,1]
	v_mul_f32_e32 v161, v4, v130
	v_mul_f32_e32 v162, v8, v136
	v_cvt_pk_fp8_f32 v160, v161, v162
	v_mul_f32_e32 v162, v20, v169
	v_mul_f32_e32 v179, v24, v170
	v_cvt_pk_fp8_f32 v161, v162, v179
	v_mul_f32_e32 v163, v12, v137
	v_mul_f32_e32 v178, v16, v168
	v_cvt_pk_fp8_f32 v160, v163, v178 op_sel:[0,0,1]
	v_mul_f32_e32 v162, v28, v171
	v_mul_f32_e32 v163, v32, v172
	v_cvt_pk_fp8_f32 v161, v162, v163 op_sel:[0,0,1]
	v_mul_f32_e32 v163, v36, v173
	v_mul_f32_e32 v178, v40, v174
	v_cvt_pk_fp8_f32 v162, v163, v178
	v_mul_f32_e32 v178, v52, v164
	v_mul_f32_e32 v181, v56, v165
	v_cvt_pk_fp8_f32 v163, v178, v181
	v_mul_f32_e32 v179, v44, v175
	v_mul_f32_e32 v180, v48, v176
	s_and_b32 s1, s1, 2
	v_cvt_pk_fp8_f32 v162, v179, v180 op_sel:[0,0,1]
	v_mul_f32_e32 v178, v60, v166
	v_mul_f32_e32 v179, v64, v167
	v_bitop3_b32 v177, s1, v139, v141 bitop3:0x36
	v_cvt_pk_fp8_f32 v163, v178, v179 op_sel:[0,0,1]
	v_lshl_add_u32 v177, v177, 4, v138
	ds_write_b128 v177, v[152:155]
	ds_write_b128 v177, v[156:159] offset:128
	ds_write_b128 v177, v[160:163] offset:256
	v_mul_f32_e32 v130, v5, v130
	v_mul_f32_e32 v136, v9, v136
	v_cvt_pk_fp8_f32 v152, v130, v136
	v_mul_f32_e32 v130, v21, v169
	v_mul_f32_e32 v136, v25, v170
	v_cvt_pk_fp8_f32 v153, v130, v136
	v_mul_f32_e32 v137, v13, v137
	v_mul_f32_e32 v154, v17, v168
	v_mul_f32_e32 v130, v29, v171
	v_mul_f32_e32 v136, v33, v172
	v_cvt_pk_fp8_f32 v152, v137, v154 op_sel:[0,0,1]
	v_cvt_pk_fp8_f32 v153, v130, v136 op_sel:[0,0,1]
	v_mul_f32_e32 v130, v37, v173
	v_mul_f32_e32 v136, v41, v174
	v_cvt_pk_fp8_f32 v154, v130, v136
	v_mul_f32_e32 v130, v53, v164
	v_mul_f32_e32 v136, v57, v165
	v_cvt_pk_fp8_f32 v155, v130, v136
	v_mul_f32_e32 v137, v45, v175
	v_mul_f32_e32 v156, v49, v176
	v_mul_f32_e32 v130, v61, v166
	v_mul_f32_e32 v136, v65, v167
	v_cvt_pk_fp8_f32 v154, v137, v156 op_sel:[0,0,1]
	v_cvt_pk_fp8_f32 v155, v130, v136 op_sel:[0,0,1]
	s_and_b64 s[14:15], s[6:7], exec
	s_cselect_b32 s42, s61, s0
	s_cmp_lt_i32 s42, 0
	ds_write_b128 v177, v[152:155] offset:384
	s_cbranch_scc1 .LBB0_703
	s_cmpk_lt_u32 s42, 0x4000
	s_cselect_b64 s[0:1], -1, 0
	s_cmpk_gt_u32 s42, 0x3fff
	s_mov_b64 s[36:37], -1
	s_waitcnt lgkmcnt(0)
	s_barrier
	s_cbranch_scc0 .LBB0_698
	s_add_i32 s4, s42, 0xffffc000
	s_lshr_b32 s4, s4, 8
	s_lshr_b32 s43, s42, 4
	s_and_b32 s44, s42, 15
	s_lshl_b64 s[14:15], s[4:5], 22
	s_add_u32 s14, s34, s14
	s_addc_u32 s15, s35, s15
	s_mov_b64 s[36:37], 0

; #define LAS __attribute__((address_space(3)))
; __device__ __forceinline__ unsigned pk4_fp8(float a, float b, float c, float d) { int w = __builtin_amdgcn_cvt_pk_fp8_f32(a, b, 0, false); w = __builtin_amdgcn_cvt_pk_fp8_f32(c, d, w, true); return (unsigned)w; }
;     __device__ __forceinline__ CvtDesc desc(int qq) const { return cvt_desc(*F, item_of(qq), qq & 1, h); }
;     __device__ __forceinline__ void flush() { if (fitem >= 0) { cvt_flush(cvt_desc(*F, fitem, 0, h), img, h, F->lane); fitem = -1; } }
; __device__ __forceinline__ void cvt_to_lds(const CvtBuf& b, const CvtDesc& d, LAS unsigned char* img, const LAS float* gl, int sub2, int h, int lane) {
;     const int hh = lane >> 5, l5 = lane & 31;
;     float gs[16];
;     const bool use_g = d.map == 2;
; #pragma unroll
;     for (int q = 0; q < 4; ++q) { const f32x4 gv = *(const LAS f32x4*)(gl + d.k0 + 16 * hh + 4 * q);
; #pragma unroll
;         for (int j = 0; j < 4; ++j) gs[4 * q + j] = use_g ? gv[j] : WSCALE; }
;     const int c8 = 4 * h + 2 * sub2 + hh;
; #pragma unroll
;     for (int j = 0; j < 4; ++j) { u32x4 o;
; #pragma unroll
;         for (int q = 0; q < 4; ++q) { const int i = 4 * q; o[q] = pk4_fp8(b.v[i][j] * gs[i], b.v[i + 1][j] * gs[i + 1], b.v[i + 2][j] * gs[i + 2], b.v[i + 3][j] * gs[i + 3]); }
;         *(LAS u32x4*)(img + (4 * l5 + j) * 128 + 16 * (c8 ^ (l5 & 7))) = o; }
; }
;     __device__ __forceinline__ void drain() {
;     ...
;             if (q + 1 < nq) cvt_load(buf, desc(q + 1), F->lane);
;             cvt_to_lds(b2, desc(q), img, gl, q & 1, h, F->lane); if (q & 1) fitem = item_of(q); ++q;
;             if (fitem >= 0) { __syncthreads(); flush(); __syncthreads(); }
.LBB0_710:
	s_ashr_i32 s0, s40, 1
	s_mul_i32 s0, s0, s55
	s_add_i32 s0, s0, s3
	s_cmpk_lt_i32 s0, 0x4000
	s_cselect_b64 vcc, -1, 0
	s_and_b64 s[14:15], vcc, exec
	s_cselect_b32 s1, 5, 4
	s_lshr_b32 s1, s0, s1
	s_lshl_b32 s1, s1, 9
	s_and_b32 s1, s1, 0x1e00
	s_lshl_b32 s4, s40, 7
	s_add_i32 s1, s11, s1
	s_and_b32 s4, s4, 0x80
	s_add_i32 s1, s1, s4
	v_add_u32_e32 v130, s1, v133
	ds_read_b128 v[152:155], v130 offset:49152
	ds_read_b128 v[156:159], v130 offset:49168
	ds_read_b128 v[160:163], v130 offset:49184
	ds_read_b128 v[164:167], v130 offset:49200
	s_lshl_b32 s1, s40, 1
	s_waitcnt lgkmcnt(3)
	v_cndmask_b32_e32 v130, v151, v152, vcc
	v_cndmask_b32_e32 v136, v151, v153, vcc
	v_cndmask_b32_e32 v137, v151, v154, vcc
	s_waitcnt lgkmcnt(2)
	v_cndmask_b32_e32 v169, v151, v156, vcc
	v_cndmask_b32_e32 v170, v151, v157, vcc
	v_mul_f32_e32 v153, v70, v130
	v_mul_f32_e32 v154, v66, v136
	v_cvt_pk_fp8_f32 v152, v153, v154
	v_mul_f32_e32 v154, v86, v169
	v_mul_f32_e32 v157, v82, v170
	v_cvt_pk_fp8_f32 v153, v154, v157
	v_cndmask_b32_e32 v168, v151, v155, vcc
	v_cndmask_b32_e32 v171, v151, v158, vcc
	v_cndmask_b32_e32 v172, v151, v159, vcc
	v_mul_f32_e32 v155, v78, v137
	v_mul_f32_e32 v156, v74, v168
	s_waitcnt lgkmcnt(1)
	v_cndmask_b32_e32 v173, v151, v160, vcc
	v_cndmask_b32_e32 v174, v151, v161, vcc
	v_cvt_pk_fp8_f32 v152, v155, v156 op_sel:[0,0,1]
	v_mul_f32_e32 v154, v94, v171
	v_mul_f32_e32 v155, v90, v172
	s_waitcnt lgkmcnt(0)
	v_cndmask_b32_e32 v164, v151, v164, vcc
	v_cndmask_b32_e32 v165, v151, v165, vcc
	v_cvt_pk_fp8_f32 v153, v154, v155 op_sel:[0,0,1]
	v_mul_f32_e32 v155, v98, v173
	v_mul_f32_e32 v156, v102, v174
	v_cvt_pk_fp8_f32 v154, v155, v156
	v_mul_f32_e32 v156, v114, v164
	v_mul_f32_e32 v159, v118, v165
	v_cvt_pk_fp8_f32 v155, v156, v159
	v_cndmask_b32_e32 v175, v151, v162, vcc
	v_cndmask_b32_e32 v176, v151, v163, vcc
	v_cndmask_b32_e32 v166, v151, v166, vcc
	v_cndmask_b32_e32 v167, v151, v167, vcc
	v_mul_f32_e32 v157, v106, v175
	v_mul_f32_e32 v158, v110, v176
	v_cvt_pk_fp8_f32 v154, v157, v158 op_sel:[0,0,1]
	v_mul_f32_e32 v156, v122, v166
	v_mul_f32_e32 v157, v126, v167
	v_cvt_pk_fp8_f32 v155, v156, v157 op_sel:[0,0,1]
	v_mul_f32_e32 v157, v71, v130
	v_mul_f32_e32 v158, v67, v136
	v_cvt_pk_fp8_f32 v156, v157, v158
	v_mul_f32_e32 v158, v87, v169
	v_mul_f32_e32 v161, v83, v170
	v_cvt_pk_fp8_f32 v157, v158, v161
	v_mul_f32_e32 v159, v79, v137
	v_mul_f32_e32 v160, v75, v168
	v_cvt_pk_fp8_f32 v156, v159, v160 op_sel:[0,0,1]
	v_mul_f32_e32 v158, v95, v171
	v_mul_f32_e32 v159, v91, v172
	v_cvt_pk_fp8_f32 v157, v158, v159 op_sel:[0,0,1]
	v_mul_f32_e32 v159, v99, v173
	v_mul_f32_e32 v160, v103, v174
	v_cvt_pk_fp8_f32 v158, v159, v160
	v_mul_f32_e32 v160, v115, v164
	v_mul_f32_e32 v163, v119, v165
	v_cvt_pk_fp8_f32 v159, v160, v163
	v_mul_f32_e32 v161, v107, v175
	v_mul_f32_e32 v162, v111, v176
	v_cvt_pk_fp8_f32 v158, v161, v162 op_sel:[0,0,1]
	v_mul_f32_e32 v160, v123, v166
	v_mul_f32_e32 v161, v127, v167
	v_cvt_pk_fp8_f32 v159, v160, v161 op_sel:[0,0,1]
	v_mul_f32_e32 v161, v72, v130
	v_mul_f32_e32 v162, v68, v136
	v_cvt_pk_fp8_f32 v160, v161, v162
	v_mul_f32_e32 v162, v88, v169
	v_mul_f32_e32 v179, v84, v170
	v_cvt_pk_fp8_f32 v161, v162, v179
	v_mul_f32_e32 v163, v80, v137
	v_mul_f32_e32 v178, v76, v168
	v_cvt_pk_fp8_f32 v160, v163, v178 op_sel:[0,0,1]
	v_mul_f32_e32 v162, v96, v171
	v_mul_f32_e32 v163, v92, v172
	v_cvt_pk_fp8_f32 v161, v162, v163 op_sel:[0,0,1]
	v_mul_f32_e32 v163, v100, v173
	v_mul_f32_e32 v178, v104, v174
	v_cvt_pk_fp8_f32 v162, v163, v178
	v_mul_f32_e32 v178, v116, v164
	v_mul_f32_e32 v181, v120, v165
	v_cvt_pk_fp8_f32 v163, v178, v181
	v_mul_f32_e32 v179, v108, v175
	v_mul_f32_e32 v180, v112, v176
	s_and_b32 s1, s1, 2
	v_cvt_pk_fp8_f32 v162, v179, v180 op_sel:[0,0,1]
	v_mul_f32_e32 v178, v124, v166
	v_mul_f32_e32 v179, v128, v167
	v_bitop3_b32 v177, s1, v139, v141 bitop3:0x36
	v_cvt_pk_fp8_f32 v163, v178, v179 op_sel:[0,0,1]
	v_lshl_add_u32 v177, v177, 4, v138
	ds_write_b128 v177, v[152:155]
	ds_write_b128 v177, v[156:159] offset:128
	ds_write_b128 v177, v[160:163] offset:256
	v_mul_f32_e32 v130, v73, v130
	v_mul_f32_e32 v136, v69, v136
	v_cvt_pk_fp8_f32 v152, v130, v136
	v_mul_f32_e32 v130, v89, v169
	v_mul_f32_e32 v136, v85, v170
	v_cvt_pk_fp8_f32 v153, v130, v136
	v_mul_f32_e32 v137, v81, v137
	v_mul_f32_e32 v154, v77, v168
	v_mul_f32_e32 v130, v97, v171
	v_mul_f32_e32 v136, v93, v172
	v_cvt_pk_fp8_f32 v152, v137, v154 op_sel:[0,0,1]
	v_cvt_pk_fp8_f32 v153, v130, v136 op_sel:[0,0,1]
	v_mul_f32_e32 v130, v101, v173
	v_mul_f32_e32 v136, v105, v174
	v_cvt_pk_fp8_f32 v154, v130, v136
	v_mul_f32_e32 v130, v117, v164
	v_mul_f32_e32 v136, v121, v165
	v_cvt_pk_fp8_f32 v155, v130, v136
	v_mul_f32_e32 v137, v109, v175
	v_mul_f32_e32 v156, v113, v176
	v_mul_f32_e32 v130, v125, v166
	v_mul_f32_e32 v136, v129, v167
	v_cvt_pk_fp8_f32 v154, v137, v156 op_sel:[0,0,1]
	v_cvt_pk_fp8_f32 v155, v130, v136 op_sel:[0,0,1]
	s_and_b64 s[14:15], s[6:7], exec
	s_cselect_b32 s61, s0, s42
	s_cmp_lt_i32 s61, 0
	ds_write_b128 v177, v[152:155] offset:384
	s_cbranch_scc1 .LBB0_688
	s_cmpk_lt_u32 s61, 0x4000
	s_cselect_b64 s[0:1], -1, 0
	s_cmpk_gt_u32 s61, 0x3fff
	s_mov_b64 s[36:37], -1
	s_waitcnt lgkmcnt(0)
	s_barrier
	s_cbranch_scc0 .LBB0_713
	s_add_i32 s4, s61, 0xffffc000
	s_lshr_b32 s4, s4, 8
	s_lshr_b32 s40, s61, 4
	s_and_b32 s41, s61, 15
	s_lshl_b64 s[14:15], s[4:5], 22
	s_add_u32 s14, s34, s14
	s_addc_u32 s15, s35, s15
	s_mov_b64 s[36:37], 0

; #define LAS __attribute__((address_space(3)))
; __device__ __forceinline__ unsigned pk4_fp8(float a, float b, float c, float d) { int w = __builtin_amdgcn_cvt_pk_fp8_f32(a, b, 0, false); w = __builtin_amdgcn_cvt_pk_fp8_f32(c, d, w, true); return (unsigned)w; }
;     __device__ __forceinline__ CvtDesc desc(int qq) const { return cvt_desc(*F, item_of(qq), qq & 1, h); }
;     __device__ __forceinline__ void flush() { if (fitem >= 0) { cvt_flush(cvt_desc(*F, fitem, 0, h), img, h, F->lane); fitem = -1; } }
; __device__ __forceinline__ void cvt_to_lds(const CvtBuf& b, const CvtDesc& d, LAS unsigned char* img, const LAS float* gl, int sub2, int h, int lane) {
;     const int hh = lane >> 5, l5 = lane & 31;
;     float gs[16];
;     const bool use_g = d.map == 2;
; #pragma unroll
;     for (int q = 0; q < 4; ++q) { const f32x4 gv = *(const LAS f32x4*)(gl + d.k0 + 16 * hh + 4 * q);
; #pragma unroll
;         for (int j = 0; j < 4; ++j) gs[4 * q + j] = use_g ? gv[j] : WSCALE; }
;     const int c8 = 4 * h + 2 * sub2 + hh;
; #pragma unroll
;     for (int j = 0; j < 4; ++j) { u32x4 o;
; #pragma unroll
;         for (int q = 0; q < 4; ++q) { const int i = 4 * q; o[q] = pk4_fp8(b.v[i][j] * gs[i], b.v[i + 1][j] * gs[i + 1], b.v[i + 2][j] * gs[i + 2], b.v[i + 3][j] * gs[i + 3]); }
;         *(LAS u32x4*)(img + (4 * l5 + j) * 128 + 16 * (c8 ^ (l5 & 7))) = o; }
; }
;     __device__ __forceinline__ void drain() {
;     ...
;         while (q < nq) {
;             if (q + 1 < nq) cvt_load(b2, desc(q + 1), F->lane);
;             cvt_to_lds(buf, desc(q), img, gl, q & 1, h, F->lane); if (q & 1) fitem = item_of(q); ++q;
;             if (fitem >= 0) { __syncthreads(); flush(); __syncthreads(); }
;             if (q >= nq) break;
;             if (q + 1 < nq) cvt_load(buf, desc(q + 1), F->lane);
;             cvt_to_lds(b2, desc(q), img, gl, q & 1, h, F->lane); if (q & 1) fitem = item_of(q); ++q;
;             if (fitem >= 0) { __syncthreads(); flush(); __syncthreads(); }
.LBB0_910:
	s_cmpk_lt_i32 s44, 0x4000
	s_cselect_b64 s[0:1], -1, 0
	s_and_b64 s[12:13], s[0:1], exec
	s_cselect_b32 s4, 5, 4
	s_lshr_b32 s4, s44, s4
	s_lshl_b32 s4, s4, 9
	s_and_b32 s4, s4, 0x1e00
	v_add_u32_e32 v136, s4, v140
	ds_read_b128 v[154:157], v136 offset:49152
	ds_read_b128 v[158:161], v136 offset:49168
	ds_read_b128 v[162:165], v136 offset:49184
	ds_read_b128 v[166:169], v136 offset:49200
	s_andn2_b64 vcc, exec, s[6:7]
	s_waitcnt lgkmcnt(3)
	v_cndmask_b32_e64 v132, v152, v154, s[0:1]
	v_cndmask_b32_e64 v137, v152, v155, s[0:1]
	v_cndmask_b32_e64 v153, v152, v156, s[0:1]
	s_waitcnt lgkmcnt(2)
	v_cndmask_b32_e64 v171, v152, v158, s[0:1]
	v_cndmask_b32_e64 v172, v152, v159, s[0:1]
	s_waitcnt vmcnt(31)
	v_mul_f32_e32 v155, v2, v132
	s_waitcnt vmcnt(30)
	v_mul_f32_e32 v156, v6, v137
	v_cvt_pk_fp8_f32 v154, v155, v156
	s_waitcnt vmcnt(27)
	v_mul_f32_e32 v156, v18, v171
	s_waitcnt vmcnt(26)
	v_mul_f32_e32 v159, v22, v172
	v_cvt_pk_fp8_f32 v155, v156, v159
	v_cndmask_b32_e64 v170, v152, v157, s[0:1]
	v_cndmask_b32_e64 v173, v152, v160, s[0:1]
	v_cndmask_b32_e64 v174, v152, v161, s[0:1]
	v_mul_f32_e32 v157, v10, v153
	v_mul_f32_e32 v158, v14, v170
	s_waitcnt lgkmcnt(1)
	v_cndmask_b32_e64 v175, v152, v162, s[0:1]
	v_cndmask_b32_e64 v176, v152, v163, s[0:1]
	v_cvt_pk_fp8_f32 v154, v157, v158 op_sel:[0,0,1]
	s_waitcnt vmcnt(25)
	v_mul_f32_e32 v156, v26, v173
	s_waitcnt vmcnt(24)
	v_mul_f32_e32 v157, v30, v174
	s_waitcnt lgkmcnt(0)
	v_cndmask_b32_e64 v179, v152, v166, s[0:1]
	v_cndmask_b32_e64 v180, v152, v167, s[0:1]
	v_cvt_pk_fp8_f32 v155, v156, v157 op_sel:[0,0,1]
	s_waitcnt vmcnt(23)
	v_mul_f32_e32 v157, v34, v175
	s_waitcnt vmcnt(22)
	v_mul_f32_e32 v158, v38, v176
	v_cvt_pk_fp8_f32 v156, v157, v158
	s_waitcnt vmcnt(19)
	v_mul_f32_e32 v158, v50, v179
	s_waitcnt vmcnt(18)
	v_mul_f32_e32 v161, v54, v180
	v_cvt_pk_fp8_f32 v157, v158, v161
	v_cndmask_b32_e64 v177, v152, v164, s[0:1]
	v_cndmask_b32_e64 v178, v152, v165, s[0:1]
	v_cndmask_b32_e64 v181, v152, v168, s[0:1]
	v_cndmask_b32_e64 v182, v152, v169, s[0:1]
	v_mul_f32_e32 v159, v42, v177
	v_mul_f32_e32 v160, v46, v178
	v_cvt_pk_fp8_f32 v156, v159, v160 op_sel:[0,0,1]
	s_waitcnt vmcnt(17)
	v_mul_f32_e32 v158, v58, v181
	s_waitcnt vmcnt(16)
	v_mul_f32_e32 v159, v62, v182
	v_cvt_pk_fp8_f32 v157, v158, v159 op_sel:[0,0,1]
	v_mul_f32_e32 v159, v3, v132
	v_mul_f32_e32 v160, v7, v137
	v_cvt_pk_fp8_f32 v158, v159, v160
	v_mul_f32_e32 v160, v19, v171
	v_mul_f32_e32 v163, v23, v172
	v_cvt_pk_fp8_f32 v159, v160, v163
	v_mul_f32_e32 v161, v11, v153
	v_mul_f32_e32 v162, v15, v170
	v_cvt_pk_fp8_f32 v158, v161, v162 op_sel:[0,0,1]
	v_mul_f32_e32 v160, v27, v173
	v_mul_f32_e32 v161, v31, v174
	v_cvt_pk_fp8_f32 v159, v160, v161 op_sel:[0,0,1]
	v_mul_f32_e32 v161, v35, v175
	v_mul_f32_e32 v162, v39, v176
	v_cvt_pk_fp8_f32 v160, v161, v162
	v_mul_f32_e32 v162, v51, v179
	v_mul_f32_e32 v165, v55, v180
	v_cvt_pk_fp8_f32 v161, v162, v165
	v_mul_f32_e32 v163, v43, v177
	v_mul_f32_e32 v164, v47, v178
	v_cvt_pk_fp8_f32 v160, v163, v164 op_sel:[0,0,1]
	v_mul_f32_e32 v162, v59, v181
	v_mul_f32_e32 v163, v63, v182
	v_cvt_pk_fp8_f32 v161, v162, v163 op_sel:[0,0,1]
	v_mul_f32_e32 v163, v4, v132
	v_mul_f32_e32 v164, v8, v137
	v_cvt_pk_fp8_f32 v162, v163, v164
	v_mul_f32_e32 v164, v20, v171
	v_mul_f32_e32 v167, v24, v172
	v_cvt_pk_fp8_f32 v163, v164, v167
	v_mul_f32_e32 v165, v12, v153
	v_mul_f32_e32 v166, v16, v170
	v_cvt_pk_fp8_f32 v162, v165, v166 op_sel:[0,0,1]
	v_mul_f32_e32 v164, v28, v173
	v_mul_f32_e32 v165, v32, v174
	v_cvt_pk_fp8_f32 v163, v164, v165 op_sel:[0,0,1]
	v_mul_f32_e32 v165, v36, v175
	v_mul_f32_e32 v166, v40, v176
	v_cvt_pk_fp8_f32 v164, v165, v166
	v_mul_f32_e32 v166, v52, v179
	v_mul_f32_e32 v169, v56, v180
	v_cvt_pk_fp8_f32 v165, v166, v169
	v_mul_f32_e32 v167, v44, v177
	v_mul_f32_e32 v168, v48, v178
	v_cvt_pk_fp8_f32 v164, v167, v168 op_sel:[0,0,1]
	v_mul_f32_e32 v166, v60, v181
	v_mul_f32_e32 v167, v64, v182
	v_cvt_pk_fp8_f32 v165, v166, v167 op_sel:[0,0,1]
	v_mul_f32_e32 v132, v5, v132
	v_mul_f32_e32 v137, v9, v137
	v_cvt_pk_fp8_f32 v166, v132, v137
	v_mul_f32_e32 v132, v21, v171
	v_mul_f32_e32 v137, v25, v172
	v_cvt_pk_fp8_f32 v167, v132, v137
	v_mul_f32_e32 v153, v13, v153
	v_mul_f32_e32 v168, v17, v170
	v_mul_f32_e32 v132, v29, v173
	v_mul_f32_e32 v137, v33, v174
	v_cvt_pk_fp8_f32 v166, v153, v168 op_sel:[0,0,1]
	v_cvt_pk_fp8_f32 v167, v132, v137 op_sel:[0,0,1]
	v_mul_f32_e32 v132, v37, v175
	v_mul_f32_e32 v137, v41, v176
	v_cvt_pk_fp8_f32 v168, v132, v137
	v_mul_f32_e32 v132, v53, v179
	v_mul_f32_e32 v137, v57, v180
	v_cvt_pk_fp8_f32 v169, v132, v137
	v_mul_f32_e32 v153, v45, v177
	v_mul_f32_e32 v170, v49, v178
	v_mul_f32_e32 v132, v61, v181
	v_mul_f32_e32 v137, v65, v182
	v_cvt_pk_fp8_f32 v168, v153, v170 op_sel:[0,0,1]
	v_cvt_pk_fp8_f32 v169, v132, v137 op_sel:[0,0,1]
	s_mov_b64 s[6:7], -1
	ds_write_b128 v150, v[154:157]
	ds_write_b128 v150, v[158:161] offset:128
	ds_write_b128 v150, v[162:165] offset:256
	ds_write_b128 v150, v[166:169] offset:384
	s_cbranch_vccnz .LBB0_903
	s_add_i32 s43, s43, 2
	s_cmp_ge_i32 s43, s34
	s_cselect_b64 s[6:7], -1, 0
	s_and_b64 vcc, exec, s[6:7]
	s_cbranch_vccz .Ldr4_goB
	s_waitcnt vmcnt(0)
	s_branch .LBB0_917

; #define LAS __attribute__((address_space(3)))
; __device__ __forceinline__ unsigned pk4_fp8(float a, float b, float c, float d) { int w = __builtin_amdgcn_cvt_pk_fp8_f32(a, b, 0, false); w = __builtin_amdgcn_cvt_pk_fp8_f32(c, d, w, true); return (unsigned)w; }
;     __device__ __forceinline__ CvtDesc desc(int qq) const { return cvt_desc(*F, item_of(qq), qq & 1, h); }
;     __device__ __forceinline__ void flush() { if (fitem >= 0) { cvt_flush(cvt_desc(*F, fitem, 0, h), img, h, F->lane); fitem = -1; } }
; __device__ __forceinline__ void cvt_to_lds(const CvtBuf& b, const CvtDesc& d, LAS unsigned char* img, const LAS float* gl, int sub2, int h, int lane) {
;     const int hh = lane >> 5, l5 = lane & 31;
;     float gs[16];
;     const bool use_g = d.map == 2;
; #pragma unroll
;     for (int q = 0; q < 4; ++q) { const f32x4 gv = *(const LAS f32x4*)(gl + d.k0 + 16 * hh + 4 * q);
; #pragma unroll
;         for (int j = 0; j < 4; ++j) gs[4 * q + j] = use_g ? gv[j] : WSCALE; }
;     const int c8 = 4 * h + 2 * sub2 + hh;
; #pragma unroll
;     for (int j = 0; j < 4; ++j) { u32x4 o;
; #pragma unroll
;         for (int q = 0; q < 4; ++q) { const int i = 4 * q; o[q] = pk4_fp8(b.v[i][j] * gs[i], b.v[i + 1][j] * gs[i + 1], b.v[i + 2][j] * gs[i + 2], b.v[i + 3][j] * gs[i + 3]); }
;         *(LAS u32x4*)(img + (4 * l5 + j) * 128 + 16 * (c8 ^ (l5 & 7))) = o; }
; }
;     __device__ __forceinline__ void drain() {
;     ...
;             cvt_to_lds(buf, desc(q), img, gl, q & 1, h, F->lane); if (q & 1) fitem = item_of(q); ++q;
;             if (fitem >= 0) { __syncthreads(); flush(); __syncthreads(); }
;             if (q >= nq) break;
;             if (q + 1 < nq) cvt_load(buf, desc(q + 1), F->lane);
;             cvt_to_lds(b2, desc(q), img, gl, q & 1, h, F->lane); if (q & 1) fitem = item_of(q); ++q;
;             if (fitem >= 0) { __syncthreads(); flush(); __syncthreads(); }
.LBB0_917:
	ds_read_b128 v[154:157], v136 offset:49280
	ds_read_b128 v[158:161], v136 offset:49296
	ds_read_b128 v[162:165], v136 offset:49312
	ds_read_b128 v[166:169], v136 offset:49328
	s_cmp_lt_i32 s44, 0
	s_waitcnt lgkmcnt(3)
	v_cndmask_b32_e64 v132, v152, v154, s[0:1]
	v_cndmask_b32_e64 v136, v152, v155, s[0:1]
	v_cndmask_b32_e64 v137, v152, v156, s[0:1]
	s_waitcnt lgkmcnt(2)
	v_cndmask_b32_e64 v170, v152, v158, s[0:1]
	v_cndmask_b32_e64 v171, v152, v159, s[0:1]
	v_mul_f32_e32 v155, v70, v132
	v_mul_f32_e32 v156, v66, v136
	v_cvt_pk_fp8_f32 v154, v155, v156
	v_mul_f32_e32 v156, v86, v170
	v_mul_f32_e32 v159, v82, v171
	v_cvt_pk_fp8_f32 v155, v156, v159
	v_cndmask_b32_e64 v153, v152, v157, s[0:1]
	v_cndmask_b32_e64 v172, v152, v160, s[0:1]
	v_cndmask_b32_e64 v173, v152, v161, s[0:1]
	v_mul_f32_e32 v157, v78, v137
	v_mul_f32_e32 v158, v74, v153
	s_waitcnt lgkmcnt(1)
	v_cndmask_b32_e64 v174, v152, v162, s[0:1]
	v_cndmask_b32_e64 v175, v152, v163, s[0:1]
	v_cvt_pk_fp8_f32 v154, v157, v158 op_sel:[0,0,1]
	v_mul_f32_e32 v156, v94, v172
	v_mul_f32_e32 v157, v90, v173
	s_waitcnt lgkmcnt(0)
	v_cndmask_b32_e64 v166, v152, v166, s[0:1]
	v_cndmask_b32_e64 v167, v152, v167, s[0:1]
	v_cvt_pk_fp8_f32 v155, v156, v157 op_sel:[0,0,1]
	v_mul_f32_e32 v157, v98, v174
	v_mul_f32_e32 v158, v102, v175
	v_cvt_pk_fp8_f32 v156, v157, v158
	v_mul_f32_e32 v158, v114, v166
	v_mul_f32_e32 v161, v118, v167
	v_cvt_pk_fp8_f32 v157, v158, v161
	v_cndmask_b32_e64 v164, v152, v164, s[0:1]
	v_cndmask_b32_e64 v165, v152, v165, s[0:1]
	v_cndmask_b32_e64 v168, v152, v168, s[0:1]
	v_cndmask_b32_e64 v169, v152, v169, s[0:1]
	v_mul_f32_e32 v159, v106, v164
	v_mul_f32_e32 v160, v110, v165
	v_cvt_pk_fp8_f32 v156, v159, v160 op_sel:[0,0,1]
	v_mul_f32_e32 v158, v122, v168
	v_mul_f32_e32 v159, v126, v169
	v_cvt_pk_fp8_f32 v157, v158, v159 op_sel:[0,0,1]
	v_mul_f32_e32 v159, v83, v171
	v_mul_f32_e32 v158, v75, v153
	v_mul_f32_e32 v161, v119, v167
	ds_write_b128 v151, v[154:157]
	v_mul_f32_e32 v155, v71, v132
	v_mul_f32_e32 v156, v67, v136
	v_cvt_pk_fp8_f32 v154, v155, v156
	v_mul_f32_e32 v156, v87, v170
	v_cvt_pk_fp8_f32 v155, v156, v159
	v_mul_f32_e32 v157, v79, v137
	v_cvt_pk_fp8_f32 v154, v157, v158 op_sel:[0,0,1]
	v_mul_f32_e32 v156, v95, v172
	v_mul_f32_e32 v157, v91, v173
	v_cvt_pk_fp8_f32 v155, v156, v157 op_sel:[0,0,1]
	v_mul_f32_e32 v157, v99, v174
	v_mul_f32_e32 v158, v103, v175
	v_cvt_pk_fp8_f32 v156, v157, v158
	v_mul_f32_e32 v158, v115, v166
	v_cvt_pk_fp8_f32 v157, v158, v161
	v_mul_f32_e32 v159, v107, v164
	v_mul_f32_e32 v160, v111, v165
	v_cvt_pk_fp8_f32 v156, v159, v160 op_sel:[0,0,1]
	v_mul_f32_e32 v158, v123, v168
	v_mul_f32_e32 v159, v127, v169
	v_cvt_pk_fp8_f32 v157, v158, v159 op_sel:[0,0,1]
	v_mul_f32_e32 v159, v72, v132
	v_mul_f32_e32 v160, v68, v136
	v_cvt_pk_fp8_f32 v158, v159, v160
	v_mul_f32_e32 v160, v88, v170
	v_mul_f32_e32 v163, v84, v171
	v_cvt_pk_fp8_f32 v159, v160, v163
	v_mul_f32_e32 v161, v80, v137
	v_mul_f32_e32 v162, v76, v153
	v_cvt_pk_fp8_f32 v158, v161, v162 op_sel:[0,0,1]
	v_mul_f32_e32 v160, v96, v172
	v_mul_f32_e32 v161, v92, v173
	v_cvt_pk_fp8_f32 v159, v160, v161 op_sel:[0,0,1]
	v_mul_f32_e32 v161, v100, v174
	v_mul_f32_e32 v162, v104, v175
	v_cvt_pk_fp8_f32 v160, v161, v162
	v_mul_f32_e32 v162, v116, v166
	v_mul_f32_e32 v177, v120, v167
	v_cvt_pk_fp8_f32 v161, v162, v177
	v_mul_f32_e32 v163, v108, v164
	v_mul_f32_e32 v176, v112, v165
	v_cvt_pk_fp8_f32 v160, v163, v176 op_sel:[0,0,1]
	v_mul_f32_e32 v162, v124, v168
	v_mul_f32_e32 v163, v128, v169
	v_cvt_pk_fp8_f32 v161, v162, v163 op_sel:[0,0,1]
	v_mul_f32_e32 v132, v73, v132
	v_mul_f32_e32 v136, v69, v136
	v_cvt_pk_fp8_f32 v162, v132, v136
	v_mul_f32_e32 v132, v89, v170
	v_mul_f32_e32 v136, v85, v171
	v_cvt_pk_fp8_f32 v163, v132, v136
	v_mul_f32_e32 v137, v81, v137
	v_mul_f32_e32 v153, v77, v153
	v_mul_f32_e32 v132, v97, v172
	v_mul_f32_e32 v136, v93, v173
	v_cvt_pk_fp8_f32 v162, v137, v153 op_sel:[0,0,1]
	v_cvt_pk_fp8_f32 v163, v132, v136 op_sel:[0,0,1]
	v_mul_f32_e32 v132, v101, v174
	v_mul_f32_e32 v136, v105, v175
	v_mul_f32_e32 v137, v109, v164
	v_mul_f32_e32 v153, v113, v165
	v_cvt_pk_fp8_f32 v164, v132, v136
	v_mul_f32_e32 v132, v117, v166
	v_mul_f32_e32 v136, v121, v167
	v_cvt_pk_fp8_f32 v165, v132, v136
	v_mul_f32_e32 v132, v125, v168
	v_mul_f32_e32 v136, v129, v169
	v_cvt_pk_fp8_f32 v164, v137, v153 op_sel:[0,0,1]
	v_cvt_pk_fp8_f32 v165, v132, v136 op_sel:[0,0,1]
	ds_write_b128 v151, v[154:157] offset:128
	ds_write_b128 v151, v[158:161] offset:256
	ds_write_b128 v151, v[162:165] offset:384
	s_cbranch_scc1 .LBB0_903
	s_cmpk_lt_u32 s44, 0x4000
	s_cselect_b64 s[0:1], -1, 0
	s_cmpk_gt_u32 s44, 0x3fff
	s_mov_b64 s[14:15], -1
	s_waitcnt lgkmcnt(0)
	s_barrier
	s_cbranch_scc0 .LBB0_920
	s_add_i32 s4, s44, 0xffffc000
	s_lshr_b32 s4, s4, 8
	s_lshr_b32 s36, s44, 4
	s_lshl_b64 s[12:13], s[4:5], 22
	s_add_u32 s12, s39, s12
	s_addc_u32 s13, s40, s13
	s_mov_b64 s[14:15], 0

; __device__ __forceinline__ unsigned cvt_pk_bf16(float lo, float hi) { unsigned r; asm volatile("v_cvt_pk_bf16_f32 %0, %1, %2" : "=v"(r) : "v"(lo), "v"(hi)); return r; }
; __device__ __forceinline__ unsigned pk4_fp8(float a, float b, float c, float d) { int w = __builtin_amdgcn_cvt_pk_fp8_f32(a, b, 0, false); w = __builtin_amdgcn_cvt_pk_fp8_f32(c, d, w, true); return (unsigned)w; }
;     __device__ __forceinline__ void operator()(AccRef acc, const Unit& u, int wr, int wc, int fr, int fq) const {
;     ...
;             for (int m = 0; m < 4; ++m) { const int row = u.pm * 256 + ai * 128 + wr * 64 + m * 16 + fr; const size_t off = (size_t)row * DM + col0; float ss = 0.f;
; #pragma unroll
;                 for (int bj = 0; bj < 2; ++bj) { const size_t o2 = off + bj * 128; const f32x4 v0 = rv[m][bj][0] + acc[ai][bj][m][0] * ascale, v1 = rv[m][bj][1] + acc[ai][bj][m][1] * ascale;
;                     if (outf) { *(f32x4*)(outf + o2) = v0; *(f32x4*)(outf + o2 + 4) = v1; }
;                     if (outb) { u32x4 w; w.x = cvt_pk_bf16(v0[0], v0[1]); w.y = cvt_pk_bf16(v0[2], v0[3]); w.z = cvt_pk_bf16(v1[0], v1[1]); w.w = cvt_pk_bf16(v1[2], v1[3]); *(u32x4*)(outb + o2) = w; }
;                     if (out8) { u32x2 w8; w8.x = pk4_fp8(v0[0], v0[1], v0[2], v0[3]); w8.y = pk4_fp8(v1[0], v1[1], v1[2], v1[3]); *(u32x2*)((unsigned char*)out8 + o2) = w8; }
;                     ss += (v0[0] * v0[0] + v0[1] * v0[1]) + (v0[2] * v0[2] + v0[3] * v0[3]) + (v1[0] * v1[0] + v1[1] * v1[1]) + (v1[2] * v1[2] + v1[3] * v1[3]); }
;                 ss += __shfl_xor(ss, 16); ss += __shfl_xor(ss, 32);
;                 if (fq == 0) atomicAdd(ssq + row, ss); }
.LBB0_1030:
	s_or_b64 exec, exec, s[48:49]
	v_lshlrev_b32_e32 v116, 16, v150
	s_waitcnt lgkmcnt(0)
	v_and_b32_e32 v117, 0xffff0000, v150
	v_lshlrev_b32_e32 v118, 16, v151
	v_and_b32_e32 v119, 0xffff0000, v151
	v_lshlrev_b32_e32 v120, 16, v152
	v_and_b32_e32 v121, 0xffff0000, v152
	v_pk_add_f32 v[112:113], v[112:113], v[118:119]
	v_pk_add_f32 v[110:111], v[110:111], v[116:117]
	v_pk_add_f32 v[118:119], v[106:107], v[120:121]
	v_cvt_pk_fp8_f32 v120, v110, v111
	v_cvt_pk_fp8_f32 v121, v118, v119
	v_lshlrev_b32_e32 v122, 16, v153
	v_and_b32_e32 v123, 0xffff0000, v153
	v_pk_add_f32 v[116:117], v[108:109], v[122:123]
	v_cvt_pk_fp8_f32 v120, v112, v113 op_sel:[0,0,1]
	v_cvt_pk_fp8_f32 v121, v116, v117 op_sel:[0,0,1]
	v_cvt_pk_bf16_f32 v106, v110, v111
	v_cvt_pk_bf16_f32 v107, v112, v113
	v_lshl_add_u64 v[122:123], v[174:175], 1, s[14:15]
	v_cvt_pk_bf16_f32 v108, v118, v119
	v_cvt_pk_bf16_f32 v109, v116, v117
	global_store_dwordx4 v[122:123], v[106:109], off
	v_lshlrev_b32_e32 v124, 16, v146
	v_and_b32_e32 v125, 0xffff0000, v146
	v_lshl_add_u64 v[106:107], s[36:37], 0, v[174:175]
	global_store_dwordx2 v[106:107], v[120:121], off
	v_mul_f32_e32 v106, v111, v111
	v_mul_f32_e32 v107, v113, v113
	v_fmac_f32_e32 v106, v110, v110
	v_fmac_f32_e32 v107, v112, v112
	v_add_f32_e32 v106, v106, v107
	v_mul_f32_e32 v107, v118, v118
	v_fmac_f32_e32 v107, v119, v119
	v_add_f32_e32 v106, v107, v106
	v_mul_f32_e32 v107, v116, v116
	v_lshlrev_b32_e32 v126, 16, v147
	v_and_b32_e32 v127, 0xffff0000, v147
	v_lshlrev_b32_e32 v146, 16, v149
	v_and_b32_e32 v147, 0xffff0000, v149
	v_fmac_f32_e32 v107, v117, v117
	v_pk_add_f32 v[102:103], v[102:103], v[124:125]
	v_add_f32_e32 v110, v107, v106
	v_pk_add_f32 v[104:105], v[104:105], v[126:127]
	v_pk_add_f32 v[106:107], v[100:101], v[146:147]
	v_cvt_pk_bf16_f32 v100, v102, v103
	v_cvt_pk_fp8_f32 v108, v102, v103
	v_mul_f32_e32 v103, v103, v103
	v_lshlrev_b32_e32 v128, 16, v148
	v_and_b32_e32 v129, 0xffff0000, v148
	v_fmac_f32_e32 v103, v102, v102
	v_mul_f32_e32 v102, v105, v105
	v_pk_add_f32 v[98:99], v[98:99], v[128:129]
	v_fmac_f32_e32 v102, v104, v104
	v_add_f32_e32 v102, v103, v102
	v_mul_f32_e32 v103, v98, v98
	v_fmac_f32_e32 v103, v99, v99
	v_add_f32_e32 v102, v103, v102
	v_mul_f32_e32 v103, v106, v106
	v_fmac_f32_e32 v103, v107, v107
	v_add_f32_e32 v102, v103, v102
	v_add_f32_e32 v110, v110, v102
	ds_bpermute_b32 v111, v114, v110
	v_cvt_pk_fp8_f32 v109, v98, v99
	v_cvt_pk_bf16_f32 v101, v104, v105
	v_cvt_pk_bf16_f32 v102, v98, v99
	s_waitcnt lgkmcnt(0)
	v_add_f32_e32 v98, v110, v111
	ds_bpermute_b32 v99, v115, v98
	v_cvt_pk_fp8_f32 v108, v104, v105 op_sel:[0,0,1]
	v_cvt_pk_fp8_f32 v109, v106, v107 op_sel:[0,0,1]
	v_or_b32_e32 v174, 0x80, v174
	v_lshl_add_u64 v[104:105], v[174:175], 1, s[14:15]
	v_cvt_pk_bf16_f32 v103, v106, v107
	global_store_dwordx4 v[104:105], v[100:103], off
	s_nop 1
	v_lshl_add_u64 v[100:101], s[36:37], 0, v[174:175]
	global_store_dwordx2 v[100:101], v[108:109], off
	s_and_saveexec_b64 s[48:49], s[0:1]
	s_cbranch_execz .LBB0_1032
	v_lshl_add_u64 v[100:101], v[172:173], 2, s[18:19]
	s_waitcnt lgkmcnt(0)
	v_add_f32_e32 v98, v98, v99
	global_atomic_add_f32 v[100:101], v98, off
; __device__ __forceinline__ unsigned cvt_pk_bf16(float lo, float hi) { unsigned r; asm volatile("v_cvt_pk_bf16_f32 %0, %1, %2" : "=v"(r) : "v"(lo), "v"(hi)); return r; }
; __device__ __forceinline__ unsigned pk4_fp8(float a, float b, float c, float d) { int w = __builtin_amdgcn_cvt_pk_fp8_f32(a, b, 0, false); w = __builtin_amdgcn_cvt_pk_fp8_f32(c, d, w, true); return (unsigned)w; }
;     __device__ __forceinline__ void operator()(AccRef acc, const Unit& u, int wr, int wc, int fr, int fq) const {
;     ...
;             for (int m = 0; m < 4; ++m) { const int row = u.pm * 256 + ai * 128 + wr * 64 + m * 16 + fr; const size_t off = (size_t)row * DM + col0; float ss = 0.f;
; #pragma unroll
;                 for (int bj = 0; bj < 2; ++bj) { const size_t o2 = off + bj * 128; const f32x4 v0 = rv[m][bj][0] + acc[ai][bj][m][0] * ascale, v1 = rv[m][bj][1] + acc[ai][bj][m][1] * ascale;
;                     if (outf) { *(f32x4*)(outf + o2) = v0; *(f32x4*)(outf + o2 + 4) = v1; }
;                     if (outb) { u32x4 w; w.x = cvt_pk_bf16(v0[0], v0[1]); w.y = cvt_pk_bf16(v0[2], v0[3]); w.z = cvt_pk_bf16(v1[0], v1[1]); w.w = cvt_pk_bf16(v1[2], v1[3]); *(u32x4*)(outb + o2) = w; }
;                     if (out8) { u32x2 w8; w8.x = pk4_fp8(v0[0], v0[1], v0[2], v0[3]); w8.y = pk4_fp8(v1[0], v1[1], v1[2], v1[3]); *(u32x2*)((unsigned char*)out8 + o2) = w8; }
;                     ss += (v0[0] * v0[0] + v0[1] * v0[1]) + (v0[2] * v0[2] + v0[3] * v0[3]) + (v1[0] * v1[0] + v1[1] * v1[1]) + (v1[2] * v1[2] + v1[3] * v1[3]); }
;                 ss += __shfl_xor(ss, 16); ss += __shfl_xor(ss, 32);
;                 if (fq == 0) atomicAdd(ssq + row, ss); }
.LBB0_1032:
	s_or_b64 exec, exec, s[48:49]
	v_lshlrev_b32_e32 v98, 16, v142
	s_waitcnt lgkmcnt(0)
	v_and_b32_e32 v99, 0xffff0000, v142
	v_lshlrev_b32_e32 v100, 16, v143
	v_and_b32_e32 v101, 0xffff0000, v143
	v_lshlrev_b32_e32 v102, 16, v144
	v_and_b32_e32 v103, 0xffff0000, v144
	v_pk_add_f32 v[96:97], v[96:97], v[100:101]
	v_pk_add_f32 v[94:95], v[94:95], v[98:99]
	v_pk_add_f32 v[100:101], v[90:91], v[102:103]
	v_cvt_pk_fp8_f32 v102, v94, v95
	v_cvt_pk_fp8_f32 v103, v100, v101
	v_lshlrev_b32_e32 v104, 16, v145
	v_and_b32_e32 v105, 0xffff0000, v145
	v_pk_add_f32 v[98:99], v[92:93], v[104:105]
	v_cvt_pk_fp8_f32 v102, v96, v97 op_sel:[0,0,1]
	v_cvt_pk_fp8_f32 v103, v98, v99 op_sel:[0,0,1]
	v_cvt_pk_bf16_f32 v90, v94, v95
	v_cvt_pk_bf16_f32 v91, v96, v97
	v_lshl_add_u64 v[104:105], v[170:171], 1, s[14:15]
	v_cvt_pk_bf16_f32 v92, v100, v101
	v_cvt_pk_bf16_f32 v93, v98, v99
	global_store_dwordx4 v[104:105], v[90:93], off
	v_lshlrev_b32_e32 v106, 16, v138
	v_and_b32_e32 v107, 0xffff0000, v138
	v_lshl_add_u64 v[90:91], s[36:37], 0, v[170:171]
	global_store_dwordx2 v[90:91], v[102:103], off
	v_mul_f32_e32 v90, v95, v95
	v_mul_f32_e32 v91, v97, v97
	v_fmac_f32_e32 v90, v94, v94
	v_fmac_f32_e32 v91, v96, v96
	v_add_f32_e32 v90, v90, v91
	v_mul_f32_e32 v91, v100, v100
	v_fmac_f32_e32 v91, v101, v101
	v_add_f32_e32 v90, v91, v90
	v_mul_f32_e32 v91, v98, v98
	v_lshlrev_b32_e32 v108, 16, v139
	v_and_b32_e32 v109, 0xffff0000, v139
	v_lshlrev_b32_e32 v112, 16, v141
	v_and_b32_e32 v113, 0xffff0000, v141
	v_fmac_f32_e32 v91, v99, v99
	v_pk_add_f32 v[86:87], v[86:87], v[106:107]
	v_add_f32_e32 v94, v91, v90
	v_pk_add_f32 v[88:89], v[88:89], v[108:109]
	v_pk_add_f32 v[90:91], v[84:85], v[112:113]
	v_cvt_pk_bf16_f32 v84, v86, v87
	v_cvt_pk_fp8_f32 v92, v86, v87
	v_mul_f32_e32 v87, v87, v87
	v_lshlrev_b32_e32 v110, 16, v140
	v_and_b32_e32 v111, 0xffff0000, v140
	v_fmac_f32_e32 v87, v86, v86
	v_mul_f32_e32 v86, v89, v89
	v_pk_add_f32 v[82:83], v[82:83], v[110:111]
	v_fmac_f32_e32 v86, v88, v88
	v_add_f32_e32 v86, v87, v86
	v_mul_f32_e32 v87, v82, v82
	v_fmac_f32_e32 v87, v83, v83
	v_add_f32_e32 v86, v87, v86
	v_mul_f32_e32 v87, v90, v90
	v_fmac_f32_e32 v87, v91, v91
	v_add_f32_e32 v86, v87, v86
	v_add_f32_e32 v94, v94, v86
	ds_bpermute_b32 v95, v114, v94
	v_cvt_pk_fp8_f32 v93, v82, v83
	v_cvt_pk_bf16_f32 v85, v88, v89
	v_cvt_pk_bf16_f32 v86, v82, v83
	s_waitcnt lgkmcnt(0)
	v_add_f32_e32 v82, v94, v95
	ds_bpermute_b32 v83, v115, v82
	v_cvt_pk_fp8_f32 v92, v88, v89 op_sel:[0,0,1]
	v_cvt_pk_fp8_f32 v93, v90, v91 op_sel:[0,0,1]
	v_or_b32_e32 v170, 0x80, v170
	v_lshl_add_u64 v[88:89], v[170:171], 1, s[14:15]
	v_cvt_pk_bf16_f32 v87, v90, v91
	global_store_dwordx4 v[88:89], v[84:87], off
	s_nop 1
	v_lshl_add_u64 v[84:85], s[36:37], 0, v[170:171]
	global_store_dwordx2 v[84:85], v[92:93], off
	s_and_saveexec_b64 s[48:49], s[0:1]
	s_cbranch_execz .LBB0_1034
	v_lshl_add_u64 v[84:85], v[168:169], 2, s[18:19]
	s_waitcnt lgkmcnt(0)
	v_add_f32_e32 v82, v82, v83
	global_atomic_add_f32 v[84:85], v82, off
.LBB0_1034:
	s_or_b64 exec, exec, s[48:49]
	v_lshlrev_b32_e32 v82, 16, v134
	s_waitcnt lgkmcnt(0)
	v_and_b32_e32 v83, 0xffff0000, v134
	v_lshlrev_b32_e32 v84, 16, v135
	v_and_b32_e32 v85, 0xffff0000, v135
	v_lshlrev_b32_e32 v86, 16, v136
	v_and_b32_e32 v87, 0xffff0000, v136
	v_pk_add_f32 v[80:81], v[80:81], v[84:85]
	v_pk_add_f32 v[78:79], v[78:79], v[82:83]
	v_pk_add_f32 v[84:85], v[74:75], v[86:87]
	v_cvt_pk_fp8_f32 v86, v78, v79
	v_cvt_pk_fp8_f32 v87, v84, v85
	v_lshlrev_b32_e32 v88, 16, v137
	v_and_b32_e32 v89, 0xffff0000, v137
	v_pk_add_f32 v[82:83], v[76:77], v[88:89]
	v_cvt_pk_fp8_f32 v86, v80, v81 op_sel:[0,0,1]
	v_cvt_pk_fp8_f32 v87, v82, v83 op_sel:[0,0,1]
	v_cvt_pk_bf16_f32 v74, v78, v79
	v_cvt_pk_bf16_f32 v75, v80, v81
	v_lshl_add_u64 v[88:89], v[166:167], 1, s[14:15]
	v_cvt_pk_bf16_f32 v76, v84, v85
	v_cvt_pk_bf16_f32 v77, v82, v83
	global_store_dwordx4 v[88:89], v[74:77], off
	v_lshlrev_b32_e32 v90, 16, v130
	v_and_b32_e32 v91, 0xffff0000, v130
	v_lshl_add_u64 v[74:75], s[36:37], 0, v[166:167]
	global_store_dwordx2 v[74:75], v[86:87], off
	v_mul_f32_e32 v74, v79, v79
	v_mul_f32_e32 v75, v81, v81
	v_fmac_f32_e32 v74, v78, v78
	v_fmac_f32_e32 v75, v80, v80
	v_add_f32_e32 v74, v74, v75
	v_mul_f32_e32 v75, v84, v84
	v_fmac_f32_e32 v75, v85, v85
	v_add_f32_e32 v74, v75, v74
	v_mul_f32_e32 v75, v82, v82
	v_lshlrev_b32_e32 v92, 16, v131
	v_and_b32_e32 v93, 0xffff0000, v131
	v_lshlrev_b32_e32 v96, 16, v133
	v_and_b32_e32 v97, 0xffff0000, v133
	v_fmac_f32_e32 v75, v83, v83
	v_pk_add_f32 v[70:71], v[70:71], v[90:91]
	v_add_f32_e32 v78, v75, v74
	v_pk_add_f32 v[72:73], v[72:73], v[92:93]
	v_pk_add_f32 v[74:75], v[68:69], v[96:97]
	v_cvt_pk_bf16_f32 v68, v70, v71
	v_cvt_pk_fp8_f32 v76, v70, v71
	v_mul_f32_e32 v71, v71, v71
	v_lshlrev_b32_e32 v94, 16, v132
	v_and_b32_e32 v95, 0xffff0000, v132
	v_fmac_f32_e32 v71, v70, v70
	v_mul_f32_e32 v70, v73, v73
	v_pk_add_f32 v[66:67], v[66:67], v[94:95]
	v_fmac_f32_e32 v70, v72, v72
	v_add_f32_e32 v70, v71, v70
	v_mul_f32_e32 v71, v66, v66
	v_fmac_f32_e32 v71, v67, v67
	v_add_f32_e32 v70, v71, v70
	v_mul_f32_e32 v71, v74, v74
	v_fmac_f32_e32 v71, v75, v75
	v_add_f32_e32 v70, v71, v70
	v_add_f32_e32 v78, v78, v70
	ds_bpermute_b32 v79, v114, v78
	v_cvt_pk_fp8_f32 v77, v66, v67
	v_cvt_pk_bf16_f32 v69, v72, v73
	v_cvt_pk_bf16_f32 v70, v66, v67
	s_waitcnt lgkmcnt(0)
	v_add_f32_e32 v66, v78, v79
	ds_bpermute_b32 v67, v115, v66
	v_cvt_pk_fp8_f32 v76, v72, v73 op_sel:[0,0,1]
	v_cvt_pk_fp8_f32 v77, v74, v75 op_sel:[0,0,1]
	v_or_b32_e32 v166, 0x80, v166
	v_lshl_add_u64 v[72:73], v[166:167], 1, s[14:15]
	v_cvt_pk_bf16_f32 v71, v74, v75
	global_store_dwordx4 v[72:73], v[68:71], off
	s_nop 1
	v_lshl_add_u64 v[68:69], s[36:37], 0, v[166:167]
	global_store_dwordx2 v[68:69], v[76:77], off
	s_and_saveexec_b64 s[48:49], s[0:1]
	s_cbranch_execz .LBB0_1036
	v_lshl_add_u64 v[68:69], v[164:165], 2, s[18:19]
	s_waitcnt lgkmcnt(0)
	v_add_f32_e32 v66, v66, v67
	global_atomic_add_f32 v[68:69], v66, off

; __device__ __forceinline__ unsigned cvt_pk_bf16(float lo, float hi) { unsigned r; asm volatile("v_cvt_pk_bf16_f32 %0, %1, %2" : "=v"(r) : "v"(lo), "v"(hi)); return r; }
; __device__ __forceinline__ unsigned pk4_fp8(float a, float b, float c, float d) { int w = __builtin_amdgcn_cvt_pk_fp8_f32(a, b, 0, false); w = __builtin_amdgcn_cvt_pk_fp8_f32(c, d, w, true); return (unsigned)w; }
;     __device__ __forceinline__ void operator()(AccRef acc, const Unit& u, int wr, int wc, int fr, int fq) const {
;     ...
;             for (int m = 0; m < 4; ++m) { const int row = u.pm * 256 + ai * 128 + wr * 64 + m * 16 + fr; const size_t off = (size_t)row * DM + col0; float ss = 0.f;
; #pragma unroll
;                 for (int bj = 0; bj < 2; ++bj) { const size_t o2 = off + bj * 128; const f32x4 v0 = rv[m][bj][0] + acc[ai][bj][m][0] * ascale, v1 = rv[m][bj][1] + acc[ai][bj][m][1] * ascale;
;                     if (outf) { *(f32x4*)(outf + o2) = v0; *(f32x4*)(outf + o2 + 4) = v1; }
;                     if (outb) { u32x4 w; w.x = cvt_pk_bf16(v0[0], v0[1]); w.y = cvt_pk_bf16(v0[2], v0[3]); w.z = cvt_pk_bf16(v1[0], v1[1]); w.w = cvt_pk_bf16(v1[2], v1[3]); *(u32x4*)(outb + o2) = w; }
;                     if (out8) { u32x2 w8; w8.x = pk4_fp8(v0[0], v0[1], v0[2], v0[3]); w8.y = pk4_fp8(v1[0], v1[1], v1[2], v1[3]); *(u32x2*)((unsigned char*)out8 + o2) = w8; }
;                     ss += (v0[0] * v0[0] + v0[1] * v0[1]) + (v0[2] * v0[2] + v0[3] * v0[3]) + (v1[0] * v1[0] + v1[1] * v1[1]) + (v1[2] * v1[2] + v1[3] * v1[3]); }
;                 ss += __shfl_xor(ss, 16); ss += __shfl_xor(ss, 32);
;                 if (fq == 0) atomicAdd(ssq + row, ss); }
.LBB0_1038:
	s_or_b64 exec, exec, s[48:49]
	s_waitcnt vmcnt(9)
	v_lshlrev_b32_e32 v50, 16, v86
	s_waitcnt lgkmcnt(0)
	v_and_b32_e32 v51, 0xffff0000, v86
	v_lshlrev_b32_e32 v52, 16, v87
	v_and_b32_e32 v53, 0xffff0000, v87
	v_lshlrev_b32_e32 v54, 16, v88
	v_and_b32_e32 v55, 0xffff0000, v88
	v_pk_add_f32 v[48:49], v[48:49], v[52:53]
	v_pk_add_f32 v[46:47], v[46:47], v[50:51]
	v_pk_add_f32 v[52:53], v[42:43], v[54:55]
	v_cvt_pk_fp8_f32 v54, v46, v47
	v_cvt_pk_fp8_f32 v55, v52, v53
	v_lshlrev_b32_e32 v56, 16, v89
	v_and_b32_e32 v57, 0xffff0000, v89
	v_pk_add_f32 v[50:51], v[44:45], v[56:57]
	v_cvt_pk_fp8_f32 v54, v48, v49 op_sel:[0,0,1]
	v_cvt_pk_fp8_f32 v55, v50, v51 op_sel:[0,0,1]
	v_cvt_pk_bf16_f32 v42, v46, v47
	v_cvt_pk_bf16_f32 v43, v48, v49
	v_lshl_add_u64 v[56:57], v[100:101], 1, s[14:15]
	v_cvt_pk_bf16_f32 v44, v52, v53
	v_cvt_pk_bf16_f32 v45, v50, v51
	global_store_dwordx4 v[56:57], v[42:45], off
	s_waitcnt vmcnt(9)
	v_lshlrev_b32_e32 v58, 16, v82
	v_and_b32_e32 v59, 0xffff0000, v82
	v_lshl_add_u64 v[42:43], s[36:37], 0, v[100:101]
	global_store_dwordx2 v[42:43], v[54:55], off
	v_mul_f32_e32 v42, v47, v47
	v_mul_f32_e32 v43, v49, v49
	v_fmac_f32_e32 v42, v46, v46
	v_fmac_f32_e32 v43, v48, v48
	v_add_f32_e32 v42, v42, v43
	v_mul_f32_e32 v43, v52, v52
	v_fmac_f32_e32 v43, v53, v53
	v_add_f32_e32 v42, v43, v42
	v_mul_f32_e32 v43, v50, v50
	v_lshlrev_b32_e32 v60, 16, v83
	v_and_b32_e32 v61, 0xffff0000, v83
	v_lshlrev_b32_e32 v64, 16, v85
	v_and_b32_e32 v65, 0xffff0000, v85
	v_fmac_f32_e32 v43, v51, v51
	v_pk_add_f32 v[38:39], v[38:39], v[58:59]
	v_add_f32_e32 v46, v43, v42
	v_pk_add_f32 v[40:41], v[40:41], v[60:61]
	v_pk_add_f32 v[42:43], v[36:37], v[64:65]
	v_cvt_pk_bf16_f32 v36, v38, v39
	v_cvt_pk_fp8_f32 v44, v38, v39
	v_mul_f32_e32 v39, v39, v39
	v_lshlrev_b32_e32 v62, 16, v84
	v_and_b32_e32 v63, 0xffff0000, v84
	v_fmac_f32_e32 v39, v38, v38
	v_mul_f32_e32 v38, v41, v41
	v_pk_add_f32 v[34:35], v[34:35], v[62:63]
	v_fmac_f32_e32 v38, v40, v40
	v_add_f32_e32 v38, v39, v38
	v_mul_f32_e32 v39, v34, v34
	v_fmac_f32_e32 v39, v35, v35
	v_add_f32_e32 v38, v39, v38
	v_mul_f32_e32 v39, v42, v42
	v_fmac_f32_e32 v39, v43, v43
	v_add_f32_e32 v38, v39, v38
	v_add_f32_e32 v46, v46, v38
	ds_bpermute_b32 v47, v114, v46
	v_cvt_pk_fp8_f32 v45, v34, v35
	v_cvt_pk_bf16_f32 v37, v40, v41
	v_cvt_pk_bf16_f32 v38, v34, v35
	s_waitcnt lgkmcnt(0)
	v_add_f32_e32 v34, v46, v47
	ds_bpermute_b32 v35, v115, v34
	v_cvt_pk_fp8_f32 v44, v40, v41 op_sel:[0,0,1]
	v_cvt_pk_fp8_f32 v45, v42, v43 op_sel:[0,0,1]
	v_or_b32_e32 v100, 0x80, v100
	v_lshl_add_u64 v[40:41], v[100:101], 1, s[14:15]
	v_cvt_pk_bf16_f32 v39, v42, v43
	global_store_dwordx4 v[40:41], v[36:39], off
	s_nop 1
	v_lshl_add_u64 v[36:37], s[36:37], 0, v[100:101]
	global_store_dwordx2 v[36:37], v[44:45], off
	s_and_saveexec_b64 s[48:49], s[0:1]
	s_cbranch_execz .LBB0_1040
	v_lshl_add_u64 v[36:37], v[98:99], 2, s[18:19]
	s_waitcnt lgkmcnt(0)
	v_add_f32_e32 v34, v34, v35
	global_atomic_add_f32 v[36:37], v34, off
; __device__ __forceinline__ unsigned cvt_pk_bf16(float lo, float hi) { unsigned r; asm volatile("v_cvt_pk_bf16_f32 %0, %1, %2" : "=v"(r) : "v"(lo), "v"(hi)); return r; }
; __device__ __forceinline__ unsigned pk4_fp8(float a, float b, float c, float d) { int w = __builtin_amdgcn_cvt_pk_fp8_f32(a, b, 0, false); w = __builtin_amdgcn_cvt_pk_fp8_f32(c, d, w, true); return (unsigned)w; }
;     __device__ __forceinline__ void operator()(AccRef acc, const Unit& u, int wr, int wc, int fr, int fq) const {
;     ...
;             for (int m = 0; m < 4; ++m) { const int row = u.pm * 256 + ai * 128 + wr * 64 + m * 16 + fr; const size_t off = (size_t)row * DM + col0; float ss = 0.f;
; #pragma unroll
;                 for (int bj = 0; bj < 2; ++bj) { const size_t o2 = off + bj * 128; const f32x4 v0 = rv[m][bj][0] + acc[ai][bj][m][0] * ascale, v1 = rv[m][bj][1] + acc[ai][bj][m][1] * ascale;
;                     if (outf) { *(f32x4*)(outf + o2) = v0; *(f32x4*)(outf + o2 + 4) = v1; }
;                     if (outb) { u32x4 w; w.x = cvt_pk_bf16(v0[0], v0[1]); w.y = cvt_pk_bf16(v0[2], v0[3]); w.z = cvt_pk_bf16(v1[0], v1[1]); w.w = cvt_pk_bf16(v1[2], v1[3]); *(u32x4*)(outb + o2) = w; }
;                     if (out8) { u32x2 w8; w8.x = pk4_fp8(v0[0], v0[1], v0[2], v0[3]); w8.y = pk4_fp8(v1[0], v1[1], v1[2], v1[3]); *(u32x2*)((unsigned char*)out8 + o2) = w8; }
;                     ss += (v0[0] * v0[0] + v0[1] * v0[1]) + (v0[2] * v0[2] + v0[3] * v0[3]) + (v1[0] * v1[0] + v1[1] * v1[1]) + (v1[2] * v1[2] + v1[3] * v1[3]); }
;                 ss += __shfl_xor(ss, 16); ss += __shfl_xor(ss, 32);
;                 if (fq == 0) atomicAdd(ssq + row, ss); }
.LBB0_1040:
	s_or_b64 exec, exec, s[48:49]
	s_waitcnt vmcnt(11)
	v_lshlrev_b32_e32 v34, 16, v78
	s_waitcnt lgkmcnt(0)
	v_and_b32_e32 v35, 0xffff0000, v78
	v_lshlrev_b32_e32 v36, 16, v79
	v_and_b32_e32 v37, 0xffff0000, v79
	v_lshlrev_b32_e32 v38, 16, v80
	v_and_b32_e32 v39, 0xffff0000, v80
	v_pk_add_f32 v[24:25], v[24:25], v[36:37]
	v_pk_add_f32 v[22:23], v[22:23], v[34:35]
	v_pk_add_f32 v[36:37], v[18:19], v[38:39]
	v_cvt_pk_fp8_f32 v38, v22, v23
	v_cvt_pk_fp8_f32 v39, v36, v37
	v_lshlrev_b32_e32 v40, 16, v81
	v_and_b32_e32 v41, 0xffff0000, v81
	v_pk_add_f32 v[34:35], v[20:21], v[40:41]
	v_cvt_pk_fp8_f32 v38, v24, v25 op_sel:[0,0,1]
	v_cvt_pk_fp8_f32 v39, v34, v35 op_sel:[0,0,1]
	v_cvt_pk_bf16_f32 v18, v22, v23
	v_cvt_pk_bf16_f32 v19, v24, v25
	v_lshl_add_u64 v[40:41], v[96:97], 1, s[14:15]
	v_cvt_pk_bf16_f32 v20, v36, v37
	v_cvt_pk_bf16_f32 v21, v34, v35
	global_store_dwordx4 v[40:41], v[18:21], off
	s_waitcnt vmcnt(11)
	v_lshlrev_b32_e32 v42, 16, v74
	v_and_b32_e32 v43, 0xffff0000, v74
	v_lshl_add_u64 v[18:19], s[36:37], 0, v[96:97]
	global_store_dwordx2 v[18:19], v[38:39], off
	v_mul_f32_e32 v18, v23, v23
	v_mul_f32_e32 v19, v25, v25
	v_fmac_f32_e32 v18, v22, v22
	v_fmac_f32_e32 v19, v24, v24
	v_add_f32_e32 v18, v18, v19
	v_mul_f32_e32 v19, v36, v36
	v_fmac_f32_e32 v19, v37, v37
	v_lshlrev_b32_e32 v48, 16, v77
	v_and_b32_e32 v49, 0xffff0000, v77
	v_add_f32_e32 v18, v19, v18
	v_mul_f32_e32 v19, v34, v34
	v_lshlrev_b32_e32 v44, 16, v75
	v_and_b32_e32 v45, 0xffff0000, v75
	v_fmac_f32_e32 v19, v35, v35
	v_pk_add_f32 v[22:23], v[30:31], v[42:43]
	v_pk_add_f32 v[24:25], v[28:29], v[48:49]
	v_add_f32_e32 v34, v19, v18
	v_pk_add_f32 v[18:19], v[32:33], v[44:45]
	v_cvt_pk_bf16_f32 v20, v22, v23
	v_cvt_pk_fp8_f32 v28, v22, v23
	v_mul_f32_e32 v23, v23, v23
	v_lshlrev_b32_e32 v46, 16, v76
	v_and_b32_e32 v47, 0xffff0000, v76
	v_fmac_f32_e32 v23, v22, v22
	v_mul_f32_e32 v22, v19, v19
	v_pk_add_f32 v[26:27], v[26:27], v[46:47]
	v_fmac_f32_e32 v22, v18, v18
	v_add_f32_e32 v22, v23, v22
	v_mul_f32_e32 v23, v26, v26
	v_fmac_f32_e32 v23, v27, v27
	v_add_f32_e32 v22, v23, v22
	v_mul_f32_e32 v23, v24, v24
	v_fmac_f32_e32 v23, v25, v25
	v_add_f32_e32 v22, v23, v22
	v_add_f32_e32 v30, v34, v22
	ds_bpermute_b32 v31, v114, v30
	v_cvt_pk_fp8_f32 v29, v26, v27
	v_cvt_pk_bf16_f32 v21, v18, v19
	v_cvt_pk_fp8_f32 v28, v18, v19 op_sel:[0,0,1]
	s_waitcnt lgkmcnt(0)
	v_add_f32_e32 v18, v30, v31
	ds_bpermute_b32 v19, v115, v18
	v_cvt_pk_fp8_f32 v29, v24, v25 op_sel:[0,0,1]
	v_or_b32_e32 v96, 0x80, v96
	v_cvt_pk_bf16_f32 v22, v26, v27
	v_cvt_pk_bf16_f32 v23, v24, v25
	v_lshl_add_u64 v[24:25], v[96:97], 1, s[14:15]
	global_store_dwordx4 v[24:25], v[20:23], off
	s_nop 1
	v_lshl_add_u64 v[20:21], s[36:37], 0, v[96:97]
	global_store_dwordx2 v[20:21], v[28:29], off
	s_and_saveexec_b64 s[48:49], s[0:1]
	s_cbranch_execz .LBB0_1042
	v_lshl_add_u64 v[20:21], v[94:95], 2, s[18:19]
	s_waitcnt lgkmcnt(0)
	v_add_f32_e32 v18, v18, v19
	global_atomic_add_f32 v[20:21], v18, off
.LBB0_1042:
	s_or_b64 exec, exec, s[48:49]
	s_waitcnt vmcnt(13)
	v_lshlrev_b32_e32 v18, 16, v70
	s_waitcnt lgkmcnt(0)
	v_and_b32_e32 v19, 0xffff0000, v70
	v_lshlrev_b32_e32 v20, 16, v71
	v_and_b32_e32 v21, 0xffff0000, v71
	v_lshlrev_b32_e32 v22, 16, v72
	v_and_b32_e32 v23, 0xffff0000, v72
	v_pk_add_f32 v[8:9], v[8:9], v[20:21]
	v_pk_add_f32 v[6:7], v[6:7], v[18:19]
	v_pk_add_f32 v[20:21], v[2:3], v[22:23]
	v_cvt_pk_fp8_f32 v22, v6, v7
	v_cvt_pk_fp8_f32 v23, v20, v21
	v_lshlrev_b32_e32 v24, 16, v73
	v_and_b32_e32 v25, 0xffff0000, v73
	v_pk_add_f32 v[18:19], v[4:5], v[24:25]
	v_cvt_pk_fp8_f32 v22, v8, v9 op_sel:[0,0,1]
	v_cvt_pk_fp8_f32 v23, v18, v19 op_sel:[0,0,1]
	v_cvt_pk_bf16_f32 v2, v6, v7
	v_cvt_pk_bf16_f32 v3, v8, v9
	v_lshl_add_u64 v[24:25], v[92:93], 1, s[14:15]
	v_cvt_pk_bf16_f32 v4, v20, v21
	v_cvt_pk_bf16_f32 v5, v18, v19
	global_store_dwordx4 v[24:25], v[2:5], off
	s_waitcnt vmcnt(13)
	v_lshlrev_b32_e32 v26, 16, v66
	v_and_b32_e32 v27, 0xffff0000, v66
	v_lshl_add_u64 v[2:3], s[36:37], 0, v[92:93]
	global_store_dwordx2 v[2:3], v[22:23], off
	v_mul_f32_e32 v2, v7, v7
	v_mul_f32_e32 v3, v9, v9
	v_fmac_f32_e32 v2, v6, v6
	v_fmac_f32_e32 v3, v8, v8
	v_add_f32_e32 v2, v2, v3
	v_mul_f32_e32 v3, v20, v20
	v_fmac_f32_e32 v3, v21, v21
	v_lshlrev_b32_e32 v32, 16, v69
	v_and_b32_e32 v33, 0xffff0000, v69
	v_add_f32_e32 v2, v3, v2
	v_mul_f32_e32 v3, v18, v18
	v_lshlrev_b32_e32 v28, 16, v67
	v_and_b32_e32 v29, 0xffff0000, v67
	v_fmac_f32_e32 v3, v19, v19
	v_pk_add_f32 v[6:7], v[14:15], v[26:27]
	v_pk_add_f32 v[8:9], v[12:13], v[32:33]
	v_add_f32_e32 v18, v3, v2
	v_pk_add_f32 v[2:3], v[16:17], v[28:29]
	v_cvt_pk_bf16_f32 v4, v6, v7
	v_cvt_pk_fp8_f32 v12, v6, v7
	v_mul_f32_e32 v7, v7, v7
	v_lshlrev_b32_e32 v30, 16, v68
	v_and_b32_e32 v31, 0xffff0000, v68
	v_fmac_f32_e32 v7, v6, v6
	v_mul_f32_e32 v6, v3, v3
	v_pk_add_f32 v[10:11], v[10:11], v[30:31]
	v_fmac_f32_e32 v6, v2, v2
	v_add_f32_e32 v6, v7, v6
	v_mul_f32_e32 v7, v10, v10
	v_fmac_f32_e32 v7, v11, v11
	v_add_f32_e32 v6, v7, v6
	v_mul_f32_e32 v7, v8, v8
	v_fmac_f32_e32 v7, v9, v9
	v_add_f32_e32 v6, v7, v6
	v_add_f32_e32 v14, v18, v6
	ds_bpermute_b32 v15, v114, v14
	v_cvt_pk_fp8_f32 v13, v10, v11
	v_cvt_pk_bf16_f32 v5, v2, v3
	v_cvt_pk_fp8_f32 v12, v2, v3 op_sel:[0,0,1]
	s_waitcnt lgkmcnt(0)
	v_add_f32_e32 v2, v14, v15
	ds_bpermute_b32 v3, v115, v2
	v_cvt_pk_fp8_f32 v13, v8, v9 op_sel:[0,0,1]
	v_or_b32_e32 v92, 0x80, v92
	v_cvt_pk_bf16_f32 v6, v10, v11
	v_cvt_pk_bf16_f32 v7, v8, v9
	v_lshl_add_u64 v[8:9], v[92:93], 1, s[14:15]
	global_store_dwordx4 v[8:9], v[4:7], off
	s_nop 1
	v_lshl_add_u64 v[4:5], s[36:37], 0, v[92:93]
	global_store_dwordx2 v[4:5], v[12:13], off
	s_and_saveexec_b64 s[48:49], s[0:1]
	s_cbranch_execz .LBB0_1044
	v_lshl_add_u64 v[4:5], v[90:91], 2, s[18:19]
	s_waitcnt lgkmcnt(0)
	v_add_f32_e32 v2, v2, v3
	global_atomic_add_f32 v[4:5], v2, off

; #define LAS __attribute__((address_space(3)))
; __device__ __forceinline__ unsigned pk4_fp8(float a, float b, float c, float d) { int w = __builtin_amdgcn_cvt_pk_fp8_f32(a, b, 0, false); w = __builtin_amdgcn_cvt_pk_fp8_f32(c, d, w, true); return (unsigned)w; }
; __device__ __forceinline__ f32x4 swiglu4(f32x4 ug, f32x4 ul) {
;     f32x4 xg, xl, e, sg;
; #pragma unroll
;     for (int j = 0; j < 4; ++j) { xg[j] = __builtin_fminf(ug[j], 7.0f); xl[j] = __builtin_fminf(__builtin_fmaxf(ul[j], -7.0f), 7.0f); }
;     const f32x4 t = xg * (-1.702f * LOG2E);
; #pragma unroll
;     for (int j = 0; j < 4; ++j) e[j] = __builtin_amdgcn_exp2f(t[j]);
;     const f32x4 d = e + 1.0f;
; #pragma unroll
;     for (int j = 0; j < 4; ++j) sg[j] = __builtin_amdgcn_rcpf(d[j]);
;     return (xg * sg) * (xl + 1.0f);
; }
;     __device__ __forceinline__ void operator()(AccRef acc, const Unit& u, int wr, int wc, int fr, int fq, const LAS unsigned char* pre) const {
;         const int o0 = u.pn * 128 + wc * 32 + 8 * fq; const int cnt = tab[98 + u.e];
;         f32x4 bb[4];
; #pragma unroll
;         for (int q = 0; q < 4; ++q) bb[q] = *(const LAS f32x4*)(pre + (2 * (wc * 32 + 8 * fq) + 4 * q) * 4);
;         f32x4 bgv[2], blv[2];
; #pragma unroll
;         for (int n = 0; n < 2; ++n)
; #pragma unroll
;             for (int j = 0; j < 4; ++j) { const int q = 4 * n + j; bgv[n][j] = bb[q >> 1][(q & 1) * 2]; blv[n][j] = bb[q >> 1][(q & 1) * 2 + 1]; }
;         float rsv[8];
; #pragma unroll
;         for (int i = 0; i < 8; ++i) rsv[i] = *(const LAS float*)(pre + 1024 + ((i >> 2) * 128 + wr * 64 + (i & 3) * 16 + fr) * 4) * WSCALE_INV;
; #pragma unroll
;         for (int ai = 0; ai < 2; ++ai)
; #pragma unroll
;             for (int m = 0; m < 4; ++m) { const int r = ai * 128 + wr * 64 + m * 16 + fr, pos = u.pm * 256 + r; const bool valid = pos < cnt;
;                 const float rs = rsv[ai * 4 + m];
;                 const f32x4 h0 = swiglu4(acc[ai][0][m][0] * rs + bgv[0], acc[ai][1][m][0] * rs + blv[0]), h1 = swiglu4(acc[ai][0][m][1] * rs + bgv[1], acc[ai][1][m][1] * rs + blv[1]);
;                 u32x2 w; w.x = pk4_fp8(h0[0], h0[1], h0[2], h0[3]); w.y = pk4_fp8(h1[0], h1[1], h1[2], h1[3]);
;                 if (valid) *(u32x2*)(H + (size_t)(u.aux + r) * DE + o0) = w; }
.LBB0_1192:
	s_lshl_b32 s43, s72, 12
	s_and_b32 s43, s43, 0x1000
	s_lshl_b32 s45, s48, 2
	s_add_i32 s43, s43, 0
	s_add_i32 s45, s45, 0
	s_add_i32 s43, s43, 0x20000
	s_add_i32 s45, s45, 0x27988
	s_nop 15
	s_nop 15
	v_mov_b32_e32 v2, s45
	v_add_u32_e32 v30, s43, v192
	v_add_u32_e32 v14, s43, v195
	ds_read_b32 v28, v2
	ds_read_b128 v[2:5], v14
	ds_read_b128 v[6:9], v14 offset:16
	ds_read_b128 v[10:13], v14 offset:32
	v_add_u32_e32 v15, 0x400, v30
	v_add_u32_e32 v18, s43, v196
	ds_read2_b32 v[26:27], v15 offset0:16 offset1:32
	ds_read_b128 v[14:17], v14 offset:48
	ds_read_b32 v29, v30 offset:1216
	v_add_u32_e32 v18, 0x400, v18
	ds_read2_b32 v[24:25], v18 offset1:16
	ds_read2_b32 v[22:23], v18 offset0:32 offset1:48
	s_lshl_b32 s43, s80, 8
	v_lshl_or_b32 v18, s46, 7, v194
	s_waitcnt lgkmcnt(0)
	v_mov_b32_e32 v20, v11
	v_mov_b32_e32 v11, v12
	v_mov_b32_e32 v12, v3
	v_mov_b32_e32 v3, v4
	v_add_u32_e32 v4, s43, v175
	v_mov_b32_e32 v21, v13
	v_mov_b32_e32 v13, v5
	v_ashrrev_i32_e32 v19, 31, v18
	v_cmp_lt_i32_e32 vcc, v4, v28
	s_and_saveexec_b64 s[46:47], vcc
	s_cbranch_execz .LBB0_1194
	ds_read_b32 v30, v30 offset:1024
	v_mov_b32_e32 v4, v15
	v_mov_b32_e32 v5, v17
	s_waitcnt lgkmcnt(0)
	v_mul_f32_e32 v30, 0x3c800000, v30
	v_pk_fma_f32 v[4:5], v[156:157], v[30:31], v[4:5] op_sel_hi:[1,0,1]
	v_pk_fma_f32 v[156:157], v[158:159], v[30:31], v[10:11] op_sel_hi:[1,0,1]
	v_pk_fma_f32 v[32:33], v[154:155], v[30:31], v[20:21] op_sel_hi:[1,0,1]
	v_mov_b32_e32 v154, v14
	v_mov_b32_e32 v155, v16
	v_min_f32_e32 v156, 0x40e00000, v156
	v_pk_fma_f32 v[154:155], v[160:161], v[30:31], v[154:155] op_sel_hi:[1,0,1]
	v_min_f32_e32 v157, 0x40e00000, v157
	v_mul_f32_e32 v31, 0xc01d265f, v156
	v_exp_f32_e32 v31, v31
	v_mul_f32_e32 v158, 0xc01d265f, v157
	v_exp_f32_e32 v159, v158
	v_min_f32_e32 v154, 0x40e00000, v154
	v_add_f32_e32 v31, 1.0, v31
	v_min_f32_e32 v155, 0x40e00000, v155
	v_rcp_f32_e32 v158, v31
	v_add_f32_e32 v31, 1.0, v159
	v_mul_f32_e32 v159, 0xc01d265f, v154
	v_exp_f32_e32 v160, v159
	v_mul_f32_e32 v159, 0xc01d265f, v155
	v_exp_f32_e32 v161, v159
	v_rcp_f32_e32 v159, v31
	v_add_f32_e32 v31, 1.0, v160
	v_med3_f32 v32, v32, s77, v205
	v_med3_f32 v33, v33, s77, v205
	v_rcp_f32_e32 v160, v31
	v_add_f32_e32 v31, 1.0, v161
	v_pk_add_f32 v[32:33], v[32:33], 1.0 op_sel_hi:[1,0]
	v_rcp_f32_e32 v161, v31
	v_pk_mul_f32 v[156:157], v[156:157], v[158:159]
	v_pk_mul_f32 v[32:33], v[32:33], v[156:157]
	v_med3_f32 v4, v4, s77, v205
	v_cvt_pk_fp8_f32 v31, v32, v33
	v_med3_f32 v5, v5, s77, v205
	v_pk_add_f32 v[4:5], v[4:5], 1.0 op_sel_hi:[1,0]
	v_pk_mul_f32 v[32:33], v[154:155], v[160:161]
	s_nop 0
	v_pk_mul_f32 v[4:5], v[4:5], v[32:33]
	s_nop 0
	v_cvt_pk_fp8_f32 v31, v4, v5 op_sel:[0,0,1]
	v_mov_b32_e32 v4, v7
	v_mov_b32_e32 v5, v9
	v_pk_fma_f32 v[4:5], v[148:149], v[30:31], v[4:5] op_sel_hi:[1,0,1]
	v_pk_fma_f32 v[148:149], v[150:151], v[30:31], v[2:3] op_sel_hi:[1,0,1]
	v_pk_fma_f32 v[32:33], v[146:147], v[30:31], v[12:13] op_sel_hi:[1,0,1]
	v_mov_b32_e32 v146, v6
	v_mov_b32_e32 v147, v8
	v_min_f32_e32 v148, 0x40e00000, v148
	v_pk_fma_f32 v[146:147], v[152:153], v[30:31], v[146:147] op_sel_hi:[1,0,1]
	v_min_f32_e32 v149, 0x40e00000, v149
	v_mul_f32_e32 v30, 0xc01d265f, v148
	v_exp_f32_e32 v30, v30
	v_mul_f32_e32 v150, 0xc01d265f, v149
	v_exp_f32_e32 v151, v150
	v_min_f32_e32 v146, 0x40e00000, v146
	v_add_f32_e32 v30, 1.0, v30
	v_min_f32_e32 v147, 0x40e00000, v147
	v_rcp_f32_e32 v150, v30
	v_add_f32_e32 v30, 1.0, v151
	v_mul_f32_e32 v151, 0xc01d265f, v146
	v_exp_f32_e32 v152, v151
	v_mul_f32_e32 v151, 0xc01d265f, v147
	v_exp_f32_e32 v153, v151
	v_rcp_f32_e32 v151, v30
	v_add_f32_e32 v30, 1.0, v152
	v_med3_f32 v32, v32, s77, v205
	v_med3_f32 v33, v33, s77, v205
	v_rcp_f32_e32 v152, v30
	v_add_f32_e32 v30, 1.0, v153
	v_pk_add_f32 v[32:33], v[32:33], 1.0 op_sel_hi:[1,0]
	v_rcp_f32_e32 v153, v30
	v_pk_mul_f32 v[148:149], v[148:149], v[150:151]
	v_pk_mul_f32 v[32:33], v[32:33], v[148:149]
	v_med3_f32 v4, v4, s77, v205
	v_cvt_pk_fp8_f32 v30, v32, v33
	v_med3_f32 v5, v5, s77, v205
	v_pk_add_f32 v[4:5], v[4:5], 1.0 op_sel_hi:[1,0]
	v_pk_mul_f32 v[32:33], v[146:147], v[152:153]
	s_nop 0
	v_pk_mul_f32 v[4:5], v[4:5], v[32:33]
	s_nop 0
	v_cvt_pk_fp8_f32 v30, v4, v5 op_sel:[0,0,1]
	v_add_u32_e32 v4, s35, v175
	v_ashrrev_i32_e32 v5, 31, v4
	v_lshlrev_b64 v[4:5], 11, v[4:5]
	v_lshl_add_u64 v[4:5], s[14:15], 0, v[4:5]
	v_lshl_add_u64 v[4:5], v[4:5], 0, v[18:19]
	global_store_dwordx2 v[4:5], v[30:31], off
; __device__ __forceinline__ unsigned pk4_fp8(float a, float b, float c, float d) { int w = __builtin_amdgcn_cvt_pk_fp8_f32(a, b, 0, false); w = __builtin_amdgcn_cvt_pk_fp8_f32(c, d, w, true); return (unsigned)w; }
; __device__ __forceinline__ f32x4 swiglu4(f32x4 ug, f32x4 ul) {
;     f32x4 xg, xl, e, sg;
; #pragma unroll
;     for (int j = 0; j < 4; ++j) { xg[j] = __builtin_fminf(ug[j], 7.0f); xl[j] = __builtin_fminf(__builtin_fmaxf(ul[j], -7.0f), 7.0f); }
;     const f32x4 t = xg * (-1.702f * LOG2E);
; #pragma unroll
;     for (int j = 0; j < 4; ++j) e[j] = __builtin_amdgcn_exp2f(t[j]);
;     const f32x4 d = e + 1.0f;
; #pragma unroll
;     for (int j = 0; j < 4; ++j) sg[j] = __builtin_amdgcn_rcpf(d[j]);
;     return (xg * sg) * (xl + 1.0f);
; }
;     __device__ __forceinline__ void operator()(AccRef acc, const Unit& u, int wr, int wc, int fr, int fq, const LAS unsigned char* pre) const {
;     ...
;             for (int m = 0; m < 4; ++m) { const int r = ai * 128 + wr * 64 + m * 16 + fr, pos = u.pm * 256 + r; const bool valid = pos < cnt;
;                 const float rs = rsv[ai * 4 + m];
;                 const f32x4 h0 = swiglu4(acc[ai][0][m][0] * rs + bgv[0], acc[ai][1][m][0] * rs + blv[0]), h1 = swiglu4(acc[ai][0][m][1] * rs + bgv[1], acc[ai][1][m][1] * rs + blv[1]);
;                 u32x2 w; w.x = pk4_fp8(h0[0], h0[1], h0[2], h0[3]); w.y = pk4_fp8(h1[0], h1[1], h1[2], h1[3]);
;                 if (valid) *(u32x2*)(H + (size_t)(u.aux + r) * DE + o0) = w; }
.LBB0_1194:
	s_or_b64 exec, exec, s[46:47]
	v_add_u32_e32 v4, s43, v197
	v_cmp_lt_i32_e32 vcc, v4, v28
	s_and_saveexec_b64 s[46:47], vcc
	s_cbranch_execz .LBB0_1196
	v_mul_f32_e32 v4, 0x3c800000, v26
	v_mov_b32_e32 v30, v15
	v_mov_b32_e32 v31, v17
	v_pk_fma_f32 v[30:31], v[140:141], v[4:5], v[30:31] op_sel_hi:[1,0,1]
	v_pk_fma_f32 v[140:141], v[142:143], v[4:5], v[10:11] op_sel_hi:[1,0,1]
	v_pk_fma_f32 v[32:33], v[138:139], v[4:5], v[20:21] op_sel_hi:[1,0,1]
	v_mov_b32_e32 v138, v14
	v_mov_b32_e32 v139, v16
	v_min_f32_e32 v140, 0x40e00000, v140
	v_pk_fma_f32 v[138:139], v[144:145], v[4:5], v[138:139] op_sel_hi:[1,0,1]
	v_min_f32_e32 v141, 0x40e00000, v141
	v_mul_f32_e32 v5, 0xc01d265f, v140
	v_exp_f32_e32 v5, v5
	v_mul_f32_e32 v26, 0xc01d265f, v141
	v_exp_f32_e32 v26, v26
	v_min_f32_e32 v138, 0x40e00000, v138
	v_add_f32_e32 v5, 1.0, v5
	v_min_f32_e32 v139, 0x40e00000, v139
	v_rcp_f32_e32 v142, v5
	v_add_f32_e32 v5, 1.0, v26
	v_mul_f32_e32 v26, 0xc01d265f, v138
	v_exp_f32_e32 v26, v26
	v_mul_f32_e32 v143, 0xc01d265f, v139
	v_exp_f32_e32 v145, v143
	v_rcp_f32_e32 v143, v5
	v_add_f32_e32 v5, 1.0, v26
	v_med3_f32 v32, v32, s77, v205
	v_med3_f32 v33, v33, s77, v205
	v_rcp_f32_e32 v144, v5
	v_add_f32_e32 v5, 1.0, v145
	v_pk_add_f32 v[32:33], v[32:33], 1.0 op_sel_hi:[1,0]
	v_rcp_f32_e32 v145, v5
	v_pk_mul_f32 v[140:141], v[140:141], v[142:143]
	v_pk_mul_f32 v[32:33], v[32:33], v[140:141]
	v_med3_f32 v30, v30, s77, v205
	v_cvt_pk_fp8_f32 v5, v32, v33
	v_med3_f32 v31, v31, s77, v205
	v_pk_add_f32 v[30:31], v[30:31], 1.0 op_sel_hi:[1,0]
	v_pk_mul_f32 v[32:33], v[138:139], v[144:145]
	s_nop 0
	v_pk_mul_f32 v[30:31], v[30:31], v[32:33]
	s_nop 0
	v_cvt_pk_fp8_f32 v5, v30, v31 op_sel:[0,0,1]
	v_mov_b32_e32 v30, v7
	v_mov_b32_e32 v31, v9
	v_pk_fma_f32 v[30:31], v[132:133], v[4:5], v[30:31] op_sel_hi:[1,0,1]
	v_pk_fma_f32 v[132:133], v[134:135], v[4:5], v[2:3] op_sel_hi:[1,0,1]
	v_pk_fma_f32 v[32:33], v[130:131], v[4:5], v[12:13] op_sel_hi:[1,0,1]
	v_mov_b32_e32 v130, v6
	v_mov_b32_e32 v131, v8
	v_min_f32_e32 v132, 0x40e00000, v132
	v_pk_fma_f32 v[130:131], v[136:137], v[4:5], v[130:131] op_sel_hi:[1,0,1]
	v_min_f32_e32 v133, 0x40e00000, v133
	v_mul_f32_e32 v4, 0xc01d265f, v132
	v_exp_f32_e32 v4, v4
	v_mul_f32_e32 v26, 0xc01d265f, v133
	v_exp_f32_e32 v26, v26
	v_min_f32_e32 v130, 0x40e00000, v130
	v_add_f32_e32 v4, 1.0, v4
	v_min_f32_e32 v131, 0x40e00000, v131
	v_rcp_f32_e32 v134, v4
	v_add_f32_e32 v4, 1.0, v26
	v_mul_f32_e32 v26, 0xc01d265f, v130
	v_exp_f32_e32 v26, v26
	v_mul_f32_e32 v135, 0xc01d265f, v131
	v_exp_f32_e32 v137, v135
	v_rcp_f32_e32 v135, v4
	v_add_f32_e32 v4, 1.0, v26
	v_med3_f32 v32, v32, s77, v205
	v_med3_f32 v33, v33, s77, v205
	v_rcp_f32_e32 v136, v4
	v_add_f32_e32 v4, 1.0, v137
	v_pk_add_f32 v[32:33], v[32:33], 1.0 op_sel_hi:[1,0]
	v_rcp_f32_e32 v137, v4
	v_pk_mul_f32 v[132:133], v[132:133], v[134:135]
	v_pk_mul_f32 v[32:33], v[32:33], v[132:133]
	v_med3_f32 v30, v30, s77, v205
	v_cvt_pk_fp8_f32 v4, v32, v33
	v_med3_f32 v31, v31, s77, v205
	v_pk_add_f32 v[30:31], v[30:31], 1.0 op_sel_hi:[1,0]
	v_pk_mul_f32 v[32:33], v[130:131], v[136:137]
	s_nop 0
	v_pk_mul_f32 v[30:31], v[30:31], v[32:33]
	s_nop 0
	v_cvt_pk_fp8_f32 v4, v30, v31 op_sel:[0,0,1]
	v_add_u32_e32 v30, s35, v197
	v_ashrrev_i32_e32 v31, 31, v30
	v_lshlrev_b64 v[30:31], 11, v[30:31]
	v_lshl_add_u64 v[30:31], s[14:15], 0, v[30:31]
	v_lshl_add_u64 v[30:31], v[30:31], 0, v[18:19]
	global_store_dwordx2 v[30:31], v[4:5], off
.LBB0_1196:
	s_or_b64 exec, exec, s[46:47]
	v_add_u32_e32 v4, s43, v198
	v_cmp_lt_i32_e32 vcc, v4, v28
	s_and_saveexec_b64 s[46:47], vcc
	s_cbranch_execz .LBB0_1198
	v_mul_f32_e32 v4, 0x3c800000, v27
	v_pk_fma_f32 v[30:31], v[122:123], v[4:5], v[20:21] op_sel_hi:[1,0,1]
	v_pk_fma_f32 v[122:123], v[126:127], v[4:5], v[10:11] op_sel_hi:[1,0,1]
	v_mov_b32_e32 v26, v15
	v_mov_b32_e32 v27, v17
	v_mov_b32_e32 v32, v14
	v_mov_b32_e32 v33, v16
	v_min_f32_e32 v122, 0x40e00000, v122
	v_pk_fma_f32 v[26:27], v[124:125], v[4:5], v[26:27] op_sel_hi:[1,0,1]
	v_pk_fma_f32 v[32:33], v[128:129], v[4:5], v[32:33] op_sel_hi:[1,0,1]
	v_min_f32_e32 v123, 0x40e00000, v123
	v_mul_f32_e32 v5, 0xc01d265f, v122
	v_exp_f32_e32 v5, v5
	v_mul_f32_e32 v124, 0xc01d265f, v123
	v_exp_f32_e32 v125, v124
	v_min_f32_e32 v32, 0x40e00000, v32
	v_add_f32_e32 v5, 1.0, v5
	v_min_f32_e32 v33, 0x40e00000, v33
	v_rcp_f32_e32 v124, v5
	v_add_f32_e32 v5, 1.0, v125
	v_mul_f32_e32 v125, 0xc01d265f, v32
	v_exp_f32_e32 v126, v125
	v_mul_f32_e32 v125, 0xc01d265f, v33
	v_exp_f32_e32 v127, v125
	v_rcp_f32_e32 v125, v5
	v_add_f32_e32 v5, 1.0, v126
	v_med3_f32 v30, v30, s77, v205
	v_med3_f32 v31, v31, s77, v205
	v_rcp_f32_e32 v126, v5
	v_add_f32_e32 v5, 1.0, v127
	v_pk_add_f32 v[30:31], v[30:31], 1.0 op_sel_hi:[1,0]
	v_rcp_f32_e32 v127, v5
	v_pk_mul_f32 v[122:123], v[122:123], v[124:125]
	v_pk_mul_f32 v[30:31], v[30:31], v[122:123]
	v_med3_f32 v26, v26, s77, v205
	v_cvt_pk_fp8_f32 v5, v30, v31
	v_med3_f32 v27, v27, s77, v205
	v_pk_add_f32 v[26:27], v[26:27], 1.0 op_sel_hi:[1,0]
	v_pk_mul_f32 v[30:31], v[32:33], v[126:127]
	v_mov_b32_e32 v32, v6
	v_pk_mul_f32 v[26:27], v[26:27], v[30:31]
	v_mov_b32_e32 v33, v8
	v_cvt_pk_fp8_f32 v5, v26, v27 op_sel:[0,0,1]
	v_mov_b32_e32 v26, v7
	v_mov_b32_e32 v27, v9
	v_pk_fma_f32 v[30:31], v[114:115], v[4:5], v[12:13] op_sel_hi:[1,0,1]
	v_pk_fma_f32 v[114:115], v[118:119], v[4:5], v[2:3] op_sel_hi:[1,0,1]
	v_pk_fma_f32 v[26:27], v[116:117], v[4:5], v[26:27] op_sel_hi:[1,0,1]
	v_min_f32_e32 v114, 0x40e00000, v114
	v_pk_fma_f32 v[32:33], v[120:121], v[4:5], v[32:33] op_sel_hi:[1,0,1]
	v_min_f32_e32 v115, 0x40e00000, v115
	v_mul_f32_e32 v4, 0xc01d265f, v114
	v_exp_f32_e32 v4, v4
	v_mul_f32_e32 v116, 0xc01d265f, v115
	v_exp_f32_e32 v117, v116
	v_min_f32_e32 v32, 0x40e00000, v32
	v_add_f32_e32 v4, 1.0, v4
	v_min_f32_e32 v33, 0x40e00000, v33
	v_rcp_f32_e32 v116, v4
	v_add_f32_e32 v4, 1.0, v117
	v_mul_f32_e32 v117, 0xc01d265f, v32
	v_exp_f32_e32 v118, v117
	v_mul_f32_e32 v117, 0xc01d265f, v33
	v_exp_f32_e32 v119, v117
	v_rcp_f32_e32 v117, v4
	v_add_f32_e32 v4, 1.0, v118
	v_med3_f32 v30, v30, s77, v205
	v_med3_f32 v31, v31, s77, v205
	v_rcp_f32_e32 v118, v4
	v_add_f32_e32 v4, 1.0, v119
	v_pk_add_f32 v[30:31], v[30:31], 1.0 op_sel_hi:[1,0]
	v_rcp_f32_e32 v119, v4
	v_pk_mul_f32 v[114:115], v[114:115], v[116:117]
	v_pk_mul_f32 v[30:31], v[30:31], v[114:115]
	v_med3_f32 v26, v26, s77, v205
	v_cvt_pk_fp8_f32 v4, v30, v31
	v_med3_f32 v27, v27, s77, v205
	v_pk_add_f32 v[26:27], v[26:27], 1.0 op_sel_hi:[1,0]
	v_pk_mul_f32 v[30:31], v[32:33], v[118:119]
	s_nop 0
	v_pk_mul_f32 v[26:27], v[26:27], v[30:31]
	s_nop 0
	v_cvt_pk_fp8_f32 v4, v26, v27 op_sel:[0,0,1]
	v_add_u32_e32 v26, s35, v198
	v_ashrrev_i32_e32 v27, 31, v26
	v_lshlrev_b64 v[26:27], 11, v[26:27]
	v_lshl_add_u64 v[26:27], s[14:15], 0, v[26:27]
	v_lshl_add_u64 v[26:27], v[26:27], 0, v[18:19]
	global_store_dwordx2 v[26:27], v[4:5], off
; __device__ __forceinline__ unsigned pk4_fp8(float a, float b, float c, float d) { int w = __builtin_amdgcn_cvt_pk_fp8_f32(a, b, 0, false); w = __builtin_amdgcn_cvt_pk_fp8_f32(c, d, w, true); return (unsigned)w; }
; __device__ __forceinline__ f32x4 swiglu4(f32x4 ug, f32x4 ul) {
;     f32x4 xg, xl, e, sg;
; #pragma unroll
;     for (int j = 0; j < 4; ++j) { xg[j] = __builtin_fminf(ug[j], 7.0f); xl[j] = __builtin_fminf(__builtin_fmaxf(ul[j], -7.0f), 7.0f); }
;     const f32x4 t = xg * (-1.702f * LOG2E);
; #pragma unroll
;     for (int j = 0; j < 4; ++j) e[j] = __builtin_amdgcn_exp2f(t[j]);
;     const f32x4 d = e + 1.0f;
; #pragma unroll
;     for (int j = 0; j < 4; ++j) sg[j] = __builtin_amdgcn_rcpf(d[j]);
;     return (xg * sg) * (xl + 1.0f);
; }
;     __device__ __forceinline__ void operator()(AccRef acc, const Unit& u, int wr, int wc, int fr, int fq, const LAS unsigned char* pre) const {
;     ...
;             for (int m = 0; m < 4; ++m) { const int r = ai * 128 + wr * 64 + m * 16 + fr, pos = u.pm * 256 + r; const bool valid = pos < cnt;
;                 const float rs = rsv[ai * 4 + m];
;                 const f32x4 h0 = swiglu4(acc[ai][0][m][0] * rs + bgv[0], acc[ai][1][m][0] * rs + blv[0]), h1 = swiglu4(acc[ai][0][m][1] * rs + bgv[1], acc[ai][1][m][1] * rs + blv[1]);
;                 u32x2 w; w.x = pk4_fp8(h0[0], h0[1], h0[2], h0[3]); w.y = pk4_fp8(h1[0], h1[1], h1[2], h1[3]);
;                 if (valid) *(u32x2*)(H + (size_t)(u.aux + r) * DE + o0) = w; }
.LBB0_1198:
	s_or_b64 exec, exec, s[46:47]
	v_add_u32_e32 v4, s43, v199
	v_cmp_lt_i32_e32 vcc, v4, v28
	s_and_saveexec_b64 s[46:47], vcc
	s_cbranch_execz .LBB0_1200
	v_mul_f32_e32 v4, 0x3c800000, v29
	v_pk_fma_f32 v[30:31], v[106:107], v[4:5], v[20:21] op_sel_hi:[1,0,1]
	v_pk_fma_f32 v[106:107], v[110:111], v[4:5], v[10:11] op_sel_hi:[1,0,1]
	v_mov_b32_e32 v26, v15
	v_mov_b32_e32 v27, v17
	v_mov_b32_e32 v32, v14
	v_mov_b32_e32 v33, v16
	v_min_f32_e32 v106, 0x40e00000, v106
	v_pk_fma_f32 v[26:27], v[108:109], v[4:5], v[26:27] op_sel_hi:[1,0,1]
	v_pk_fma_f32 v[32:33], v[112:113], v[4:5], v[32:33] op_sel_hi:[1,0,1]
	v_min_f32_e32 v107, 0x40e00000, v107
	v_mul_f32_e32 v5, 0xc01d265f, v106
	v_exp_f32_e32 v5, v5
	v_mul_f32_e32 v29, 0xc01d265f, v107
	v_exp_f32_e32 v29, v29
	v_min_f32_e32 v32, 0x40e00000, v32
	v_add_f32_e32 v5, 1.0, v5
	v_min_f32_e32 v33, 0x40e00000, v33
	v_rcp_f32_e32 v108, v5
	v_add_f32_e32 v5, 1.0, v29
	v_mul_f32_e32 v29, 0xc01d265f, v32
	v_exp_f32_e32 v29, v29
	v_mul_f32_e32 v109, 0xc01d265f, v33
	v_exp_f32_e32 v111, v109
	v_rcp_f32_e32 v109, v5
	v_add_f32_e32 v5, 1.0, v29
	v_med3_f32 v30, v30, s77, v205
	v_med3_f32 v31, v31, s77, v205
	v_rcp_f32_e32 v110, v5
	v_add_f32_e32 v5, 1.0, v111
	v_pk_add_f32 v[30:31], v[30:31], 1.0 op_sel_hi:[1,0]
	v_rcp_f32_e32 v111, v5
	v_pk_mul_f32 v[106:107], v[106:107], v[108:109]
	v_pk_mul_f32 v[30:31], v[30:31], v[106:107]
	v_med3_f32 v26, v26, s77, v205
	v_cvt_pk_fp8_f32 v5, v30, v31
	v_med3_f32 v27, v27, s77, v205
	v_pk_add_f32 v[26:27], v[26:27], 1.0 op_sel_hi:[1,0]
	v_pk_mul_f32 v[30:31], v[32:33], v[110:111]
	v_mov_b32_e32 v32, v6
	v_pk_mul_f32 v[26:27], v[26:27], v[30:31]
	v_mov_b32_e32 v33, v8
	v_cvt_pk_fp8_f32 v5, v26, v27 op_sel:[0,0,1]
	v_mov_b32_e32 v26, v7
	v_mov_b32_e32 v27, v9
	v_pk_fma_f32 v[30:31], v[98:99], v[4:5], v[12:13] op_sel_hi:[1,0,1]
	v_pk_fma_f32 v[98:99], v[102:103], v[4:5], v[2:3] op_sel_hi:[1,0,1]
	v_pk_fma_f32 v[26:27], v[100:101], v[4:5], v[26:27] op_sel_hi:[1,0,1]
	v_min_f32_e32 v98, 0x40e00000, v98
	v_pk_fma_f32 v[32:33], v[104:105], v[4:5], v[32:33] op_sel_hi:[1,0,1]
	v_min_f32_e32 v99, 0x40e00000, v99
	v_mul_f32_e32 v4, 0xc01d265f, v98
	v_exp_f32_e32 v4, v4
	v_mul_f32_e32 v29, 0xc01d265f, v99
	v_exp_f32_e32 v29, v29
	v_min_f32_e32 v32, 0x40e00000, v32
	v_add_f32_e32 v4, 1.0, v4
	v_min_f32_e32 v33, 0x40e00000, v33
	v_rcp_f32_e32 v100, v4
	v_add_f32_e32 v4, 1.0, v29
	v_mul_f32_e32 v29, 0xc01d265f, v32
	v_exp_f32_e32 v29, v29
	v_mul_f32_e32 v101, 0xc01d265f, v33
	v_exp_f32_e32 v103, v101
	v_rcp_f32_e32 v101, v4
	v_add_f32_e32 v4, 1.0, v29
	v_med3_f32 v30, v30, s77, v205
	v_med3_f32 v31, v31, s77, v205
	v_rcp_f32_e32 v102, v4
	v_add_f32_e32 v4, 1.0, v103
	v_pk_add_f32 v[30:31], v[30:31], 1.0 op_sel_hi:[1,0]
	v_rcp_f32_e32 v103, v4
	v_pk_mul_f32 v[98:99], v[98:99], v[100:101]
	v_pk_mul_f32 v[30:31], v[30:31], v[98:99]
	v_med3_f32 v26, v26, s77, v205
	v_cvt_pk_fp8_f32 v4, v30, v31
	v_med3_f32 v27, v27, s77, v205
	v_pk_add_f32 v[26:27], v[26:27], 1.0 op_sel_hi:[1,0]
	v_pk_mul_f32 v[30:31], v[32:33], v[102:103]
	s_nop 0
	v_pk_mul_f32 v[26:27], v[26:27], v[30:31]
	s_nop 0
	v_cvt_pk_fp8_f32 v4, v26, v27 op_sel:[0,0,1]
	v_add_u32_e32 v26, s35, v199
	v_ashrrev_i32_e32 v27, 31, v26
	v_lshlrev_b64 v[26:27], 11, v[26:27]
	v_lshl_add_u64 v[26:27], s[14:15], 0, v[26:27]
	v_lshl_add_u64 v[26:27], v[26:27], 0, v[18:19]
	global_store_dwordx2 v[26:27], v[4:5], off
.LBB0_1200:
	s_or_b64 exec, exec, s[46:47]
	v_add_u32_e32 v4, s43, v200
	v_cmp_lt_i32_e32 vcc, v4, v28
	s_and_saveexec_b64 s[46:47], vcc
	s_cbranch_execz .LBB0_1202
	v_mul_f32_e32 v4, 0x3c800000, v24
	v_pk_fma_f32 v[30:31], v[90:91], v[4:5], v[20:21] op_sel_hi:[1,0,1]
	v_pk_fma_f32 v[90:91], v[94:95], v[4:5], v[10:11] op_sel_hi:[1,0,1]
	v_mov_b32_e32 v26, v15
	v_mov_b32_e32 v27, v17
	v_mov_b32_e32 v32, v14
	v_mov_b32_e32 v33, v16
	v_min_f32_e32 v90, 0x40e00000, v90
	v_pk_fma_f32 v[26:27], v[92:93], v[4:5], v[26:27] op_sel_hi:[1,0,1]
	v_pk_fma_f32 v[32:33], v[96:97], v[4:5], v[32:33] op_sel_hi:[1,0,1]
	v_min_f32_e32 v91, 0x40e00000, v91
	v_mul_f32_e32 v5, 0xc01d265f, v90
	v_exp_f32_e32 v5, v5
	v_mul_f32_e32 v24, 0xc01d265f, v91
	v_exp_f32_e32 v24, v24
	v_min_f32_e32 v32, 0x40e00000, v32
	v_add_f32_e32 v5, 1.0, v5
	v_min_f32_e32 v33, 0x40e00000, v33
	v_rcp_f32_e32 v92, v5
	v_add_f32_e32 v5, 1.0, v24
	v_mul_f32_e32 v24, 0xc01d265f, v32
	v_exp_f32_e32 v24, v24
	v_mul_f32_e32 v29, 0xc01d265f, v33
	v_exp_f32_e32 v29, v29
	v_rcp_f32_e32 v93, v5
	v_add_f32_e32 v5, 1.0, v24
	v_med3_f32 v30, v30, s77, v205
	v_med3_f32 v31, v31, s77, v205
	v_rcp_f32_e32 v94, v5
	v_add_f32_e32 v5, 1.0, v29
	v_pk_add_f32 v[30:31], v[30:31], 1.0 op_sel_hi:[1,0]
	v_rcp_f32_e32 v95, v5
	v_pk_mul_f32 v[90:91], v[90:91], v[92:93]
	v_pk_mul_f32 v[30:31], v[30:31], v[90:91]
	v_med3_f32 v26, v26, s77, v205
	v_cvt_pk_fp8_f32 v5, v30, v31
	v_med3_f32 v27, v27, s77, v205
	v_pk_add_f32 v[26:27], v[26:27], 1.0 op_sel_hi:[1,0]
	v_pk_mul_f32 v[30:31], v[32:33], v[94:95]
	v_mov_b32_e32 v32, v6
	v_pk_mul_f32 v[26:27], v[26:27], v[30:31]
	v_mov_b32_e32 v33, v8
	v_cvt_pk_fp8_f32 v5, v26, v27 op_sel:[0,0,1]
	v_mov_b32_e32 v26, v7
	v_mov_b32_e32 v27, v9
	v_pk_fma_f32 v[30:31], v[82:83], v[4:5], v[12:13] op_sel_hi:[1,0,1]
	v_pk_fma_f32 v[82:83], v[86:87], v[4:5], v[2:3] op_sel_hi:[1,0,1]
	v_pk_fma_f32 v[26:27], v[84:85], v[4:5], v[26:27] op_sel_hi:[1,0,1]
	v_min_f32_e32 v82, 0x40e00000, v82
	v_pk_fma_f32 v[32:33], v[88:89], v[4:5], v[32:33] op_sel_hi:[1,0,1]
	v_min_f32_e32 v83, 0x40e00000, v83
	v_mul_f32_e32 v4, 0xc01d265f, v82
	v_exp_f32_e32 v4, v4
	v_mul_f32_e32 v24, 0xc01d265f, v83
	v_exp_f32_e32 v24, v24
	v_min_f32_e32 v32, 0x40e00000, v32
	v_add_f32_e32 v4, 1.0, v4
	v_min_f32_e32 v33, 0x40e00000, v33
	v_rcp_f32_e32 v84, v4
	v_add_f32_e32 v4, 1.0, v24
	v_mul_f32_e32 v24, 0xc01d265f, v32
	v_exp_f32_e32 v24, v24
	v_mul_f32_e32 v29, 0xc01d265f, v33
	v_exp_f32_e32 v29, v29
	v_rcp_f32_e32 v85, v4
	v_add_f32_e32 v4, 1.0, v24
	v_med3_f32 v30, v30, s77, v205
	v_med3_f32 v31, v31, s77, v205
	v_rcp_f32_e32 v86, v4
	v_add_f32_e32 v4, 1.0, v29
	v_pk_add_f32 v[30:31], v[30:31], 1.0 op_sel_hi:[1,0]
	v_rcp_f32_e32 v87, v4
	v_pk_mul_f32 v[82:83], v[82:83], v[84:85]
	v_pk_mul_f32 v[30:31], v[30:31], v[82:83]
	v_med3_f32 v26, v26, s77, v205
	v_cvt_pk_fp8_f32 v4, v30, v31
	v_med3_f32 v27, v27, s77, v205
	v_pk_add_f32 v[26:27], v[26:27], 1.0 op_sel_hi:[1,0]
	v_pk_mul_f32 v[30:31], v[32:33], v[86:87]
	s_nop 0
	v_pk_mul_f32 v[26:27], v[26:27], v[30:31]
	s_nop 0
	v_cvt_pk_fp8_f32 v4, v26, v27 op_sel:[0,0,1]
	v_add_u32_e32 v26, s35, v200
	v_ashrrev_i32_e32 v27, 31, v26
	v_lshlrev_b64 v[26:27], 11, v[26:27]
	v_lshl_add_u64 v[26:27], s[14:15], 0, v[26:27]
	v_lshl_add_u64 v[26:27], v[26:27], 0, v[18:19]
	global_store_dwordx2 v[26:27], v[4:5], off
; __device__ __forceinline__ unsigned pk4_fp8(float a, float b, float c, float d) { int w = __builtin_amdgcn_cvt_pk_fp8_f32(a, b, 0, false); w = __builtin_amdgcn_cvt_pk_fp8_f32(c, d, w, true); return (unsigned)w; }
; __device__ __forceinline__ f32x4 swiglu4(f32x4 ug, f32x4 ul) {
;     f32x4 xg, xl, e, sg;
; #pragma unroll
;     for (int j = 0; j < 4; ++j) { xg[j] = __builtin_fminf(ug[j], 7.0f); xl[j] = __builtin_fminf(__builtin_fmaxf(ul[j], -7.0f), 7.0f); }
;     const f32x4 t = xg * (-1.702f * LOG2E);
; #pragma unroll
;     for (int j = 0; j < 4; ++j) e[j] = __builtin_amdgcn_exp2f(t[j]);
;     const f32x4 d = e + 1.0f;
; #pragma unroll
;     for (int j = 0; j < 4; ++j) sg[j] = __builtin_amdgcn_rcpf(d[j]);
;     return (xg * sg) * (xl + 1.0f);
; }
;     __device__ __forceinline__ void operator()(AccRef acc, const Unit& u, int wr, int wc, int fr, int fq, const LAS unsigned char* pre) const {
;     ...
;             for (int m = 0; m < 4; ++m) { const int r = ai * 128 + wr * 64 + m * 16 + fr, pos = u.pm * 256 + r; const bool valid = pos < cnt;
;                 const float rs = rsv[ai * 4 + m];
;                 const f32x4 h0 = swiglu4(acc[ai][0][m][0] * rs + bgv[0], acc[ai][1][m][0] * rs + blv[0]), h1 = swiglu4(acc[ai][0][m][1] * rs + bgv[1], acc[ai][1][m][1] * rs + blv[1]);
;                 u32x2 w; w.x = pk4_fp8(h0[0], h0[1], h0[2], h0[3]); w.y = pk4_fp8(h1[0], h1[1], h1[2], h1[3]);
;                 if (valid) *(u32x2*)(H + (size_t)(u.aux + r) * DE + o0) = w; }
.LBB0_1202:
	s_or_b64 exec, exec, s[46:47]
	v_add_u32_e32 v4, s43, v201
	v_cmp_lt_i32_e32 vcc, v4, v28
	s_and_saveexec_b64 s[46:47], vcc
	s_cbranch_execz .LBB0_1204
	v_mul_f32_e32 v4, 0x3c800000, v25
	v_pk_fma_f32 v[32:33], v[78:79], v[4:5], v[10:11] op_sel_hi:[1,0,1]
	v_mov_b32_e32 v24, v15
	v_mov_b32_e32 v25, v17
	v_mov_b32_e32 v30, v14
	v_mov_b32_e32 v31, v16
	v_min_f32_e32 v32, 0x40e00000, v32
	v_pk_fma_f32 v[24:25], v[76:77], v[4:5], v[24:25] op_sel_hi:[1,0,1]
	v_pk_fma_f32 v[26:27], v[74:75], v[4:5], v[20:21] op_sel_hi:[1,0,1]
	v_pk_fma_f32 v[30:31], v[80:81], v[4:5], v[30:31] op_sel_hi:[1,0,1]
	v_min_f32_e32 v33, 0x40e00000, v33
	v_mul_f32_e32 v5, 0xc01d265f, v32
	v_exp_f32_e32 v5, v5
	v_mul_f32_e32 v29, 0xc01d265f, v33
	v_exp_f32_e32 v29, v29
	v_min_f32_e32 v30, 0x40e00000, v30
	v_add_f32_e32 v5, 1.0, v5
	v_min_f32_e32 v31, 0x40e00000, v31
	v_rcp_f32_e32 v74, v5
	v_add_f32_e32 v5, 1.0, v29
	v_mul_f32_e32 v29, 0xc01d265f, v30
	v_exp_f32_e32 v29, v29
	v_mul_f32_e32 v75, 0xc01d265f, v31
	v_exp_f32_e32 v77, v75
	v_rcp_f32_e32 v75, v5
	v_add_f32_e32 v5, 1.0, v29
	v_med3_f32 v26, v26, s77, v205
	v_med3_f32 v27, v27, s77, v205
	v_rcp_f32_e32 v76, v5
	v_add_f32_e32 v5, 1.0, v77
	v_pk_add_f32 v[26:27], v[26:27], 1.0 op_sel_hi:[1,0]
	v_rcp_f32_e32 v77, v5
	v_pk_mul_f32 v[32:33], v[32:33], v[74:75]
	v_pk_mul_f32 v[26:27], v[26:27], v[32:33]
	v_med3_f32 v24, v24, s77, v205
	v_cvt_pk_fp8_f32 v5, v26, v27
	v_med3_f32 v25, v25, s77, v205
	v_pk_add_f32 v[24:25], v[24:25], 1.0 op_sel_hi:[1,0]
	v_pk_mul_f32 v[26:27], v[30:31], v[76:77]
	v_mov_b32_e32 v30, v6
	v_pk_mul_f32 v[24:25], v[24:25], v[26:27]
	v_mov_b32_e32 v31, v8
	v_cvt_pk_fp8_f32 v5, v24, v25 op_sel:[0,0,1]
	v_mov_b32_e32 v24, v7
	v_mov_b32_e32 v25, v9
	v_pk_fma_f32 v[32:33], v[66:67], v[4:5], v[2:3] op_sel_hi:[1,0,1]
	s_nop 0
	v_min_f32_e32 v32, 0x40e00000, v32
	v_pk_fma_f32 v[24:25], v[64:65], v[4:5], v[24:25] op_sel_hi:[1,0,1]
	v_pk_fma_f32 v[26:27], v[62:63], v[4:5], v[12:13] op_sel_hi:[1,0,1]
	v_pk_fma_f32 v[30:31], v[68:69], v[4:5], v[30:31] op_sel_hi:[1,0,1]
	v_min_f32_e32 v33, 0x40e00000, v33
	v_mul_f32_e32 v4, 0xc01d265f, v32
	v_exp_f32_e32 v4, v4
	v_mul_f32_e32 v29, 0xc01d265f, v33
	v_exp_f32_e32 v29, v29
	v_min_f32_e32 v30, 0x40e00000, v30
	v_add_f32_e32 v4, 1.0, v4
	v_min_f32_e32 v31, 0x40e00000, v31
	v_rcp_f32_e32 v62, v4
	v_add_f32_e32 v4, 1.0, v29
	v_mul_f32_e32 v29, 0xc01d265f, v30
	v_exp_f32_e32 v29, v29
	v_mul_f32_e32 v63, 0xc01d265f, v31
	v_exp_f32_e32 v65, v63
	v_rcp_f32_e32 v63, v4
	v_add_f32_e32 v4, 1.0, v29
	v_med3_f32 v26, v26, s77, v205
	v_med3_f32 v27, v27, s77, v205
	v_rcp_f32_e32 v64, v4
	v_add_f32_e32 v4, 1.0, v65
	v_pk_add_f32 v[26:27], v[26:27], 1.0 op_sel_hi:[1,0]
	v_rcp_f32_e32 v65, v4
	v_pk_mul_f32 v[32:33], v[32:33], v[62:63]
	v_pk_mul_f32 v[26:27], v[26:27], v[32:33]
	v_med3_f32 v24, v24, s77, v205
	v_cvt_pk_fp8_f32 v4, v26, v27
	v_med3_f32 v25, v25, s77, v205
	v_pk_add_f32 v[24:25], v[24:25], 1.0 op_sel_hi:[1,0]
	v_pk_mul_f32 v[26:27], v[30:31], v[64:65]
	s_nop 0
	v_pk_mul_f32 v[24:25], v[24:25], v[26:27]
	s_nop 0
	v_cvt_pk_fp8_f32 v4, v24, v25 op_sel:[0,0,1]
	v_add_u32_e32 v24, s35, v201
	v_ashrrev_i32_e32 v25, 31, v24
	v_lshlrev_b64 v[24:25], 11, v[24:25]
	v_lshl_add_u64 v[24:25], s[14:15], 0, v[24:25]
	v_lshl_add_u64 v[24:25], v[24:25], 0, v[18:19]
	global_store_dwordx2 v[24:25], v[4:5], off
; __device__ __forceinline__ unsigned pk4_fp8(float a, float b, float c, float d) { int w = __builtin_amdgcn_cvt_pk_fp8_f32(a, b, 0, false); w = __builtin_amdgcn_cvt_pk_fp8_f32(c, d, w, true); return (unsigned)w; }
; __device__ __forceinline__ f32x4 swiglu4(f32x4 ug, f32x4 ul) {
;     f32x4 xg, xl, e, sg;
; #pragma unroll
;     for (int j = 0; j < 4; ++j) { xg[j] = __builtin_fminf(ug[j], 7.0f); xl[j] = __builtin_fminf(__builtin_fmaxf(ul[j], -7.0f), 7.0f); }
;     const f32x4 t = xg * (-1.702f * LOG2E);
; #pragma unroll
;     for (int j = 0; j < 4; ++j) e[j] = __builtin_amdgcn_exp2f(t[j]);
;     const f32x4 d = e + 1.0f;
; #pragma unroll
;     for (int j = 0; j < 4; ++j) sg[j] = __builtin_amdgcn_rcpf(d[j]);
;     return (xg * sg) * (xl + 1.0f);
; }
;     __device__ __forceinline__ void operator()(AccRef acc, const Unit& u, int wr, int wc, int fr, int fq, const LAS unsigned char* pre) const {
;     ...
;             for (int m = 0; m < 4; ++m) { const int r = ai * 128 + wr * 64 + m * 16 + fr, pos = u.pm * 256 + r; const bool valid = pos < cnt;
;                 const float rs = rsv[ai * 4 + m];
;                 const f32x4 h0 = swiglu4(acc[ai][0][m][0] * rs + bgv[0], acc[ai][1][m][0] * rs + blv[0]), h1 = swiglu4(acc[ai][0][m][1] * rs + bgv[1], acc[ai][1][m][1] * rs + blv[1]);
;                 u32x2 w; w.x = pk4_fp8(h0[0], h0[1], h0[2], h0[3]); w.y = pk4_fp8(h1[0], h1[1], h1[2], h1[3]);
;                 if (valid) *(u32x2*)(H + (size_t)(u.aux + r) * DE + o0) = w; }
.LBB0_1204:
	s_or_b64 exec, exec, s[46:47]
	v_add_u32_e32 v4, s43, v202
	v_cmp_lt_i32_e32 vcc, v4, v28
	s_and_saveexec_b64 s[46:47], vcc
	s_cbranch_execz .LBB0_1206
	v_mul_f32_e32 v4, 0x3c800000, v22
	v_pk_fma_f32 v[32:33], v[54:55], v[4:5], v[10:11] op_sel_hi:[1,0,1]
	v_mov_b32_e32 v24, v15
	v_mov_b32_e32 v25, v17
	v_mov_b32_e32 v30, v14
	v_mov_b32_e32 v31, v16
	v_min_f32_e32 v32, 0x40e00000, v32
	v_pk_fma_f32 v[24:25], v[72:73], v[4:5], v[24:25] op_sel_hi:[1,0,1]
	v_pk_fma_f32 v[26:27], v[70:71], v[4:5], v[20:21] op_sel_hi:[1,0,1]
	v_pk_fma_f32 v[30:31], v[56:57], v[4:5], v[30:31] op_sel_hi:[1,0,1]
	v_min_f32_e32 v33, 0x40e00000, v33
	v_mul_f32_e32 v5, 0xc01d265f, v32
	v_exp_f32_e32 v5, v5
	v_mul_f32_e32 v22, 0xc01d265f, v33
	v_exp_f32_e32 v22, v22
	v_min_f32_e32 v30, 0x40e00000, v30
	v_add_f32_e32 v5, 1.0, v5
	v_min_f32_e32 v31, 0x40e00000, v31
	v_rcp_f32_e32 v54, v5
	v_add_f32_e32 v5, 1.0, v22
	v_mul_f32_e32 v22, 0xc01d265f, v30
	v_exp_f32_e32 v22, v22
	v_mul_f32_e32 v29, 0xc01d265f, v31
	v_exp_f32_e32 v29, v29
	v_rcp_f32_e32 v55, v5
	v_add_f32_e32 v5, 1.0, v22
	v_med3_f32 v26, v26, s77, v205
	v_med3_f32 v27, v27, s77, v205
	v_rcp_f32_e32 v56, v5
	v_add_f32_e32 v5, 1.0, v29
	v_pk_add_f32 v[26:27], v[26:27], 1.0 op_sel_hi:[1,0]
	v_rcp_f32_e32 v57, v5
	v_pk_mul_f32 v[32:33], v[32:33], v[54:55]
	v_pk_mul_f32 v[26:27], v[26:27], v[32:33]
	v_med3_f32 v24, v24, s77, v205
	v_cvt_pk_fp8_f32 v5, v26, v27
	v_med3_f32 v25, v25, s77, v205
	v_pk_add_f32 v[24:25], v[24:25], 1.0 op_sel_hi:[1,0]
	v_pk_mul_f32 v[26:27], v[30:31], v[56:57]
	v_mov_b32_e32 v30, v6
	v_pk_mul_f32 v[24:25], v[24:25], v[26:27]
	v_mov_b32_e32 v31, v8
	v_cvt_pk_fp8_f32 v5, v24, v25 op_sel:[0,0,1]
	v_mov_b32_e32 v24, v7
	v_mov_b32_e32 v25, v9
	v_pk_fma_f32 v[32:33], v[46:47], v[4:5], v[2:3] op_sel_hi:[1,0,1]
	s_nop 0
	v_min_f32_e32 v32, 0x40e00000, v32
	v_pk_fma_f32 v[24:25], v[60:61], v[4:5], v[24:25] op_sel_hi:[1,0,1]
	v_pk_fma_f32 v[26:27], v[58:59], v[4:5], v[12:13] op_sel_hi:[1,0,1]
	v_pk_fma_f32 v[30:31], v[48:49], v[4:5], v[30:31] op_sel_hi:[1,0,1]
	v_min_f32_e32 v33, 0x40e00000, v33
	v_mul_f32_e32 v4, 0xc01d265f, v32
	v_exp_f32_e32 v4, v4
	v_mul_f32_e32 v22, 0xc01d265f, v33
	v_exp_f32_e32 v22, v22
	v_min_f32_e32 v30, 0x40e00000, v30
	v_add_f32_e32 v4, 1.0, v4
	v_min_f32_e32 v31, 0x40e00000, v31
	v_rcp_f32_e32 v46, v4
	v_add_f32_e32 v4, 1.0, v22
	v_mul_f32_e32 v22, 0xc01d265f, v30
	v_exp_f32_e32 v22, v22
	v_mul_f32_e32 v29, 0xc01d265f, v31
	v_exp_f32_e32 v29, v29
	v_rcp_f32_e32 v47, v4
	v_add_f32_e32 v4, 1.0, v22
	v_med3_f32 v26, v26, s77, v205
	v_med3_f32 v27, v27, s77, v205
	v_rcp_f32_e32 v48, v4
	v_add_f32_e32 v4, 1.0, v29
	v_pk_add_f32 v[26:27], v[26:27], 1.0 op_sel_hi:[1,0]
	v_rcp_f32_e32 v49, v4
	v_pk_mul_f32 v[32:33], v[32:33], v[46:47]
	v_pk_mul_f32 v[26:27], v[26:27], v[32:33]
	v_med3_f32 v24, v24, s77, v205
	v_cvt_pk_fp8_f32 v4, v26, v27
	v_med3_f32 v25, v25, s77, v205
	v_pk_add_f32 v[24:25], v[24:25], 1.0 op_sel_hi:[1,0]
	v_pk_mul_f32 v[26:27], v[30:31], v[48:49]
	s_nop 0
	v_pk_mul_f32 v[24:25], v[24:25], v[26:27]
	s_nop 0
	v_cvt_pk_fp8_f32 v4, v24, v25 op_sel:[0,0,1]
	v_add_u32_e32 v24, s35, v202
	v_ashrrev_i32_e32 v25, 31, v24
	v_lshlrev_b64 v[24:25], 11, v[24:25]
	v_lshl_add_u64 v[24:25], s[14:15], 0, v[24:25]
	v_lshl_add_u64 v[24:25], v[24:25], 0, v[18:19]
	global_store_dwordx2 v[24:25], v[4:5], off
.LBB0_1206:
	s_or_b64 exec, exec, s[46:47]
	v_add_u32_e32 v4, s43, v203
	v_cmp_lt_i32_e32 vcc, v4, v28
	s_and_saveexec_b64 s[46:47], vcc
	s_cbranch_execz .LBB0_1208
	v_mul_f32_e32 v4, 0x3c800000, v23
	v_pk_fma_f32 v[10:11], v[38:39], v[4:5], v[10:11] op_sel_hi:[1,0,1]
	v_mov_b32_e32 v22, v15
	v_mov_b32_e32 v23, v17
	v_mov_b32_e32 v15, v16
	v_min_f32_e32 v10, 0x40e00000, v10
	v_pk_fma_f32 v[22:23], v[52:53], v[4:5], v[22:23] op_sel_hi:[1,0,1]
	v_pk_fma_f32 v[20:21], v[50:51], v[4:5], v[20:21] op_sel_hi:[1,0,1]
	v_pk_fma_f32 v[14:15], v[40:41], v[4:5], v[14:15] op_sel_hi:[1,0,1]
	v_min_f32_e32 v11, 0x40e00000, v11
	v_mul_f32_e32 v5, 0xc01d265f, v10
	v_exp_f32_e32 v5, v5
	v_mul_f32_e32 v16, 0xc01d265f, v11
	v_exp_f32_e32 v17, v16
	v_min_f32_e32 v14, 0x40e00000, v14
	v_add_f32_e32 v5, 1.0, v5
	v_min_f32_e32 v15, 0x40e00000, v15
	v_rcp_f32_e32 v16, v5
	v_add_f32_e32 v5, 1.0, v17
	v_mul_f32_e32 v17, 0xc01d265f, v14
	v_exp_f32_e32 v24, v17
	v_mul_f32_e32 v17, 0xc01d265f, v15
	v_exp_f32_e32 v25, v17
	v_rcp_f32_e32 v17, v5
	v_add_f32_e32 v5, 1.0, v24
	v_med3_f32 v20, v20, s77, v205
	v_med3_f32 v21, v21, s77, v205
	v_rcp_f32_e32 v24, v5
	v_add_f32_e32 v5, 1.0, v25
	v_pk_add_f32 v[20:21], v[20:21], 1.0 op_sel_hi:[1,0]
	v_rcp_f32_e32 v25, v5
	v_pk_mul_f32 v[10:11], v[10:11], v[16:17]
	v_pk_mul_f32 v[10:11], v[20:21], v[10:11]
	v_med3_f32 v22, v22, s77, v205
	v_cvt_pk_fp8_f32 v5, v10, v11
	v_med3_f32 v23, v23, s77, v205
	v_pk_add_f32 v[10:11], v[22:23], 1.0 op_sel_hi:[1,0]
	v_pk_mul_f32 v[14:15], v[14:15], v[24:25]
	s_nop 0
	v_pk_mul_f32 v[10:11], v[10:11], v[14:15]
	s_nop 0
	v_cvt_pk_fp8_f32 v5, v10, v11 op_sel:[0,0,1]
	v_mov_b32_e32 v10, v7
	v_mov_b32_e32 v11, v9
	v_mov_b32_e32 v7, v8
	v_pk_fma_f32 v[2:3], v[34:35], v[4:5], v[2:3] op_sel_hi:[1,0,1]
	v_pk_fma_f32 v[10:11], v[44:45], v[4:5], v[10:11] op_sel_hi:[1,0,1]
	v_min_f32_e32 v2, 0x40e00000, v2
	v_pk_fma_f32 v[12:13], v[42:43], v[4:5], v[12:13] op_sel_hi:[1,0,1]
	v_pk_fma_f32 v[6:7], v[36:37], v[4:5], v[6:7] op_sel_hi:[1,0,1]
	v_min_f32_e32 v3, 0x40e00000, v3
	v_mul_f32_e32 v4, 0xc01d265f, v2
	v_exp_f32_e32 v4, v4
	v_mul_f32_e32 v8, 0xc01d265f, v3
	v_exp_f32_e32 v9, v8
	v_min_f32_e32 v6, 0x40e00000, v6
	v_add_f32_e32 v4, 1.0, v4
	v_min_f32_e32 v7, 0x40e00000, v7
	v_rcp_f32_e32 v8, v4
	v_add_f32_e32 v4, 1.0, v9
	v_mul_f32_e32 v9, 0xc01d265f, v6
	v_exp_f32_e32 v14, v9
	v_mul_f32_e32 v9, 0xc01d265f, v7
	v_exp_f32_e32 v15, v9
	v_rcp_f32_e32 v9, v4
	v_add_f32_e32 v4, 1.0, v14
	v_med3_f32 v12, v12, s77, v205
	v_med3_f32 v13, v13, s77, v205
	v_rcp_f32_e32 v14, v4
	v_add_f32_e32 v4, 1.0, v15
	v_pk_add_f32 v[12:13], v[12:13], 1.0 op_sel_hi:[1,0]
	v_rcp_f32_e32 v15, v4
	v_pk_mul_f32 v[2:3], v[2:3], v[8:9]
	v_pk_mul_f32 v[2:3], v[12:13], v[2:3]
	v_med3_f32 v10, v10, s77, v205
	v_cvt_pk_fp8_f32 v4, v2, v3
	v_med3_f32 v11, v11, s77, v205
	v_pk_add_f32 v[2:3], v[10:11], 1.0 op_sel_hi:[1,0]
	v_pk_mul_f32 v[6:7], v[6:7], v[14:15]
	s_nop 0
	v_pk_mul_f32 v[2:3], v[2:3], v[6:7]
	s_nop 0
	v_cvt_pk_fp8_f32 v4, v2, v3 op_sel:[0,0,1]
	v_add_u32_e32 v2, s35, v203
	v_ashrrev_i32_e32 v3, 31, v2
	v_lshlrev_b64 v[2:3], 11, v[2:3]
	v_lshl_add_u64 v[2:3], s[14:15], 0, v[2:3]
	v_lshl_add_u64 v[2:3], v[2:3], 0, v[18:19]
	global_store_dwordx2 v[2:3], v[4:5], off

; #define LAS __attribute__((address_space(3)))
; __device__ __forceinline__ unsigned pk4_fp8(float a, float b, float c, float d) { int w = __builtin_amdgcn_cvt_pk_fp8_f32(a, b, 0, false); w = __builtin_amdgcn_cvt_pk_fp8_f32(c, d, w, true); return (unsigned)w; }
;     __device__ __forceinline__ CvtDesc desc(int qq) const { return cvt_desc(*F, item_of(qq), qq & 1, h); }
;     __device__ __forceinline__ void flush() { if (fitem >= 0) { cvt_flush(cvt_desc(*F, fitem, 0, h), img, h, F->lane); fitem = -1; } }
; __device__ __forceinline__ void cvt_to_lds(const CvtBuf& b, const CvtDesc& d, LAS unsigned char* img, const LAS float* gl, int sub2, int h, int lane) {
;     ...
;     for (int q = 0; q < 4; ++q) { const f32x4 gv = *(const LAS f32x4*)(gl + d.k0 + 16 * hh + 4 * q);
; #pragma unroll
;         for (int j = 0; j < 4; ++j) gs[4 * q + j] = use_g ? gv[j] : WSCALE; }
;     const int c8 = 4 * h + 2 * sub2 + hh;
; #pragma unroll
;     for (int j = 0; j < 4; ++j) { u32x4 o;
; #pragma unroll
;         for (int q = 0; q < 4; ++q) { const int i = 4 * q; o[q] = pk4_fp8(b.v[i][j] * gs[i], b.v[i + 1][j] * gs[i + 1], b.v[i + 2][j] * gs[i + 2], b.v[i + 3][j] * gs[i + 3]); }
;         *(LAS u32x4*)(img + (4 * l5 + j) * 128 + 16 * (c8 ^ (l5 & 7))) = o; }
;     __device__ __forceinline__ void drain() {
;     ...
;         while (q < nq) {
;             if (q + 1 < nq) cvt_load(b2, desc(q + 1), F->lane);
;             cvt_to_lds(buf, desc(q), img, gl, q & 1, h, F->lane); if (q & 1) fitem = item_of(q); ++q;
;             if (fitem >= 0) { __syncthreads(); flush(); __syncthreads(); }
;             if (q >= nq) break;
;             if (q + 1 < nq) cvt_load(buf, desc(q + 1), F->lane);
;             cvt_to_lds(b2, desc(q), img, gl, q & 1, h, F->lane); if (q & 1) fitem = item_of(q); ++q;
;             if (fitem >= 0) { __syncthreads(); flush(); __syncthreads(); }
;         }
.LBB0_1280:
	s_waitcnt vmcnt(31)
	v_mul_f32_e32 v130, 0x42800000, v2
	s_waitcnt vmcnt(30)
	v_mul_f32_e32 v137, 0x42800000, v6
	v_cvt_pk_fp8_f32 v136, v130, v137
	s_waitcnt vmcnt(27)
	v_mul_f32_e32 v130, 0x42800000, v18
	s_waitcnt vmcnt(26)
	v_mul_f32_e32 v140, 0x42800000, v22
	v_cvt_pk_fp8_f32 v137, v130, v140
	v_mul_f32_e32 v138, 0x42800000, v10
	v_mul_f32_e32 v139, 0x42800000, v14
	v_cvt_pk_fp8_f32 v136, v138, v139 op_sel:[0,0,1]
	s_waitcnt vmcnt(25)
	v_mul_f32_e32 v130, 0x42800000, v26
	s_waitcnt vmcnt(24)
	v_mul_f32_e32 v138, 0x42800000, v30
	v_cvt_pk_fp8_f32 v137, v130, v138 op_sel:[0,0,1]
	s_waitcnt vmcnt(23)
	v_mul_f32_e32 v130, 0x42800000, v34
	s_waitcnt vmcnt(22)
	v_mul_f32_e32 v139, 0x42800000, v38
	v_cvt_pk_fp8_f32 v138, v130, v139
	s_waitcnt vmcnt(19)
	v_mul_f32_e32 v130, 0x42800000, v50
	s_waitcnt vmcnt(18)
	v_mul_f32_e32 v142, 0x42800000, v54
	v_cvt_pk_fp8_f32 v139, v130, v142
	v_mul_f32_e32 v140, 0x42800000, v42
	v_mul_f32_e32 v141, 0x42800000, v46
	v_cvt_pk_fp8_f32 v138, v140, v141 op_sel:[0,0,1]
	s_waitcnt vmcnt(17)
	v_mul_f32_e32 v130, 0x42800000, v58
	s_waitcnt vmcnt(16)
	v_mul_f32_e32 v140, 0x42800000, v62
	v_cvt_pk_fp8_f32 v139, v130, v140 op_sel:[0,0,1]
	v_mul_f32_e32 v130, 0x42800000, v3
	v_mul_f32_e32 v141, 0x42800000, v7
	v_cvt_pk_fp8_f32 v140, v130, v141
	v_mul_f32_e32 v130, 0x42800000, v19
	v_mul_f32_e32 v154, 0x42800000, v23
	v_cvt_pk_fp8_f32 v141, v130, v154
	v_mul_f32_e32 v142, 0x42800000, v11
	v_mul_f32_e32 v143, 0x42800000, v15
	v_cvt_pk_fp8_f32 v140, v142, v143 op_sel:[0,0,1]
	v_mul_f32_e32 v130, 0x42800000, v27
	v_mul_f32_e32 v142, 0x42800000, v31
	v_cvt_pk_fp8_f32 v141, v130, v142 op_sel:[0,0,1]
	v_mul_f32_e32 v130, 0x42800000, v35
	v_mul_f32_e32 v143, 0x42800000, v39
	v_cvt_pk_fp8_f32 v142, v130, v143
	v_mul_f32_e32 v130, 0x42800000, v51
	v_mul_f32_e32 v156, 0x42800000, v55
	v_cvt_pk_fp8_f32 v143, v130, v156
	v_mul_f32_e32 v154, 0x42800000, v43
	v_mul_f32_e32 v155, 0x42800000, v47
	v_cvt_pk_fp8_f32 v142, v154, v155 op_sel:[0,0,1]
	v_mul_f32_e32 v130, 0x42800000, v59
	v_mul_f32_e32 v154, 0x42800000, v63
	v_cvt_pk_fp8_f32 v143, v130, v154 op_sel:[0,0,1]
	v_mul_f32_e32 v130, 0x42800000, v4
	v_mul_f32_e32 v155, 0x42800000, v8
	v_cvt_pk_fp8_f32 v154, v130, v155
	v_mul_f32_e32 v130, 0x42800000, v20
	v_mul_f32_e32 v158, 0x42800000, v24
	v_cvt_pk_fp8_f32 v155, v130, v158
	v_mul_f32_e32 v156, 0x42800000, v12
	v_mul_f32_e32 v157, 0x42800000, v16
	v_cvt_pk_fp8_f32 v154, v156, v157 op_sel:[0,0,1]
	v_mul_f32_e32 v130, 0x42800000, v28
	v_mul_f32_e32 v156, 0x42800000, v32
	v_cvt_pk_fp8_f32 v155, v130, v156 op_sel:[0,0,1]
	v_mul_f32_e32 v130, 0x42800000, v36
	v_mul_f32_e32 v157, 0x42800000, v40
	v_cvt_pk_fp8_f32 v156, v130, v157
	v_mul_f32_e32 v130, 0x42800000, v52
	v_mul_f32_e32 v160, 0x42800000, v56
	v_cvt_pk_fp8_f32 v157, v130, v160
	v_mul_f32_e32 v158, 0x42800000, v44
	v_mul_f32_e32 v159, 0x42800000, v48
	v_cvt_pk_fp8_f32 v156, v158, v159 op_sel:[0,0,1]
	v_mul_f32_e32 v130, 0x42800000, v60
	v_mul_f32_e32 v158, 0x42800000, v64
	v_cvt_pk_fp8_f32 v157, v130, v158 op_sel:[0,0,1]
	v_mul_f32_e32 v130, 0x42800000, v5
	v_mul_f32_e32 v159, 0x42800000, v9
	v_cvt_pk_fp8_f32 v158, v130, v159
	v_mul_f32_e32 v130, 0x42800000, v21
	v_mul_f32_e32 v162, 0x42800000, v25
	v_cvt_pk_fp8_f32 v159, v130, v162
	v_mul_f32_e32 v160, 0x42800000, v13
	v_mul_f32_e32 v161, 0x42800000, v17
	v_cvt_pk_fp8_f32 v158, v160, v161 op_sel:[0,0,1]
	v_mul_f32_e32 v130, 0x42800000, v29
	v_mul_f32_e32 v160, 0x42800000, v33
	v_cvt_pk_fp8_f32 v159, v130, v160 op_sel:[0,0,1]
	v_mul_f32_e32 v130, 0x42800000, v37
	v_mul_f32_e32 v161, 0x42800000, v41
	v_cvt_pk_fp8_f32 v160, v130, v161
	v_mul_f32_e32 v130, 0x42800000, v53
	v_mul_f32_e32 v164, 0x42800000, v57
	v_cvt_pk_fp8_f32 v161, v130, v164
	v_mul_f32_e32 v162, 0x42800000, v45
	v_mul_f32_e32 v163, 0x42800000, v49
	v_cvt_pk_fp8_f32 v160, v162, v163 op_sel:[0,0,1]
	v_mul_f32_e32 v130, 0x42800000, v61
	v_mul_f32_e32 v162, 0x42800000, v65
	v_cvt_pk_fp8_f32 v161, v130, v162 op_sel:[0,0,1]
	s_andn2_b64 vcc, exec, s[4:5]
	s_mov_b64 s[4:5], -1
	ds_write_b128 v152, v[136:139]
	ds_write_b128 v152, v[140:143] offset:128
	ds_write_b128 v152, v[154:157] offset:256
	ds_write_b128 v152, v[158:161] offset:384
	s_cbranch_vccnz .LBB0_1277
	s_add_i32 s59, s59, 2
	s_cmp_ge_u32 s59, s12
	s_cselect_b64 s[4:5], -1, 0
	s_and_b64 vcc, exec, s[4:5]
	s_cbranch_vccz .Ldr9_goB
	s_waitcnt vmcnt(0)
	s_branch .LBB0_1283

; #define LAS __attribute__((address_space(3)))
; __device__ __forceinline__ unsigned pk4_fp8(float a, float b, float c, float d) { int w = __builtin_amdgcn_cvt_pk_fp8_f32(a, b, 0, false); w = __builtin_amdgcn_cvt_pk_fp8_f32(c, d, w, true); return (unsigned)w; }
;     __device__ __forceinline__ CvtDesc desc(int qq) const { return cvt_desc(*F, item_of(qq), qq & 1, h); }
;     __device__ __forceinline__ void flush() { if (fitem >= 0) { cvt_flush(cvt_desc(*F, fitem, 0, h), img, h, F->lane); fitem = -1; } }
; __device__ __forceinline__ void cvt_to_lds(const CvtBuf& b, const CvtDesc& d, LAS unsigned char* img, const LAS float* gl, int sub2, int h, int lane) {
;     ...
;     for (int q = 0; q < 4; ++q) { const f32x4 gv = *(const LAS f32x4*)(gl + d.k0 + 16 * hh + 4 * q);
; #pragma unroll
;         for (int j = 0; j < 4; ++j) gs[4 * q + j] = use_g ? gv[j] : WSCALE; }
;     const int c8 = 4 * h + 2 * sub2 + hh;
; #pragma unroll
;     for (int j = 0; j < 4; ++j) { u32x4 o;
; #pragma unroll
;         for (int q = 0; q < 4; ++q) { const int i = 4 * q; o[q] = pk4_fp8(b.v[i][j] * gs[i], b.v[i + 1][j] * gs[i + 1], b.v[i + 2][j] * gs[i + 2], b.v[i + 3][j] * gs[i + 3]); }
;         *(LAS u32x4*)(img + (4 * l5 + j) * 128 + 16 * (c8 ^ (l5 & 7))) = o; }
;     __device__ __forceinline__ void drain() {
;     ...
;             cvt_to_lds(buf, desc(q), img, gl, q & 1, h, F->lane); if (q & 1) fitem = item_of(q); ++q;
;             if (fitem >= 0) { __syncthreads(); flush(); __syncthreads(); }
;             if (q >= nq) break;
;             if (q + 1 < nq) cvt_load(buf, desc(q + 1), F->lane);
;             cvt_to_lds(b2, desc(q), img, gl, q & 1, h, F->lane); if (q & 1) fitem = item_of(q); ++q;
;             if (fitem >= 0) { __syncthreads(); flush(); __syncthreads(); }
.LBB0_1283:
	s_lshr_b32 s0, s42, 8
	s_lshl_b64 s[8:9], s[0:1], 22
	s_and_b32 s0, s14, 0x780
	s_or_b32 s0, s8, s0
	s_and_b32 s8, s41, 0x780
	v_or_b32_e32 v130, s8, v144
	v_lshl_or_b32 v142, v130, 11, s0
	v_mov_b32_e32 v143, s9
	v_or_b32_e32 v130, s8, v147
	v_lshl_add_u64 v[136:137], v[134:135], 0, v[142:143]
	v_lshl_or_b32 v142, v130, 11, s0
	v_or_b32_e32 v130, s8, v149
	v_lshl_add_u64 v[138:139], v[134:135], 0, v[142:143]
	v_lshl_or_b32 v142, v130, 11, s0
	v_or_b32_e32 v130, s8, v133
	v_lshl_add_u64 v[140:141], v[134:135], 0, v[142:143]
	v_lshl_or_b32 v142, v130, 11, s0
	v_mul_f32_e32 v130, 0x42800000, v66
	v_mul_f32_e32 v155, 0x42800000, v70
	v_cvt_pk_fp8_f32 v154, v130, v155
	v_mul_f32_e32 v130, 0x42800000, v82
	v_mul_f32_e32 v158, 0x42800000, v86
	v_cvt_pk_fp8_f32 v155, v130, v158
	v_mul_f32_e32 v156, 0x42800000, v74
	v_mul_f32_e32 v157, 0x42800000, v78
	v_cvt_pk_fp8_f32 v154, v156, v157 op_sel:[0,0,1]
	v_mul_f32_e32 v130, 0x42800000, v90
	v_mul_f32_e32 v156, 0x42800000, v94
	v_cvt_pk_fp8_f32 v155, v130, v156 op_sel:[0,0,1]
	v_mul_f32_e32 v130, 0x42800000, v98
	v_mul_f32_e32 v157, 0x42800000, v102
	v_cvt_pk_fp8_f32 v156, v130, v157
	v_mul_f32_e32 v130, 0x42800000, v114
	v_mul_f32_e32 v160, 0x42800000, v118
	v_cvt_pk_fp8_f32 v157, v130, v160
	v_mul_f32_e32 v158, 0x42800000, v106
	v_mul_f32_e32 v159, 0x42800000, v110
	v_cvt_pk_fp8_f32 v156, v158, v159 op_sel:[0,0,1]
	v_mul_f32_e32 v130, 0x42800000, v122
	v_mul_f32_e32 v158, 0x42800000, v126
	v_cvt_pk_fp8_f32 v157, v130, v158 op_sel:[0,0,1]
	v_mul_f32_e32 v130, 0x42800000, v67
	v_mul_f32_e32 v159, 0x42800000, v71
	v_cvt_pk_fp8_f32 v158, v130, v159
	v_mul_f32_e32 v130, 0x42800000, v83
	v_mul_f32_e32 v162, 0x42800000, v87
	v_cvt_pk_fp8_f32 v159, v130, v162
	v_mul_f32_e32 v160, 0x42800000, v75
	v_mul_f32_e32 v161, 0x42800000, v79
	v_cvt_pk_fp8_f32 v158, v160, v161 op_sel:[0,0,1]
	v_mul_f32_e32 v130, 0x42800000, v91
	v_mul_f32_e32 v160, 0x42800000, v95
	v_cvt_pk_fp8_f32 v159, v130, v160 op_sel:[0,0,1]
	v_mul_f32_e32 v130, 0x42800000, v99
	v_mul_f32_e32 v161, 0x42800000, v103
	v_cvt_pk_fp8_f32 v160, v130, v161
	v_mul_f32_e32 v130, 0x42800000, v115
	v_mul_f32_e32 v164, 0x42800000, v119
	v_cvt_pk_fp8_f32 v161, v130, v164
	v_mul_f32_e32 v162, 0x42800000, v107
	v_mul_f32_e32 v163, 0x42800000, v111
	v_cvt_pk_fp8_f32 v160, v162, v163 op_sel:[0,0,1]
	v_mul_f32_e32 v130, 0x42800000, v123
	v_mul_f32_e32 v162, 0x42800000, v127
	v_cvt_pk_fp8_f32 v161, v130, v162 op_sel:[0,0,1]
	v_mul_f32_e32 v130, 0x42800000, v68
	v_mul_f32_e32 v163, 0x42800000, v72
	v_cvt_pk_fp8_f32 v162, v130, v163
	v_mul_f32_e32 v130, 0x42800000, v84
	v_mul_f32_e32 v166, 0x42800000, v88
	v_cvt_pk_fp8_f32 v163, v130, v166
	v_mul_f32_e32 v164, 0x42800000, v76
	v_mul_f32_e32 v165, 0x42800000, v80
	v_cvt_pk_fp8_f32 v162, v164, v165 op_sel:[0,0,1]
	v_mul_f32_e32 v130, 0x42800000, v92
	v_mul_f32_e32 v164, 0x42800000, v96
	v_cvt_pk_fp8_f32 v163, v130, v164 op_sel:[0,0,1]
	v_mul_f32_e32 v130, 0x42800000, v100
	v_mul_f32_e32 v165, 0x42800000, v104
	v_cvt_pk_fp8_f32 v164, v130, v165
	v_mul_f32_e32 v130, 0x42800000, v116
	v_mul_f32_e32 v168, 0x42800000, v120
	v_cvt_pk_fp8_f32 v165, v130, v168
	v_mul_f32_e32 v166, 0x42800000, v108
	v_mul_f32_e32 v167, 0x42800000, v112
	v_cvt_pk_fp8_f32 v164, v166, v167 op_sel:[0,0,1]
	v_mul_f32_e32 v130, 0x42800000, v124
	v_mul_f32_e32 v166, 0x42800000, v128
	v_cvt_pk_fp8_f32 v165, v130, v166 op_sel:[0,0,1]
	v_mul_f32_e32 v130, 0x42800000, v69
	v_mul_f32_e32 v167, 0x42800000, v73
	v_cvt_pk_fp8_f32 v166, v130, v167
	v_mul_f32_e32 v130, 0x42800000, v85
	v_mul_f32_e32 v170, 0x42800000, v89
	v_cvt_pk_fp8_f32 v167, v130, v170
	v_mul_f32_e32 v168, 0x42800000, v77
	v_mul_f32_e32 v169, 0x42800000, v81
	v_cvt_pk_fp8_f32 v166, v168, v169 op_sel:[0,0,1]
	v_mul_f32_e32 v130, 0x42800000, v93
	v_mul_f32_e32 v168, 0x42800000, v97
	v_cvt_pk_fp8_f32 v167, v130, v168 op_sel:[0,0,1]
	v_mul_f32_e32 v130, 0x42800000, v101
	v_mul_f32_e32 v169, 0x42800000, v105
	v_cvt_pk_fp8_f32 v168, v130, v169
	v_mul_f32_e32 v130, 0x42800000, v117
	v_mul_f32_e32 v172, 0x42800000, v121
	v_cvt_pk_fp8_f32 v169, v130, v172
	v_mul_f32_e32 v170, 0x42800000, v109
	v_mul_f32_e32 v171, 0x42800000, v113
	v_cvt_pk_fp8_f32 v168, v170, v171 op_sel:[0,0,1]
	v_mul_f32_e32 v130, 0x42800000, v125
	v_mul_f32_e32 v170, 0x42800000, v129
	v_cvt_pk_fp8_f32 v169, v130, v170 op_sel:[0,0,1]
	v_lshl_add_u64 v[142:143], v[134:135], 0, v[142:143]
	ds_write_b128 v153, v[154:157]
	ds_write_b128 v153, v[158:161] offset:128
	ds_write_b128 v153, v[162:165] offset:256
	ds_write_b128 v153, v[166:169] offset:384
	s_mov_b64 s[8:9], 0
	v_mov_b32_e32 v130, v151
	v_mov_b32_e32 v154, v150
	v_mov_b32_e32 v155, v148
	v_mov_b32_e32 v156, v146
	v_mov_b32_e32 v157, v145
	s_waitcnt lgkmcnt(0)
	s_barrier

; #define LAS __attribute__((address_space(3)))
; __device__ __forceinline__ unsigned pk4_fp8(float a, float b, float c, float d) { int w = __builtin_amdgcn_cvt_pk_fp8_f32(a, b, 0, false); w = __builtin_amdgcn_cvt_pk_fp8_f32(c, d, w, true); return (unsigned)w; }
;     __device__ __forceinline__ void operator()(AccRef acc, const Unit& u, int wr, int wc, int fr, int fq, const LAS unsigned char* pre) const {
;         const int col0 = u.pn * 256 + wc * 32 + 8 * fq; const int cnt = tab[98 + u.e];
;         f32x4 bv[2][2];
; #pragma unroll
;         for (int bj = 0; bj < 2; ++bj)
; #pragma unroll
;             for (int n = 0; n < 2; ++n) bv[bj][n] = *(const LAS f32x4*)(pre + (wc * 32 + 8 * fq + bj * 128 + 4 * n) * 4);
;         int tsv[8]; float gtv[8];
; #pragma unroll
;         for (int i = 0; i < 8; ++i) { const int rr = (i >> 2) * 128 + wr * 64 + (i & 3) * 16 + fr; tsv[i] = *(const LAS int*)(pre + 1024 + rr * 4); gtv[i] = *(const LAS float*)(pre + 2048 + rr * 4); }
; #pragma unroll
;         for (int ai = 0; ai < 2; ++ai)
; #pragma unroll
;             for (int m = 0; m < 4; ++m) { const int r = ai * 128 + wr * 64 + m * 16 + fr, pos = u.pm * 256 + r; const bool valid = pos < cnt;
;                 const int ts = tsv[ai * 4 + m]; const float gt = gtv[ai * 4 + m];
;                 unsigned char* rowp = Y + (size_t)ts * DM + col0;
; #pragma unroll
;                 for (int bj = 0; bj < 2; ++bj) { const f32x4 v0 = (acc[ai][bj][m][0] * WSCALE_INV + bv[bj][0]) * gt, v1 = (acc[ai][bj][m][1] * WSCALE_INV + bv[bj][1]) * gt;
;                     u32x2 w; w.x = pk4_fp8(v0[0], v0[1], v0[2], v0[3]); w.y = pk4_fp8(v1[0], v1[1], v1[2], v1[3]);
;                     if (valid) *(u32x2*)(rowp + bj * 128) = w; } }
.LBB0_1332:
	s_lshl_b32 s41, s47, 12
	s_and_b32 s41, s41, 0x1000
	s_add_i32 s41, s41, 0
	s_lshl_b32 s43, s48, 2
	s_add_i32 s41, s41, 0x20000
	s_add_i32 s43, s43, 0
	s_add_i32 s43, s43, 0x27988
	v_add_u32_e32 v171, s41, v177
	s_nop 15
	s_nop 15
	v_mov_b32_e32 v2, s43
	v_add_u32_e32 v3, s41, v198
	v_add_u32_e32 v18, 0x400, v171
	ds_read_b32 v166, v2
	ds_read_b128 v[14:17], v3
	ds_read_b128 v[10:13], v3 offset:16
	ds_read_b128 v[6:9], v3 offset:512
	ds_read_b128 v[2:5], v3 offset:528
	ds_read2_b32 v[32:33], v18 offset0:16 offset1:32
	v_add_u32_e32 v18, 0x480, v171
	ds_read2_b32 v[30:31], v18 offset0:16 offset1:240
	v_add_u32_e32 v18, 0x800, v171
	ds_read2_b32 v[28:29], v18 offset0:32 offset1:48
	v_add_u32_e32 v18, s41, v199
	v_add_u32_e32 v19, 0x400, v18
	v_add_u32_e32 v18, 0x800, v18
	ds_read2_b32 v[26:27], v19 offset1:16
	ds_read2_b32 v[24:25], v18 offset1:16
	ds_read2_b32 v[22:23], v19 offset0:32 offset1:48
	ds_read2_b32 v[20:21], v18 offset0:32 offset1:48
	s_lshl_b32 s41, s80, 8
	v_lshl_or_b32 v18, s46, 8, v197
	v_add_u32_e32 v170, s41, v173
	v_ashrrev_i32_e32 v19, 31, v18
	s_waitcnt lgkmcnt(0)
	v_cmp_lt_i32_e32 vcc, v170, v166
	s_and_saveexec_b64 s[46:47], vcc
	s_cbranch_execz .LBB0_1334
	ds_read2st64_b32 v[174:175], v171 offset0:4 offset1:8
	v_pk_fma_f32 v[154:155], v[154:155], s[20:21], v[10:11] op_sel_hi:[1,0,1]
	v_pk_fma_f32 v[158:159], v[158:159], s[20:21], v[14:15] op_sel_hi:[1,0,1]
	v_pk_fma_f32 v[150:151], v[150:151], s[20:21], v[6:7] op_sel_hi:[1,0,1]
	v_pk_fma_f32 v[146:147], v[146:147], s[20:21], v[2:3] op_sel_hi:[1,0,1]
	s_waitcnt lgkmcnt(0)
	v_ashrrev_i32_e32 v179, 31, v174
	v_mov_b32_e32 v178, v174
	v_mov_b32_e32 v172, v175
	v_lshlrev_b64 v[174:175], 11, v[178:179]
	v_pk_mul_f32 v[154:155], v[154:155], v[172:173] op_sel_hi:[1,0]
	v_mov_b32_e32 v179, v167
	v_cvt_pk_fp8_f32 v179, v154, v155
	v_pk_fma_f32 v[154:155], v[156:157], s[20:21], v[12:13] op_sel_hi:[1,0,1]
	v_pk_mul_f32 v[158:159], v[158:159], v[172:173] op_sel_hi:[1,0]
	v_pk_mul_f32 v[154:155], v[154:155], v[172:173] op_sel_hi:[1,0]
	v_cvt_pk_fp8_f32 v178, v158, v159
	v_cvt_pk_fp8_f32 v179, v154, v155 op_sel:[0,0,1]
	v_pk_mul_f32 v[150:151], v[150:151], v[172:173] op_sel_hi:[1,0]
	v_pk_mul_f32 v[146:147], v[146:147], v[172:173] op_sel_hi:[1,0]
	v_cvt_pk_fp8_f32 v154, v150, v151
	v_cvt_pk_fp8_f32 v155, v146, v147
	v_pk_fma_f32 v[160:161], v[160:161], s[20:21], v[16:17] op_sel_hi:[1,0,1]
	v_pk_fma_f32 v[152:153], v[152:153], s[20:21], v[8:9] op_sel_hi:[1,0,1]
	v_pk_mul_f32 v[160:161], v[160:161], v[172:173] op_sel_hi:[1,0]
	v_pk_fma_f32 v[146:147], v[148:149], s[20:21], v[4:5] op_sel_hi:[1,0,1]
	v_cvt_pk_fp8_f32 v178, v160, v161 op_sel:[0,0,1]
	v_pk_mul_f32 v[152:153], v[152:153], v[172:173] op_sel_hi:[1,0]
	v_pk_mul_f32 v[146:147], v[146:147], v[172:173] op_sel_hi:[1,0]
	v_cvt_pk_fp8_f32 v154, v152, v153 op_sel:[0,0,1]
	v_cvt_pk_fp8_f32 v155, v146, v147 op_sel:[0,0,1]
	v_lshl_add_u64 v[146:147], s[10:11], 0, v[174:175]
	v_lshl_add_u64 v[146:147], v[146:147], 0, v[18:19]
	global_store_dwordx2 v[146:147], v[178:179], off
	global_store_dwordx2 v[146:147], v[154:155], off offset:128
.LBB0_1334:
	s_or_b64 exec, exec, s[46:47]
	v_add_u32_e32 v146, s41, v200
	v_cmp_lt_i32_e32 vcc, v146, v166
	s_and_saveexec_b64 s[46:47], vcc
	s_cbranch_execz .LBB0_1336
	v_ashrrev_i32_e32 v147, 31, v32
	v_mov_b32_e32 v146, v32
	v_mov_b32_e32 v32, v31
	v_pk_fma_f32 v[138:139], v[138:139], s[20:21], v[10:11] op_sel_hi:[1,0,1]
	v_mov_b32_e32 v149, v167
	v_pk_mul_f32 v[138:139], v[138:139], v[32:33] op_sel_hi:[1,0]
	v_pk_fma_f32 v[142:143], v[142:143], s[20:21], v[14:15] op_sel_hi:[1,0,1]
	v_cvt_pk_fp8_f32 v149, v138, v139
	v_pk_fma_f32 v[138:139], v[140:141], s[20:21], v[12:13] op_sel_hi:[1,0,1]
	v_pk_mul_f32 v[142:143], v[142:143], v[32:33] op_sel_hi:[1,0]
	v_pk_mul_f32 v[138:139], v[138:139], v[32:33] op_sel_hi:[1,0]
	v_pk_fma_f32 v[134:135], v[134:135], s[20:21], v[6:7] op_sel_hi:[1,0,1]
	v_pk_fma_f32 v[130:131], v[130:131], s[20:21], v[2:3] op_sel_hi:[1,0,1]
	v_cvt_pk_fp8_f32 v148, v142, v143
	v_cvt_pk_fp8_f32 v149, v138, v139 op_sel:[0,0,1]
	v_pk_mul_f32 v[134:135], v[134:135], v[32:33] op_sel_hi:[1,0]
	v_pk_mul_f32 v[130:131], v[130:131], v[32:33] op_sel_hi:[1,0]
	v_cvt_pk_fp8_f32 v138, v134, v135
	v_cvt_pk_fp8_f32 v139, v130, v131
	v_pk_fma_f32 v[144:145], v[144:145], s[20:21], v[16:17] op_sel_hi:[1,0,1]
	v_pk_fma_f32 v[136:137], v[136:137], s[20:21], v[8:9] op_sel_hi:[1,0,1]
	v_pk_mul_f32 v[144:145], v[144:145], v[32:33] op_sel_hi:[1,0]
	v_pk_fma_f32 v[130:131], v[132:133], s[20:21], v[4:5] op_sel_hi:[1,0,1]
	v_cvt_pk_fp8_f32 v148, v144, v145 op_sel:[0,0,1]
	v_pk_mul_f32 v[136:137], v[136:137], v[32:33] op_sel_hi:[1,0]
	v_pk_mul_f32 v[130:131], v[130:131], v[32:33] op_sel_hi:[1,0]
	v_lshlrev_b64 v[146:147], 11, v[146:147]
	v_cvt_pk_fp8_f32 v138, v136, v137 op_sel:[0,0,1]
	v_cvt_pk_fp8_f32 v139, v130, v131 op_sel:[0,0,1]
	v_lshl_add_u64 v[130:131], s[10:11], 0, v[146:147]
	v_lshl_add_u64 v[130:131], v[130:131], 0, v[18:19]
	global_store_dwordx2 v[130:131], v[148:149], off
	global_store_dwordx2 v[130:131], v[138:139], off offset:128
; #define LAS __attribute__((address_space(3)))
; __device__ __forceinline__ unsigned pk4_fp8(float a, float b, float c, float d) { int w = __builtin_amdgcn_cvt_pk_fp8_f32(a, b, 0, false); w = __builtin_amdgcn_cvt_pk_fp8_f32(c, d, w, true); return (unsigned)w; }
;     __device__ __forceinline__ void operator()(AccRef acc, const Unit& u, int wr, int wc, int fr, int fq, const LAS unsigned char* pre) const {
;         const int col0 = u.pn * 256 + wc * 32 + 8 * fq; const int cnt = tab[98 + u.e];
;         f32x4 bv[2][2];
; #pragma unroll
;         for (int bj = 0; bj < 2; ++bj)
; #pragma unroll
;             for (int n = 0; n < 2; ++n) bv[bj][n] = *(const LAS f32x4*)(pre + (wc * 32 + 8 * fq + bj * 128 + 4 * n) * 4);
;         int tsv[8]; float gtv[8];
; #pragma unroll
;         for (int i = 0; i < 8; ++i) { const int rr = (i >> 2) * 128 + wr * 64 + (i & 3) * 16 + fr; tsv[i] = *(const LAS int*)(pre + 1024 + rr * 4); gtv[i] = *(const LAS float*)(pre + 2048 + rr * 4); }
; #pragma unroll
;         for (int ai = 0; ai < 2; ++ai)
; #pragma unroll
;             for (int m = 0; m < 4; ++m) { const int r = ai * 128 + wr * 64 + m * 16 + fr, pos = u.pm * 256 + r; const bool valid = pos < cnt;
;                 const int ts = tsv[ai * 4 + m]; const float gt = gtv[ai * 4 + m];
;                 unsigned char* rowp = Y + (size_t)ts * DM + col0;
; #pragma unroll
;                 for (int bj = 0; bj < 2; ++bj) { const f32x4 v0 = (acc[ai][bj][m][0] * WSCALE_INV + bv[bj][0]) * gt, v1 = (acc[ai][bj][m][1] * WSCALE_INV + bv[bj][1]) * gt;
;                     u32x2 w; w.x = pk4_fp8(v0[0], v0[1], v0[2], v0[3]); w.y = pk4_fp8(v1[0], v1[1], v1[2], v1[3]);
;                     if (valid) *(u32x2*)(rowp + bj * 128) = w; } }
.LBB0_1336:
	s_or_b64 exec, exec, s[46:47]
	v_add_u32_e32 v31, s41, v201
	v_cmp_lt_i32_e32 vcc, v31, v166
	s_and_saveexec_b64 s[46:47], vcc
	s_cbranch_execz .LBB0_1338
	v_ashrrev_i32_e32 v131, 31, v33
	v_mov_b32_e32 v130, v33
	v_pk_fma_f32 v[122:123], v[122:123], s[20:21], v[10:11] op_sel_hi:[1,0,1]
	v_lshlrev_b64 v[32:33], 11, v[130:131]
	v_pk_mul_f32 v[122:123], v[122:123], v[28:29] op_sel_hi:[1,0]
	v_mov_b32_e32 v131, v167
	v_cvt_pk_fp8_f32 v131, v122, v123
	v_pk_fma_f32 v[126:127], v[126:127], s[20:21], v[14:15] op_sel_hi:[1,0,1]
	v_pk_fma_f32 v[122:123], v[124:125], s[20:21], v[12:13] op_sel_hi:[1,0,1]
	v_pk_mul_f32 v[126:127], v[126:127], v[28:29] op_sel_hi:[1,0]
	v_pk_mul_f32 v[122:123], v[122:123], v[28:29] op_sel_hi:[1,0]
	v_pk_fma_f32 v[118:119], v[118:119], s[20:21], v[6:7] op_sel_hi:[1,0,1]
	v_pk_fma_f32 v[114:115], v[114:115], s[20:21], v[2:3] op_sel_hi:[1,0,1]
	v_cvt_pk_fp8_f32 v130, v126, v127
	v_cvt_pk_fp8_f32 v131, v122, v123 op_sel:[0,0,1]
	v_pk_mul_f32 v[118:119], v[118:119], v[28:29] op_sel_hi:[1,0]
	v_pk_mul_f32 v[114:115], v[114:115], v[28:29] op_sel_hi:[1,0]
	v_cvt_pk_fp8_f32 v122, v118, v119
	v_cvt_pk_fp8_f32 v123, v114, v115
	v_pk_fma_f32 v[128:129], v[128:129], s[20:21], v[16:17] op_sel_hi:[1,0,1]
	v_pk_fma_f32 v[120:121], v[120:121], s[20:21], v[8:9] op_sel_hi:[1,0,1]
	v_pk_mul_f32 v[128:129], v[128:129], v[28:29] op_sel_hi:[1,0]
	v_pk_fma_f32 v[114:115], v[116:117], s[20:21], v[4:5] op_sel_hi:[1,0,1]
	v_cvt_pk_fp8_f32 v130, v128, v129 op_sel:[0,0,1]
	v_pk_mul_f32 v[120:121], v[120:121], v[28:29] op_sel_hi:[1,0]
	v_pk_mul_f32 v[114:115], v[114:115], v[28:29] op_sel_hi:[1,0]
	v_cvt_pk_fp8_f32 v122, v120, v121 op_sel:[0,0,1]
	v_cvt_pk_fp8_f32 v123, v114, v115 op_sel:[0,0,1]
	v_lshl_add_u64 v[32:33], s[10:11], 0, v[32:33]
	v_lshl_add_u64 v[32:33], v[32:33], 0, v[18:19]
	global_store_dwordx2 v[32:33], v[130:131], off
	global_store_dwordx2 v[32:33], v[122:123], off offset:128
.LBB0_1338:
	s_or_b64 exec, exec, s[46:47]
	v_add_u32_e32 v28, s41, v202
	v_cmp_lt_i32_e32 vcc, v28, v166
	s_and_saveexec_b64 s[46:47], vcc
	s_cbranch_execz .LBB0_1340
	v_pk_fma_f32 v[110:111], v[110:111], s[20:21], v[14:15] op_sel_hi:[1,0,1]
	v_mov_b32_e32 v28, v29
	v_pk_fma_f32 v[32:33], v[112:113], s[20:21], v[16:17] op_sel_hi:[1,0,1]
	v_pk_mul_f32 v[110:111], v[110:111], v[28:29] op_sel_hi:[1,0]
	v_mov_b32_e32 v112, v167
	v_cvt_pk_fp8_f32 v112, v110, v111
	v_pk_fma_f32 v[106:107], v[106:107], s[20:21], v[10:11] op_sel_hi:[1,0,1]
	v_mov_b32_e32 v113, v167
	v_pk_mul_f32 v[106:107], v[106:107], v[28:29] op_sel_hi:[1,0]
	v_pk_mul_f32 v[32:33], v[32:33], v[28:29] op_sel_hi:[1,0]
	v_cvt_pk_fp8_f32 v113, v106, v107
	v_cvt_pk_fp8_f32 v112, v32, v33 op_sel:[0,0,1]
	v_pk_fma_f32 v[32:33], v[108:109], s[20:21], v[12:13] op_sel_hi:[1,0,1]
	v_pk_fma_f32 v[102:103], v[102:103], s[20:21], v[6:7] op_sel_hi:[1,0,1]
	v_pk_mul_f32 v[32:33], v[32:33], v[28:29] op_sel_hi:[1,0]
	v_pk_mul_f32 v[102:103], v[102:103], v[28:29] op_sel_hi:[1,0]
	v_cvt_pk_fp8_f32 v113, v32, v33 op_sel:[0,0,1]
	v_pk_fma_f32 v[32:33], v[104:105], s[20:21], v[8:9] op_sel_hi:[1,0,1]
	v_cvt_pk_fp8_f32 v104, v102, v103
	v_pk_fma_f32 v[98:99], v[98:99], s[20:21], v[2:3] op_sel_hi:[1,0,1]
	v_mov_b32_e32 v105, v167
	v_pk_mul_f32 v[98:99], v[98:99], v[28:29] op_sel_hi:[1,0]
	v_pk_mul_f32 v[32:33], v[32:33], v[28:29] op_sel_hi:[1,0]
	v_cvt_pk_fp8_f32 v105, v98, v99
	v_cvt_pk_fp8_f32 v104, v32, v33 op_sel:[0,0,1]
	v_pk_fma_f32 v[32:33], v[100:101], s[20:21], v[4:5] op_sel_hi:[1,0,1]
	v_ashrrev_i32_e32 v31, 31, v30
	v_pk_mul_f32 v[28:29], v[32:33], v[28:29] op_sel_hi:[1,0]
	v_lshlrev_b64 v[30:31], 11, v[30:31]
	v_cvt_pk_fp8_f32 v105, v28, v29 op_sel:[0,0,1]
	v_lshl_add_u64 v[28:29], s[10:11], 0, v[30:31]
	v_lshl_add_u64 v[28:29], v[28:29], 0, v[18:19]
	global_store_dwordx2 v[28:29], v[112:113], off
	global_store_dwordx2 v[28:29], v[104:105], off offset:128
.LBB0_1340:
	s_or_b64 exec, exec, s[46:47]
	v_add_u32_e32 v28, 0x80, v170
	v_cmp_lt_i32_e32 vcc, v28, v166
	s_and_saveexec_b64 s[46:47], vcc
	s_cbranch_execz .LBB0_1342
	v_pk_fma_f32 v[32:33], v[94:95], s[20:21], v[14:15] op_sel_hi:[1,0,1]
	v_mov_b32_e32 v94, v167
	v_pk_mul_f32 v[32:33], v[32:33], v[24:25] op_sel_hi:[1,0]
	v_mov_b32_e32 v95, v167
	v_cvt_pk_fp8_f32 v94, v32, v33
	v_pk_fma_f32 v[32:33], v[90:91], s[20:21], v[10:11] op_sel_hi:[1,0,1]
	v_pk_fma_f32 v[30:31], v[96:97], s[20:21], v[16:17] op_sel_hi:[1,0,1]
	v_pk_mul_f32 v[32:33], v[32:33], v[24:25] op_sel_hi:[1,0]
	v_pk_mul_f32 v[30:31], v[30:31], v[24:25] op_sel_hi:[1,0]
	v_cvt_pk_fp8_f32 v95, v32, v33
	v_pk_fma_f32 v[32:33], v[86:87], s[20:21], v[6:7] op_sel_hi:[1,0,1]
	v_mov_b32_e32 v86, v167
	v_pk_mul_f32 v[32:33], v[32:33], v[24:25] op_sel_hi:[1,0]
	v_cvt_pk_fp8_f32 v94, v30, v31 op_sel:[0,0,1]
	v_pk_fma_f32 v[30:31], v[92:93], s[20:21], v[12:13] op_sel_hi:[1,0,1]
	v_cvt_pk_fp8_f32 v86, v32, v33
	v_pk_fma_f32 v[32:33], v[82:83], s[20:21], v[2:3] op_sel_hi:[1,0,1]
	v_pk_mul_f32 v[30:31], v[30:31], v[24:25] op_sel_hi:[1,0]
	v_pk_mul_f32 v[32:33], v[32:33], v[24:25] op_sel_hi:[1,0]
	v_cvt_pk_fp8_f32 v95, v30, v31 op_sel:[0,0,1]
	v_pk_fma_f32 v[30:31], v[88:89], s[20:21], v[8:9] op_sel_hi:[1,0,1]
	v_cvt_pk_fp8_f32 v87, v32, v33
	v_pk_mul_f32 v[30:31], v[30:31], v[24:25] op_sel_hi:[1,0]
	v_ashrrev_i32_e32 v29, 31, v26
	v_cvt_pk_fp8_f32 v86, v30, v31 op_sel:[0,0,1]
	v_pk_fma_f32 v[30:31], v[84:85], s[20:21], v[4:5] op_sel_hi:[1,0,1]
	v_mov_b32_e32 v28, v26
	v_pk_mul_f32 v[30:31], v[30:31], v[24:25] op_sel_hi:[1,0]
	v_lshlrev_b64 v[28:29], 11, v[28:29]
	v_cvt_pk_fp8_f32 v87, v30, v31 op_sel:[0,0,1]
	v_lshl_add_u64 v[28:29], s[10:11], 0, v[28:29]
	v_lshl_add_u64 v[28:29], v[28:29], 0, v[18:19]
	global_store_dwordx2 v[28:29], v[94:95], off
	global_store_dwordx2 v[28:29], v[86:87], off offset:128
; #define LAS __attribute__((address_space(3)))
; __device__ __forceinline__ unsigned pk4_fp8(float a, float b, float c, float d) { int w = __builtin_amdgcn_cvt_pk_fp8_f32(a, b, 0, false); w = __builtin_amdgcn_cvt_pk_fp8_f32(c, d, w, true); return (unsigned)w; }
;     __device__ __forceinline__ void operator()(AccRef acc, const Unit& u, int wr, int wc, int fr, int fq, const LAS unsigned char* pre) const {
;         const int col0 = u.pn * 256 + wc * 32 + 8 * fq; const int cnt = tab[98 + u.e];
;         f32x4 bv[2][2];
; #pragma unroll
;         for (int bj = 0; bj < 2; ++bj)
; #pragma unroll
;             for (int n = 0; n < 2; ++n) bv[bj][n] = *(const LAS f32x4*)(pre + (wc * 32 + 8 * fq + bj * 128 + 4 * n) * 4);
;         int tsv[8]; float gtv[8];
; #pragma unroll
;         for (int i = 0; i < 8; ++i) { const int rr = (i >> 2) * 128 + wr * 64 + (i & 3) * 16 + fr; tsv[i] = *(const LAS int*)(pre + 1024 + rr * 4); gtv[i] = *(const LAS float*)(pre + 2048 + rr * 4); }
; #pragma unroll
;         for (int ai = 0; ai < 2; ++ai)
; #pragma unroll
;             for (int m = 0; m < 4; ++m) { const int r = ai * 128 + wr * 64 + m * 16 + fr, pos = u.pm * 256 + r; const bool valid = pos < cnt;
;                 const int ts = tsv[ai * 4 + m]; const float gt = gtv[ai * 4 + m];
;                 unsigned char* rowp = Y + (size_t)ts * DM + col0;
; #pragma unroll
;                 for (int bj = 0; bj < 2; ++bj) { const f32x4 v0 = (acc[ai][bj][m][0] * WSCALE_INV + bv[bj][0]) * gt, v1 = (acc[ai][bj][m][1] * WSCALE_INV + bv[bj][1]) * gt;
;                     u32x2 w; w.x = pk4_fp8(v0[0], v0[1], v0[2], v0[3]); w.y = pk4_fp8(v1[0], v1[1], v1[2], v1[3]);
;                     if (valid) *(u32x2*)(rowp + bj * 128) = w; } }
.LBB0_1342:
	s_or_b64 exec, exec, s[46:47]
	v_add_u32_e32 v24, 0x90, v170
	v_cmp_lt_i32_e32 vcc, v24, v166
	s_and_saveexec_b64 s[46:47], vcc
	s_cbranch_execz .LBB0_1344
	v_pk_fma_f32 v[30:31], v[78:79], s[20:21], v[14:15] op_sel_hi:[1,0,1]
	v_mov_b32_e32 v24, v25
	v_pk_mul_f32 v[30:31], v[30:31], v[24:25] op_sel_hi:[1,0]
	v_mov_b32_e32 v32, v167
	v_cvt_pk_fp8_f32 v32, v30, v31
	v_pk_fma_f32 v[30:31], v[74:75], s[20:21], v[10:11] op_sel_hi:[1,0,1]
	v_ashrrev_i32_e32 v29, 31, v27
	v_mov_b32_e32 v28, v27
	v_pk_mul_f32 v[30:31], v[30:31], v[24:25] op_sel_hi:[1,0]
	v_lshlrev_b64 v[26:27], 11, v[28:29]
	v_pk_fma_f32 v[28:29], v[80:81], s[20:21], v[16:17] op_sel_hi:[1,0,1]
	v_cvt_pk_fp8_f32 v33, v30, v31
	v_pk_fma_f32 v[30:31], v[62:63], s[20:21], v[6:7] op_sel_hi:[1,0,1]
	v_pk_mul_f32 v[28:29], v[28:29], v[24:25] op_sel_hi:[1,0]
	v_pk_mul_f32 v[30:31], v[30:31], v[24:25] op_sel_hi:[1,0]
	v_cvt_pk_fp8_f32 v32, v28, v29 op_sel:[0,0,1]
	v_pk_fma_f32 v[28:29], v[76:77], s[20:21], v[12:13] op_sel_hi:[1,0,1]
	v_cvt_pk_fp8_f32 v62, v30, v31
	v_pk_fma_f32 v[30:31], v[54:55], s[20:21], v[2:3] op_sel_hi:[1,0,1]
	v_pk_mul_f32 v[28:29], v[28:29], v[24:25] op_sel_hi:[1,0]
	v_pk_mul_f32 v[30:31], v[30:31], v[24:25] op_sel_hi:[1,0]
	v_cvt_pk_fp8_f32 v33, v28, v29 op_sel:[0,0,1]
	v_pk_fma_f32 v[28:29], v[64:65], s[20:21], v[8:9] op_sel_hi:[1,0,1]
	v_cvt_pk_fp8_f32 v63, v30, v31
	v_pk_mul_f32 v[28:29], v[28:29], v[24:25] op_sel_hi:[1,0]
	s_nop 0
	v_cvt_pk_fp8_f32 v62, v28, v29 op_sel:[0,0,1]
	v_pk_fma_f32 v[28:29], v[56:57], s[20:21], v[4:5] op_sel_hi:[1,0,1]
	s_nop 0
	v_pk_mul_f32 v[24:25], v[28:29], v[24:25] op_sel_hi:[1,0]
	s_nop 0
	v_cvt_pk_fp8_f32 v63, v24, v25 op_sel:[0,0,1]
	v_lshl_add_u64 v[24:25], s[10:11], 0, v[26:27]
	v_lshl_add_u64 v[24:25], v[24:25], 0, v[18:19]
	global_store_dwordx2 v[24:25], v[32:33], off
	global_store_dwordx2 v[24:25], v[62:63], off offset:128
.LBB0_1344:
	s_or_b64 exec, exec, s[46:47]
	v_add_u32_e32 v24, 0xa0, v170
	v_cmp_lt_i32_e32 vcc, v24, v166
	s_and_saveexec_b64 s[46:47], vcc
	s_cbranch_execz .LBB0_1346
	v_pk_fma_f32 v[28:29], v[58:59], s[20:21], v[14:15] op_sel_hi:[1,0,1]
	v_mov_b32_e32 v30, v167
	v_pk_mul_f32 v[28:29], v[28:29], v[20:21] op_sel_hi:[1,0]
	v_mov_b32_e32 v31, v167
	v_cvt_pk_fp8_f32 v30, v28, v29
	v_pk_fma_f32 v[28:29], v[46:47], s[20:21], v[10:11] op_sel_hi:[1,0,1]
	v_pk_fma_f32 v[26:27], v[60:61], s[20:21], v[16:17] op_sel_hi:[1,0,1]
	v_pk_mul_f32 v[28:29], v[28:29], v[20:21] op_sel_hi:[1,0]
	v_pk_mul_f32 v[26:27], v[26:27], v[20:21] op_sel_hi:[1,0]
	v_cvt_pk_fp8_f32 v31, v28, v29
	v_pk_fma_f32 v[28:29], v[70:71], s[20:21], v[6:7] op_sel_hi:[1,0,1]
	v_mov_b32_e32 v32, v167
	v_pk_mul_f32 v[28:29], v[28:29], v[20:21] op_sel_hi:[1,0]
	v_cvt_pk_fp8_f32 v30, v26, v27 op_sel:[0,0,1]
	v_pk_fma_f32 v[26:27], v[48:49], s[20:21], v[12:13] op_sel_hi:[1,0,1]
	v_cvt_pk_fp8_f32 v32, v28, v29
	v_pk_fma_f32 v[28:29], v[66:67], s[20:21], v[2:3] op_sel_hi:[1,0,1]
	v_pk_mul_f32 v[26:27], v[26:27], v[20:21] op_sel_hi:[1,0]
	v_pk_mul_f32 v[28:29], v[28:29], v[20:21] op_sel_hi:[1,0]
	v_cvt_pk_fp8_f32 v31, v26, v27 op_sel:[0,0,1]
	v_pk_fma_f32 v[26:27], v[72:73], s[20:21], v[8:9] op_sel_hi:[1,0,1]
	v_cvt_pk_fp8_f32 v33, v28, v29
	v_pk_mul_f32 v[26:27], v[26:27], v[20:21] op_sel_hi:[1,0]
	v_ashrrev_i32_e32 v25, 31, v22
	v_cvt_pk_fp8_f32 v32, v26, v27 op_sel:[0,0,1]
	v_pk_fma_f32 v[26:27], v[68:69], s[20:21], v[4:5] op_sel_hi:[1,0,1]
	v_mov_b32_e32 v24, v22
	v_pk_mul_f32 v[26:27], v[26:27], v[20:21] op_sel_hi:[1,0]
	v_lshlrev_b64 v[24:25], 11, v[24:25]
	v_cvt_pk_fp8_f32 v33, v26, v27 op_sel:[0,0,1]
	v_lshl_add_u64 v[24:25], s[10:11], 0, v[24:25]
	v_lshl_add_u64 v[24:25], v[24:25], 0, v[18:19]
	global_store_dwordx2 v[24:25], v[30:31], off
	global_store_dwordx2 v[24:25], v[32:33], off offset:128
.LBB0_1346:
	s_or_b64 exec, exec, s[46:47]
	v_add_u32_e32 v20, 0xb0, v170
	v_cmp_lt_i32_e32 vcc, v20, v166
	s_and_saveexec_b64 s[46:47], vcc
	s_cbranch_execz .LBB0_1348
	v_ashrrev_i32_e32 v25, 31, v23
	v_mov_b32_e32 v24, v23
	v_mov_b32_e32 v20, v21
	v_pk_fma_f32 v[10:11], v[34:35], s[20:21], v[10:11] op_sel_hi:[1,0,1]
	v_lshlrev_b64 v[22:23], 11, v[24:25]
	v_pk_mul_f32 v[10:11], v[10:11], v[20:21] op_sel_hi:[1,0]
	v_mov_b32_e32 v25, v167
	v_cvt_pk_fp8_f32 v25, v10, v11
	v_pk_fma_f32 v[14:15], v[38:39], s[20:21], v[14:15] op_sel_hi:[1,0,1]
	v_pk_fma_f32 v[10:11], v[36:37], s[20:21], v[12:13] op_sel_hi:[1,0,1]
	v_pk_mul_f32 v[14:15], v[14:15], v[20:21] op_sel_hi:[1,0]
	v_pk_mul_f32 v[10:11], v[10:11], v[20:21] op_sel_hi:[1,0]
	v_pk_fma_f32 v[6:7], v[50:51], s[20:21], v[6:7] op_sel_hi:[1,0,1]
	v_pk_fma_f32 v[2:3], v[42:43], s[20:21], v[2:3] op_sel_hi:[1,0,1]
	v_cvt_pk_fp8_f32 v24, v14, v15
	v_cvt_pk_fp8_f32 v25, v10, v11 op_sel:[0,0,1]
	v_pk_mul_f32 v[6:7], v[6:7], v[20:21] op_sel_hi:[1,0]
	v_pk_mul_f32 v[2:3], v[2:3], v[20:21] op_sel_hi:[1,0]
	v_cvt_pk_fp8_f32 v10, v6, v7
	v_cvt_pk_fp8_f32 v11, v2, v3
	v_pk_fma_f32 v[16:17], v[40:41], s[20:21], v[16:17] op_sel_hi:[1,0,1]
	v_pk_fma_f32 v[8:9], v[52:53], s[20:21], v[8:9] op_sel_hi:[1,0,1]
	v_pk_mul_f32 v[16:17], v[16:17], v[20:21] op_sel_hi:[1,0]
	v_pk_fma_f32 v[2:3], v[44:45], s[20:21], v[4:5] op_sel_hi:[1,0,1]
	v_cvt_pk_fp8_f32 v24, v16, v17 op_sel:[0,0,1]
	v_pk_mul_f32 v[8:9], v[8:9], v[20:21] op_sel_hi:[1,0]
	v_pk_mul_f32 v[2:3], v[2:3], v[20:21] op_sel_hi:[1,0]
	v_cvt_pk_fp8_f32 v10, v8, v9 op_sel:[0,0,1]
	v_cvt_pk_fp8_f32 v11, v2, v3 op_sel:[0,0,1]
	v_lshl_add_u64 v[2:3], s[10:11], 0, v[22:23]
	v_lshl_add_u64 v[2:3], v[2:3], 0, v[18:19]
	global_store_dwordx2 v[2:3], v[24:25], off
	global_store_dwordx2 v[2:3], v[10:11], off offset:128
